# C1 + GEMM epilogue bulk stores (P1, P6, P7, P9) made write-through (sc0 sc1) so dirty L2 drains during the phase, not at the grid-barrier release fence
# speedup vs baseline: 1.0035x; 1.0035x over previous
.LBB0_109:
	s_add_i32 s25, s25, 1
	s_mul_i32 s18, s25, s37
	s_mul_hi_u32 s19, s25, s28
	s_add_i32 s19, s19, s18
	s_mul_i32 s18, s25, s28
	v_mov_b64_e32 v[146:147], s[14:15]
	v_cmp_ge_i64_e32 vcc, s[18:19], v[146:147]
	v_mov_b32_e32 v146, 0
	v_mov_b32_e32 v147, 0
	v_cvt_pk_bf16_f32 v126, v126, v127
	v_cvt_pk_bf16_f32 v127, v128, v129
	v_cvt_pk_bf16_f32 v128, v122, v123
	v_cvt_pk_bf16_f32 v129, v124, v125
	s_nop 0
	v_add_u32_e32 v146, v146, v148
	v_add_u32_e32 v147, v147, v1
	v_lshl_add_u32 v156, v147, 3, s29
	v_ashrrev_i32_e32 v147, 31, v146
	v_lshlrev_b64 v[158:159], 11, v[146:147]
	v_ashrrev_i32_e32 v157, 31, v156
	v_lshl_add_u64 v[158:159], s[40:41], 0, v[158:159]
	v_lshlrev_b64 v[122:123], 1, v[156:157]
	v_lshl_add_u64 v[124:125], v[158:159], 0, v[122:123]
	global_store_dwordx4 v[124:125], v[126:129], off sc0 sc1
	v_cvt_pk_bf16_f32 v114, v114, v115
	v_cvt_pk_bf16_f32 v115, v116, v117
	v_cvt_pk_bf16_f32 v116, v106, v107
	v_add_u32_e32 v106, 16, v146
	v_ashrrev_i32_e32 v107, 31, v106
	v_lshlrev_b64 v[106:107], 11, v[106:107]
	v_cvt_pk_bf16_f32 v117, v108, v109
	global_store_dwordx4 v[124:125], v[114:117], off offset:256 sc0 sc1
	v_add_u32_e32 v154, 0x80, v146
	v_ashrrev_i32_e32 v155, 31, v154
	v_lshl_add_u64 v[114:115], s[40:41], 0, v[106:107]
	v_cvt_pk_bf16_f32 v106, v118, v119
	v_cvt_pk_bf16_f32 v107, v120, v121
	v_cvt_pk_bf16_f32 v108, v110, v111
	v_lshl_add_u64 v[110:111], v[114:115], 0, v[122:123]
	v_cvt_pk_bf16_f32 v109, v112, v113
	global_store_dwordx4 v[110:111], v[106:109], off sc0 sc1
	v_cvt_pk_bf16_f32 v98, v98, v99
	v_cvt_pk_bf16_f32 v99, v100, v101
	v_cvt_pk_bf16_f32 v100, v90, v91
	v_add_u32_e32 v90, 32, v146
	v_ashrrev_i32_e32 v91, 31, v90
	v_lshlrev_b64 v[90:91], 11, v[90:91]
	v_cvt_pk_bf16_f32 v101, v92, v93
	global_store_dwordx4 v[110:111], v[98:101], off offset:256 sc0 sc1
	s_mov_b64 s[18:19], -1
	s_and_b64 vcc, exec, vcc
	v_lshl_add_u64 v[98:99], s[40:41], 0, v[90:91]
	v_cvt_pk_bf16_f32 v90, v102, v103
	v_cvt_pk_bf16_f32 v91, v104, v105
	v_cvt_pk_bf16_f32 v92, v94, v95
	v_lshl_add_u64 v[94:95], v[98:99], 0, v[122:123]
	v_cvt_pk_bf16_f32 v93, v96, v97
	global_store_dwordx4 v[94:95], v[90:93], off sc0 sc1
	v_cvt_pk_bf16_f32 v82, v82, v83
	v_cvt_pk_bf16_f32 v83, v84, v85
	v_cvt_pk_bf16_f32 v84, v74, v75
	v_add_u32_e32 v74, 48, v146
	v_ashrrev_i32_e32 v75, 31, v74
	v_lshlrev_b64 v[74:75], 11, v[74:75]
	v_cvt_pk_bf16_f32 v85, v76, v77
	global_store_dwordx4 v[94:95], v[82:85], off offset:256 sc0 sc1
	s_nop 1
	v_lshl_add_u64 v[82:83], s[40:41], 0, v[74:75]
	v_cvt_pk_bf16_f32 v74, v86, v87
	v_cvt_pk_bf16_f32 v75, v88, v89
	v_cvt_pk_bf16_f32 v76, v78, v79
	v_lshl_add_u64 v[78:79], v[82:83], 0, v[122:123]
	v_cvt_pk_bf16_f32 v77, v80, v81
	global_store_dwordx4 v[78:79], v[74:77], off sc0 sc1
	v_cvt_pk_bf16_f32 v62, v62, v63
	v_cvt_pk_bf16_f32 v63, v64, v65
	v_cvt_pk_bf16_f32 v64, v58, v59
	v_lshlrev_b64 v[58:59], 11, v[154:155]
	v_lshl_add_u64 v[58:59], s[40:41], 0, v[58:59]
	v_lshl_add_u64 v[58:59], v[58:59], 0, v[122:123]
	v_cvt_pk_bf16_f32 v65, v60, v61
	global_store_dwordx4 v[78:79], v[62:65], off offset:256 sc0 sc1
	v_cvt_pk_bf16_f32 v46, v46, v47
	v_cvt_pk_bf16_f32 v47, v48, v49
	v_cvt_pk_bf16_f32 v48, v42, v43
	v_cvt_pk_bf16_f32 v49, v44, v45
	global_store_dwordx4 v[58:59], v[46:49], off sc0 sc1
	v_cvt_pk_bf16_f32 v42, v70, v71
	v_cvt_pk_bf16_f32 v43, v72, v73
	v_cvt_pk_bf16_f32 v44, v66, v67
	v_cvt_pk_bf16_f32 v45, v68, v69
	global_store_dwordx4 v[58:59], v[42:45], off offset:256 sc0 sc1
	v_cvt_pk_bf16_f32 v26, v26, v27
	v_cvt_pk_bf16_f32 v27, v28, v29
	v_cvt_pk_bf16_f32 v28, v18, v19
	v_cvt_pk_bf16_f32 v29, v20, v21
	s_nop 1
	v_add_u32_e32 v42, 0x90, v146
	v_ashrrev_i32_e32 v43, 31, v42
	v_lshlrev_b64 v[42:43], 11, v[42:43]
	v_lshl_add_u64 v[42:43], s[40:41], 0, v[42:43]
	v_lshl_add_u64 v[42:43], v[42:43], 0, v[122:123]
	global_store_dwordx4 v[42:43], v[26:29], off sc0 sc1
	v_cvt_pk_bf16_f32 v18, v54, v55
	v_cvt_pk_bf16_f32 v19, v56, v57
	v_cvt_pk_bf16_f32 v20, v50, v51
	v_cvt_pk_bf16_f32 v21, v52, v53
	global_store_dwordx4 v[42:43], v[18:21], off offset:256 sc0 sc1
	v_cvt_pk_bf16_f32 v14, v14, v15
	v_cvt_pk_bf16_f32 v15, v16, v17
	v_cvt_pk_bf16_f32 v16, v10, v11
	v_cvt_pk_bf16_f32 v17, v12, v13
	s_nop 1
	v_add_u32_e32 v18, 0xa0, v146
	v_ashrrev_i32_e32 v19, 31, v18
	v_lshlrev_b64 v[18:19], 11, v[18:19]
	v_lshl_add_u64 v[18:19], s[40:41], 0, v[18:19]
	v_lshl_add_u64 v[18:19], v[18:19], 0, v[122:123]
	global_store_dwordx4 v[18:19], v[14:17], off sc0 sc1
	v_cvt_pk_bf16_f32 v10, v38, v39
	v_cvt_pk_bf16_f32 v11, v40, v41
	v_cvt_pk_bf16_f32 v12, v34, v35
	v_cvt_pk_bf16_f32 v13, v36, v37
	global_store_dwordx4 v[18:19], v[10:13], off offset:256 sc0 sc1
	v_cvt_pk_bf16_f32 v6, v6, v7
	v_cvt_pk_bf16_f32 v7, v8, v9
	v_cvt_pk_bf16_f32 v8, v2, v3
	v_cvt_pk_bf16_f32 v9, v4, v5
	s_nop 1
	v_add_u32_e32 v10, 0xb0, v146
	v_ashrrev_i32_e32 v11, 31, v10
	v_lshlrev_b64 v[10:11], 11, v[10:11]
	v_lshl_add_u64 v[10:11], s[40:41], 0, v[10:11]
	v_lshl_add_u64 v[10:11], v[10:11], 0, v[122:123]
	global_store_dwordx4 v[10:11], v[6:9], off sc0 sc1
	v_cvt_pk_bf16_f32 v2, v30, v31
	v_cvt_pk_bf16_f32 v3, v32, v33
	v_cvt_pk_bf16_f32 v4, v22, v23
	v_cvt_pk_bf16_f32 v5, v24, v25
	global_store_dwordx4 v[10:11], v[2:5], off offset:256 sc0 sc1
	s_cbranch_vccnz .LBB0_104
	s_andn2_b64 vcc, exec, s[8:9]
	s_cbranch_vccnz .LBB0_103
	s_barrier
	s_branch .LBB0_103

.LBB0_125:
	s_ashr_i32 s46, s10, 2
	s_ashr_i32 s47, s46, 31
	v_cvt_f32_i32_e32 v204, v86
	v_cvt_f32_i32_e32 v86, v58
	v_cvt_f32_i32_e32 v58, v6
	v_mov_b32_e32 v6, 0
	s_lshl_b64 s[48:49], s[46:47], 26
	s_and_b32 s31, s10, 3
	s_lshl_b32 s35, s44, 8
	v_cvt_f32_i32_e32 v170, v104
	v_cvt_f32_i32_e32 v104, v52
	v_cvt_f32_i32_e32 v171, v105
	v_add3_u32 v52, s35, v159, v6
	s_add_u32 s35, s40, s48
	v_cvt_f32_i32_e32 v162, v70
	v_cvt_f32_i32_e32 v105, v53
	v_cvt_f32_i32_e32 v70, v42
	v_mov_b32_e32 v42, 0
	v_ashrrev_i32_e32 v53, 31, v52
	s_addc_u32 s45, s41, s49
	s_lshl_b32 s10, s10, 8
	v_cvt_f32_i32_e32 v205, v87
	v_cvt_f32_i32_e32 v210, v88
	v_cvt_f32_i32_e32 v88, v62
	v_cvt_f32_i32_e32 v87, v59
	v_cvt_f32_i32_e32 v62, v50
	v_cvt_f32_i32_e32 v59, v7
	v_lshl_add_u64 v[6:7], v[52:53], 2, s[14:15]
	v_add_lshl_u32 v50, v42, v1, 3
	s_or_b32 s47, s10, s60
	s_lshl_b64 s[48:49], s[10:11], 2
	s_add_u32 s48, s64, s48
	s_addc_u32 s49, s65, s49
	v_ashrrev_i32_e32 v253, 31, v50
	v_mov_b32_e32 v252, v50
	v_lshl_add_u64 v[252:253], v[252:253], 2, s[48:49]
	global_load_dwordx4 v[236:239], v[252:253], off
	global_load_dwordx4 v[240:243], v[252:253], off offset:16
	global_load_dwordx4 v[244:247], v[252:253], off offset:512
	global_load_dwordx4 v[248:251], v[252:253], off offset:528
	v_cvt_f32_i32_e32 v150, v64
	v_cvt_f32_i32_e32 v64, v54
	global_load_dword v54, v[6:7], off
	v_add_u32_e32 v6, s47, v50
	v_ashrrev_i32_e32 v7, 31, v6
	v_cvt_f32_i32_e32 v154, v112
	v_cvt_f32_i32_e32 v112, v90
	v_cvt_f32_i32_e32 v189, v77
	v_cvt_f32_i32_e32 v188, v76
	v_cvt_f32_i32_e32 v77, v47
	v_cvt_f32_i32_e32 v76, v46
	v_lshl_add_u64 v[46:47], v[6:7], 2, s[16:17]
	v_cvt_f32_i32_e32 v90, v2
	v_add_u32_e32 v2, 0x80, v6
	v_cvt_f32_i32_e32 v155, v113
	v_cvt_f32_i32_e32 v113, v91
	v_cvt_f32_i32_e32 v187, v79
	v_cvt_f32_i32_e32 v186, v78
	v_cvt_f32_i32_e32 v195, v81
	v_cvt_f32_i32_e32 v194, v80
	v_cvt_f32_i32_e32 v163, v71
	v_cvt_f32_i32_e32 v81, v49
	v_cvt_f32_i32_e32 v80, v48
	v_cvt_f32_i32_e32 v71, v43
	v_cvt_f32_i32_e32 v79, v45
	v_cvt_f32_i32_e32 v78, v44
	global_load_dwordx4 v[42:45], v[46:47], off offset:16
	s_nop 0
	global_load_dwordx4 v[46:49], v[46:47], off
	v_cvt_f32_i32_e32 v91, v3
	v_ashrrev_i32_e32 v3, 31, v2
	v_cvt_f32_i32_e32 v196, v40
	v_lshl_add_u64 v[6:7], v[2:3], 2, s[16:17]
	v_cvt_f32_i32_e32 v40, v30
	v_add_u32_e32 v30, 16, v52
	v_cvt_f32_i32_e32 v209, v117
	v_cvt_f32_i32_e32 v208, v116
	v_cvt_f32_i32_e32 v221, v97
	v_cvt_f32_i32_e32 v220, v96
	v_cvt_f32_i32_e32 v117, v93
	v_cvt_f32_i32_e32 v116, v92
	v_cvt_f32_i32_e32 v97, v9
	v_cvt_f32_i32_e32 v96, v8
	v_cvt_f32_i32_e32 v93, v5
	v_cvt_f32_i32_e32 v92, v4
	v_cvt_f32_i32_e32 v197, v41
	v_cvt_f32_i32_e32 v41, v31
	global_load_dwordx4 v[2:5], v[6:7], off offset:16
	s_nop 0
	global_load_dwordx4 v[6:9], v[6:7], off
	v_ashrrev_i32_e32 v31, 31, v30
	v_cvt_f32_i32_e32 v173, v11
	v_cvt_f32_i32_e32 v172, v10
	v_lshl_add_u64 v[10:11], v[30:31], 2, s[14:15]
	v_cvt_f32_i32_e32 v160, v66
	global_load_dword v66, v[10:11], off
	v_cvt_f32_i32_e32 v206, v118
	v_cvt_f32_i32_e32 v118, v18
	v_add_u32_e32 v18, 32, v52
	v_cvt_f32_i32_e32 v207, v119
	v_cvt_f32_i32_e32 v119, v19
	v_ashrrev_i32_e32 v19, 31, v18
	v_lshl_add_u64 v[10:11], v[18:19], 2, s[14:15]
	v_cvt_f32_i32_e32 v156, v110
	v_cvt_f32_i32_e32 v110, v98
	v_cvt_f32_i32_e32 v98, v22
	global_load_dword v22, v[10:11], off
	v_cvt_f32_i32_e32 v218, v94
	v_cvt_f32_i32_e32 v94, v26
	v_add_u32_e32 v26, 48, v52
	v_cvt_f32_i32_e32 v222, v124
	v_cvt_f32_i32_e32 v219, v95
	v_cvt_f32_i32_e32 v95, v27
	v_ashrrev_i32_e32 v27, 31, v26
	v_add_u32_e32 v216, 0x80, v52
	v_add_u32_e32 v200, 0x90, v52
	v_add_u32_e32 v180, 0xa0, v52
	v_add_u32_e32 v124, 0xb0, v52
	v_cvt_f32_i32_e32 v223, v125
	v_lshl_add_u64 v[10:11], v[26:27], 2, s[14:15]
	v_ashrrev_i32_e32 v217, 31, v216
	v_ashrrev_i32_e32 v201, 31, v200
	v_ashrrev_i32_e32 v181, 31, v180
	v_ashrrev_i32_e32 v125, 31, v124
	v_cvt_f32_i32_e32 v225, v127
	v_cvt_f32_i32_e32 v224, v126
	v_cvt_f32_i32_e32 v153, v123
	v_cvt_f32_i32_e32 v152, v122
	v_cvt_f32_i32_e32 v213, v121
	v_cvt_f32_i32_e32 v212, v120
	v_cvt_f32_i32_e32 v202, v114
	v_cvt_f32_i32_e32 v166, v100
	v_cvt_f32_i32_e32 v177, v13
	v_cvt_f32_i32_e32 v176, v12
	v_cvt_f32_i32_e32 v121, v15
	v_cvt_f32_i32_e32 v120, v14
	v_cvt_f32_i32_e32 v127, v17
	v_cvt_f32_i32_e32 v126, v16
	v_cvt_f32_i32_e32 v123, v21
	v_cvt_f32_i32_e32 v122, v20
	v_cvt_f32_i32_e32 v100, v28
	v_lshl_add_u64 v[12:13], v[216:217], 2, s[14:15]
	v_lshl_add_u64 v[14:15], v[200:201], 2, s[14:15]
	v_lshl_add_u64 v[16:17], v[180:181], 2, s[14:15]
	v_lshl_add_u64 v[20:21], v[124:125], 2, s[14:15]
	global_load_dword v28, v[10:11], off
	global_load_dword v214, v[12:13], off
	global_load_dword v190, v[14:15], off
	global_load_dword v158, v[16:17], off
	global_load_dword v114, v[20:21], off
	v_cvt_f32_i32_e32 v227, v129
	v_cvt_f32_i32_e32 v226, v128
	s_lshl_b32 s47, s31, 9
	s_add_u32 s48, s35, s47
	v_cvt_f32_i32_e32 v183, v75
	v_cvt_f32_i32_e32 v182, v74
	v_cvt_f32_i32_e32 v169, v73
	v_cvt_f32_i32_e32 v168, v72
	v_cvt_f32_i32_e32 v179, v37
	v_cvt_f32_i32_e32 v178, v36
	s_addc_u32 s49, s45, 0
	v_add_u32_e32 v14, s60, v50
	v_lshlrev_b64 v[10:11], 11, v[52:53]
	s_waitcnt vmcnt(0)
	v_pk_mul_f32 v[72:73], v[54:55], v[226:227] op_sel_hi:[0,1]
	v_pk_mul_f32 v[74:75], v[54:55], v[224:225] op_sel_hi:[0,1]
	v_pk_mul_f32 v[36:37], v[54:55], v[152:153] op_sel_hi:[0,1]
	v_cvt_f32_i32_e32 v193, v109
	v_cvt_f32_i32_e32 v192, v108
	v_cvt_f32_i32_e32 v109, v103
	v_cvt_f32_i32_e32 v108, v102
	v_cvt_f32_i32_e32 v175, v35
	v_cvt_f32_i32_e32 v174, v34
	v_cvt_f32_i32_e32 v103, v25
	v_cvt_f32_i32_e32 v102, v24
	v_lshl_add_u64 v[16:17], s[48:49], 0, v[10:11]
	v_pk_mul_f32 v[12:13], v[72:73], v[48:49]
	v_pk_mul_f32 v[10:11], v[74:75], v[46:47]
	v_pk_mul_f32 v[34:35], v[54:55], v[222:223] op_sel_hi:[0,1]
	v_pk_mul_f32 v[24:25], v[36:37], v[42:43]
	v_ashrrev_i32_e32 v15, 31, v14
	v_cvt_f32_i32_e32 v203, v115
	v_pk_mul_f32 v[20:21], v[34:35], v[44:45]
	v_cvt_pk_bf16_f32 v10, v10, v11
	v_cvt_pk_bf16_f32 v11, v12, v13
	v_cvt_pk_bf16_f32 v12, v24, v25
	v_lshlrev_b64 v[152:153], 1, v[14:15]
	v_pk_mul_f32 v[24:25], v[54:55], v[218:219] op_sel_hi:[0,1]
	v_cvt_f32_i32_e32 v211, v89
	v_cvt_f32_i32_e32 v199, v33
	v_cvt_f32_i32_e32 v198, v32
	v_cvt_pk_bf16_f32 v13, v20, v21
	v_lshl_add_u64 v[32:33], v[16:17], 0, v[152:153]
	v_pk_mul_f32 v[20:21], v[54:55], v[220:221] op_sel_hi:[0,1]
	v_pk_mul_f32 v[14:15], v[24:25], v[6:7]
	v_cvt_f32_i32_e32 v83, v83
	v_cvt_f32_i32_e32 v82, v82
	v_cvt_f32_i32_e32 v85, v85
	v_cvt_f32_i32_e32 v84, v84
	global_store_dwordx4 v[32:33], v[10:13], off sc0 sc1
	v_pk_mul_f32 v[16:17], v[20:21], v[8:9]
	v_cvt_pk_bf16_f32 v14, v14, v15
	v_cvt_f32_i32_e32 v157, v111
	v_pk_mul_f32 v[10:11], v[54:55], v[116:117] op_sel_hi:[0,1]
	v_pk_mul_f32 v[12:13], v[54:55], v[112:113] op_sel_hi:[0,1]
	v_cvt_pk_bf16_f32 v15, v16, v17
	v_cvt_f32_i32_e32 v185, v107
	v_cvt_f32_i32_e32 v184, v106
	v_cvt_f32_i32_e32 v151, v65
	v_cvt_f32_i32_e32 v65, v55
	v_cvt_f32_i32_e32 v107, v57
	v_cvt_f32_i32_e32 v106, v56
	v_pk_mul_f32 v[52:53], v[10:11], v[4:5]
	v_pk_mul_f32 v[54:55], v[12:13], v[2:3]
	v_pk_mul_f32 v[112:113], v[66:67], v[212:213] op_sel_hi:[0,1]
	v_cvt_pk_bf16_f32 v16, v54, v55
	v_cvt_pk_bf16_f32 v17, v52, v53
	global_store_dwordx4 v[32:33], v[14:17], off offset:256 sc0 sc1
	v_pk_mul_f32 v[116:117], v[66:67], v[206:207] op_sel_hi:[0,1]
	v_pk_mul_f32 v[56:57], v[66:67], v[208:209] op_sel_hi:[0,1]
	v_lshlrev_b64 v[14:15], 11, v[30:31]
	v_cvt_f32_i32_e32 v129, v61
	v_cvt_f32_i32_e32 v128, v60
	v_lshl_add_u64 v[30:31], s[48:49], 0, v[14:15]
	v_pk_mul_f32 v[16:17], v[112:113], v[48:49]
	v_pk_mul_f32 v[14:15], v[116:117], v[46:47]
	v_pk_mul_f32 v[60:61], v[66:67], v[202:203] op_sel_hi:[0,1]
	v_pk_mul_f32 v[32:33], v[56:57], v[44:45]
	v_cvt_f32_i32_e32 v165, v69
	v_cvt_f32_i32_e32 v164, v68
	v_pk_mul_f32 v[52:53], v[60:61], v[42:43]
	v_cvt_pk_bf16_f32 v14, v14, v15
	v_cvt_pk_bf16_f32 v15, v16, v17
	v_lshl_add_u64 v[68:69], v[30:31], 0, v[152:153]
	v_cvt_pk_bf16_f32 v16, v52, v53
	v_cvt_pk_bf16_f32 v17, v32, v33
	v_pk_mul_f32 v[30:31], v[66:67], v[210:211] op_sel_hi:[0,1]
	v_pk_mul_f32 v[32:33], v[66:67], v[204:205] op_sel_hi:[0,1]
	global_store_dwordx4 v[68:69], v[14:17], off sc0 sc1
	v_pk_mul_f32 v[54:55], v[30:31], v[8:9]
	v_pk_mul_f32 v[52:53], v[32:33], v[6:7]
	v_pk_mul_f32 v[14:15], v[66:67], v[84:85] op_sel_hi:[0,1]
	v_pk_mul_f32 v[16:17], v[66:67], v[82:83] op_sel_hi:[0,1]
	v_cvt_f32_i32_e32 v161, v67
	v_pk_mul_f32 v[66:67], v[14:15], v[4:5]
	v_pk_mul_f32 v[82:83], v[16:17], v[2:3]
	v_cvt_pk_bf16_f32 v52, v52, v53
	v_cvt_pk_bf16_f32 v53, v54, v55
	v_lshlrev_b64 v[18:19], 11, v[18:19]
	v_cvt_pk_bf16_f32 v54, v82, v83
	v_cvt_pk_bf16_f32 v55, v66, v67
	v_pk_mul_f32 v[154:155], v[22:23], v[154:155] op_sel_hi:[0,1]
	v_pk_mul_f32 v[156:157], v[22:23], v[156:157] op_sel_hi:[0,1]
	v_cvt_f32_i32_e32 v167, v101
	global_store_dwordx4 v[68:69], v[52:55], off offset:256 sc0 sc1
	v_lshl_add_u64 v[18:19], s[48:49], 0, v[18:19]
	v_pk_mul_f32 v[82:83], v[22:23], v[192:193] op_sel_hi:[0,1]
	v_pk_mul_f32 v[54:55], v[154:155], v[48:49]
	v_pk_mul_f32 v[52:53], v[156:157], v[46:47]
	v_pk_mul_f32 v[84:85], v[22:23], v[184:185] op_sel_hi:[0,1]
	v_cvt_f32_i32_e32 v111, v99
	v_pk_mul_f32 v[66:67], v[82:83], v[44:45]
	v_pk_mul_f32 v[68:69], v[84:85], v[42:43]
	v_cvt_pk_bf16_f32 v52, v52, v53
	v_cvt_pk_bf16_f32 v53, v54, v55
	v_lshl_add_u64 v[184:185], v[18:19], 0, v[152:153]
	v_cvt_pk_bf16_f32 v54, v68, v69
	v_cvt_pk_bf16_f32 v55, v66, v67
	global_store_dwordx4 v[184:185], v[52:55], off sc0 sc1
	v_pk_mul_f32 v[18:19], v[22:23], v[188:189] op_sel_hi:[0,1]
	v_cvt_f32_i32_e32 v99, v23
	v_pk_mul_f32 v[52:53], v[22:23], v[194:195] op_sel_hi:[0,1]
	v_pk_mul_f32 v[54:55], v[22:23], v[186:187] op_sel_hi:[0,1]
	v_pk_mul_f32 v[68:69], v[52:53], v[8:9]
	v_pk_mul_f32 v[66:67], v[54:55], v[6:7]
	v_pk_mul_f32 v[22:23], v[22:23], v[182:183] op_sel_hi:[0,1]
	v_pk_mul_f32 v[182:183], v[18:19], v[4:5]
	v_pk_mul_f32 v[186:187], v[22:23], v[2:3]
	v_cvt_pk_bf16_f32 v66, v66, v67
	v_cvt_pk_bf16_f32 v67, v68, v69
	v_lshlrev_b64 v[26:27], 11, v[26:27]
	v_cvt_pk_bf16_f32 v68, v186, v187
	v_cvt_pk_bf16_f32 v69, v182, v183
	v_pk_mul_f32 v[170:171], v[28:29], v[170:171] op_sel_hi:[0,1]
	v_pk_mul_f32 v[182:183], v[28:29], v[108:109] op_sel_hi:[0,1]
	v_pk_mul_f32 v[108:109], v[28:29], v[166:167] op_sel_hi:[0,1]
	global_store_dwordx4 v[184:185], v[66:69], off offset:256 sc0 sc1
	v_lshl_add_u64 v[26:27], s[48:49], 0, v[26:27]
	v_pk_mul_f32 v[110:111], v[28:29], v[110:111] op_sel_hi:[0,1]
	v_pk_mul_f32 v[68:69], v[170:171], v[48:49]
	v_pk_mul_f32 v[66:67], v[182:183], v[46:47]
	v_pk_mul_f32 v[166:167], v[108:109], v[44:45]
	v_cvt_f32_i32_e32 v89, v63
	v_pk_mul_f32 v[184:185], v[110:111], v[42:43]
	v_cvt_pk_bf16_f32 v66, v66, v67
	v_cvt_pk_bf16_f32 v67, v68, v69
	v_cvt_f32_i32_e32 v39, v39
	v_cvt_pk_bf16_f32 v68, v184, v185
	v_cvt_pk_bf16_f32 v69, v166, v167
	v_lshl_add_u64 v[166:167], v[26:27], 0, v[152:153]
	global_store_dwordx4 v[166:167], v[66:69], off sc0 sc1
	v_cvt_f32_i32_e32 v38, v38
	v_cvt_f32_i32_e32 v101, v29
	v_pk_mul_f32 v[66:67], v[28:29], v[168:169] op_sel_hi:[0,1]
	v_pk_mul_f32 v[68:69], v[28:29], v[162:163] op_sel_hi:[0,1]
	v_pk_mul_f32 v[162:163], v[66:67], v[8:9]
	v_pk_mul_f32 v[168:169], v[68:69], v[6:7]
	v_pk_mul_f32 v[26:27], v[28:29], v[164:165] op_sel_hi:[0,1]
	v_pk_mul_f32 v[28:29], v[28:29], v[160:161] op_sel_hi:[0,1]
	v_cvt_pk_bf16_f32 v160, v168, v169
	v_cvt_pk_bf16_f32 v161, v162, v163
	v_pk_mul_f32 v[164:165], v[26:27], v[4:5]
	v_pk_mul_f32 v[184:185], v[28:29], v[2:3]
	v_pk_mul_f32 v[168:169], v[214:215], v[150:151] op_sel_hi:[0,1]
	v_cvt_pk_bf16_f32 v162, v184, v185
	v_cvt_pk_bf16_f32 v163, v164, v165
	global_store_dwordx4 v[166:167], v[160:163], off offset:256 sc0 sc1
	v_pk_mul_f32 v[128:129], v[214:215], v[128:129] op_sel_hi:[0,1]
	v_pk_mul_f32 v[184:185], v[214:215], v[88:89] op_sel_hi:[0,1]
	v_lshlrev_b64 v[160:161], 11, v[216:217]
	v_lshl_add_u64 v[160:161], s[48:49], 0, v[160:161]
	v_pk_mul_f32 v[88:89], v[48:49], v[168:169]
	v_pk_mul_f32 v[150:151], v[214:215], v[86:87] op_sel_hi:[0,1]
	v_pk_mul_f32 v[164:165], v[128:129], v[44:45]
	v_pk_mul_f32 v[162:163], v[46:47], v[184:185]
	v_pk_mul_f32 v[166:167], v[150:151], v[42:43]
	v_cvt_pk_bf16_f32 v86, v162, v163
	v_cvt_pk_bf16_f32 v87, v88, v89
	v_cvt_f32_i32_e32 v63, v51
	v_cvt_pk_bf16_f32 v88, v166, v167
	v_cvt_pk_bf16_f32 v89, v164, v165
	v_lshl_add_u64 v[164:165], v[160:161], 0, v[152:153]
	global_store_dwordx4 v[164:165], v[86:89], off sc0 sc1
	v_pk_mul_f32 v[40:41], v[214:215], v[40:41] op_sel_hi:[0,1]
	v_pk_mul_f32 v[186:187], v[40:41], v[2:3]
	v_pk_mul_f32 v[88:89], v[214:215], v[38:39] op_sel_hi:[0,1]
	v_pk_mul_f32 v[86:87], v[214:215], v[196:197] op_sel_hi:[0,1]
	v_pk_mul_f32 v[160:161], v[88:89], v[6:7]
	v_pk_mul_f32 v[162:163], v[86:87], v[8:9]
	v_pk_mul_f32 v[38:39], v[214:215], v[198:199] op_sel_hi:[0,1]
	v_cvt_pk_bf16_f32 v160, v160, v161
	v_cvt_pk_bf16_f32 v161, v162, v163
	v_pk_mul_f32 v[166:167], v[38:39], v[4:5]
	v_cvt_pk_bf16_f32 v162, v186, v187
	v_pk_mul_f32 v[186:187], v[190:191], v[106:107] op_sel_hi:[0,1]
	v_cvt_pk_bf16_f32 v163, v166, v167
	global_store_dwordx4 v[164:165], v[160:163], off offset:256 sc0 sc1
	v_pk_mul_f32 v[188:189], v[190:191], v[64:65] op_sel_hi:[0,1]
	v_pk_mul_f32 v[64:65], v[48:49], v[186:187]
	v_lshlrev_b64 v[160:161], 11, v[200:201]
	v_lshl_add_u64 v[164:165], s[48:49], 0, v[160:161]
	v_pk_mul_f32 v[160:161], v[190:191], v[104:105] op_sel_hi:[0,1]
	v_pk_mul_f32 v[106:107], v[46:47], v[188:189]
	v_pk_mul_f32 v[162:163], v[190:191], v[62:63] op_sel_hi:[0,1]
	v_pk_mul_f32 v[104:105], v[44:45], v[160:161]
	v_pk_mul_f32 v[166:167], v[42:43], v[162:163]
	v_cvt_pk_bf16_f32 v62, v106, v107
	v_cvt_pk_bf16_f32 v63, v64, v65
	v_lshl_add_u64 v[192:193], v[164:165], 0, v[152:153]
	v_cvt_pk_bf16_f32 v64, v166, v167
	v_cvt_pk_bf16_f32 v65, v104, v105
	v_pk_mul_f32 v[104:105], v[190:191], v[178:179] op_sel_hi:[0,1]
	v_pk_mul_f32 v[106:107], v[190:191], v[174:175] op_sel_hi:[0,1]
	global_store_dwordx4 v[192:193], v[62:65], off sc0 sc1
	v_pk_mul_f32 v[166:167], v[104:105], v[8:9]
	v_pk_mul_f32 v[164:165], v[106:107], v[6:7]
	v_pk_mul_f32 v[62:63], v[190:191], v[176:177] op_sel_hi:[0,1]
	v_pk_mul_f32 v[64:65], v[190:191], v[172:173] op_sel_hi:[0,1]
	v_pk_mul_f32 v[172:173], v[62:63], v[4:5]
	v_pk_mul_f32 v[174:175], v[64:65], v[2:3]
	v_cvt_pk_bf16_f32 v164, v164, v165
	v_cvt_pk_bf16_f32 v165, v166, v167
	v_pk_mul_f32 v[96:97], v[114:115], v[96:97] op_sel_hi:[0,1]
	v_cvt_pk_bf16_f32 v166, v174, v175
	v_cvt_pk_bf16_f32 v167, v172, v173
	global_store_dwordx4 v[192:193], v[164:167], off offset:256 sc0 sc1
	v_pk_mul_f32 v[174:175], v[158:159], v[76:77] op_sel_hi:[0,1]
	v_pk_mul_f32 v[172:173], v[158:159], v[80:81] op_sel_hi:[0,1]
	v_lshlrev_b64 v[164:165], 11, v[180:181]
	v_pk_mul_f32 v[166:167], v[158:159], v[70:71] op_sel_hi:[0,1]
	v_lshl_add_u64 v[176:177], s[48:49], 0, v[164:165]
	v_pk_mul_f32 v[76:77], v[46:47], v[174:175]
	v_pk_mul_f32 v[164:165], v[158:159], v[78:79] op_sel_hi:[0,1]
	v_pk_mul_f32 v[78:79], v[42:43], v[166:167]
	v_pk_mul_f32 v[80:81], v[48:49], v[172:173]
	v_pk_mul_f32 v[70:71], v[44:45], v[164:165]
	v_cvt_pk_bf16_f32 v76, v76, v77
	v_cvt_pk_bf16_f32 v77, v80, v81
	v_cvt_pk_bf16_f32 v78, v78, v79
	v_lshl_add_u64 v[176:177], v[176:177], 0, v[152:153]
	v_cvt_pk_bf16_f32 v79, v70, v71
	global_store_dwordx4 v[176:177], v[76:79], off sc0 sc1
	v_pk_mul_f32 v[80:81], v[158:159], v[120:121] op_sel_hi:[0,1]
	v_pk_mul_f32 v[70:71], v[158:159], v[122:123] op_sel_hi:[0,1]
	v_pk_mul_f32 v[78:79], v[158:159], v[126:127] op_sel_hi:[0,1]
	v_pk_mul_f32 v[120:121], v[8:9], v[78:79]
	v_pk_mul_f32 v[76:77], v[158:159], v[118:119] op_sel_hi:[0,1]
	v_pk_mul_f32 v[126:127], v[6:7], v[80:81]
	v_pk_mul_f32 v[122:123], v[70:71], v[4:5]
	v_pk_mul_f32 v[178:179], v[76:77], v[2:3]
	v_cvt_pk_bf16_f32 v118, v126, v127
	v_cvt_pk_bf16_f32 v119, v120, v121
	v_pk_mul_f32 v[58:59], v[114:115], v[58:59] op_sel_hi:[0,1]
	v_cvt_pk_bf16_f32 v120, v178, v179
	v_cvt_pk_bf16_f32 v121, v122, v123
	global_store_dwordx4 v[176:177], v[118:121], off offset:256 sc0 sc1
	v_pk_mul_f32 v[122:123], v[46:47], v[58:59]
	v_pk_mul_f32 v[46:47], v[114:115], v[92:93] op_sel_hi:[0,1]
	v_lshlrev_b64 v[118:119], 11, v[124:125]
	v_pk_mul_f32 v[120:121], v[48:49], v[96:97]
	v_pk_mul_f32 v[48:49], v[114:115], v[90:91] op_sel_hi:[0,1]
	v_lshl_add_u64 v[118:119], s[48:49], 0, v[118:119]
	v_pk_mul_f32 v[90:91], v[44:45], v[46:47]
	v_pk_mul_f32 v[44:45], v[42:43], v[48:49]
	v_cvt_pk_bf16_f32 v42, v122, v123
	v_cvt_pk_bf16_f32 v43, v120, v121
	s_cmp_lg_u32 s46, 1
	v_cvt_pk_bf16_f32 v44, v44, v45
	v_cvt_pk_bf16_f32 v45, v90, v91
	v_lshl_add_u64 v[90:91], v[118:119], 0, v[152:153]
	global_store_dwordx4 v[90:91], v[42:45], off sc0 sc1
	s_nop 1
	v_pk_mul_f32 v[42:43], v[114:115], v[102:103] op_sel_hi:[0,1]
	v_pk_mul_f32 v[44:45], v[114:115], v[98:99] op_sel_hi:[0,1]
	v_pk_mul_f32 v[92:93], v[8:9], v[42:43]
	v_pk_mul_f32 v[98:99], v[6:7], v[44:45]
	v_pk_mul_f32 v[6:7], v[114:115], v[100:101] op_sel_hi:[0,1]
	v_pk_mul_f32 v[8:9], v[114:115], v[94:95] op_sel_hi:[0,1]
	v_pk_mul_f32 v[94:95], v[4:5], v[6:7]
	v_pk_mul_f32 v[4:5], v[2:3], v[8:9]
	v_cvt_pk_bf16_f32 v2, v98, v99
	v_cvt_pk_bf16_f32 v3, v92, v93
	s_nop 0
	v_cvt_pk_bf16_f32 v4, v4, v5
	v_cvt_pk_bf16_f32 v5, v94, v95
	global_store_dwordx4 v[90:91], v[2:5], off offset:256 sc0 sc1
	s_cbranch_scc1 .LBB0_135
	s_ashr_i32 s35, s44, 2
	s_and_b32 s35, s35, -8
	s_lshl_b32 s31, s31, 1
	s_or_b32 s46, s35, s31
	s_lshl_b32 s31, s44, 7
	s_ashr_i32 s47, s46, 31
	s_and_b32 s31, s31, 0xf80
	s_lshl_b64 s[44:45], s[46:47], 14
	s_lshl_b64 s[48:49], s[10:11], 2
	s_add_u32 s48, s64, s48
	v_ashrrev_i32_e32 v51, 31, v50
	s_addc_u32 s49, s65, s49
	v_lshl_add_u64 v[2:3], v[50:51], 2, s[48:49]
	v_mov_b64_e32 v[90:91], v[236:237]
	v_mov_b64_e32 v[92:93], v[238:239]
	v_pk_add_f32 v[4:5], v[72:73], 0 op_sel_hi:[1,0]
	v_pk_add_f32 v[72:73], v[74:75], 0 op_sel_hi:[1,0]
	v_pk_add_f32 v[4:5], v[4:5], v[112:113]
	v_pk_add_f32 v[72:73], v[72:73], v[116:117]
	v_pk_add_f32 v[4:5], v[4:5], v[154:155]
	v_pk_add_f32 v[72:73], v[72:73], v[156:157]
	v_pk_add_f32 v[4:5], v[4:5], v[170:171]
	v_pk_add_f32 v[72:73], v[72:73], v[182:183]
	v_pk_add_f32 v[4:5], v[4:5], v[168:169]
	v_pk_add_f32 v[72:73], v[72:73], v[184:185]
	v_pk_add_f32 v[4:5], v[4:5], v[186:187]
	v_pk_add_f32 v[72:73], v[72:73], v[188:189]
	v_pk_add_f32 v[4:5], v[4:5], v[172:173]
	v_pk_add_f32 v[72:73], v[72:73], v[174:175]
	v_pk_add_f32 v[4:5], v[4:5], v[96:97]
	v_pk_add_f32 v[58:59], v[72:73], v[58:59]
	v_pk_mul_f32 v[4:5], v[4:5], v[92:93]
	v_pk_mul_f32 v[58:59], v[58:59], v[90:91]
	ds_bpermute_b32 v72, v215, v58
	ds_bpermute_b32 v73, v215, v59
	ds_bpermute_b32 v74, v215, v4
	ds_bpermute_b32 v75, v215, v5
	s_waitcnt lgkmcnt(3)
	v_add_f32_e32 v58, v58, v72
	s_waitcnt lgkmcnt(2)
	v_add_f32_e32 v59, v59, v73
	s_waitcnt lgkmcnt(1)
	v_add_f32_e32 v4, v4, v74
	s_waitcnt lgkmcnt(0)
	v_add_f32_e32 v5, v5, v75
	ds_bpermute_b32 v72, v229, v58
	ds_bpermute_b32 v73, v229, v59
	ds_bpermute_b32 v74, v229, v4
	ds_bpermute_b32 v75, v229, v5
	s_waitcnt lgkmcnt(3)
	v_add_f32_e32 v58, v58, v72
	s_waitcnt lgkmcnt(2)
	v_add_f32_e32 v59, v59, v73
	s_waitcnt lgkmcnt(1)
	v_add_f32_e32 v72, v4, v74
	s_waitcnt lgkmcnt(0)
	v_add_f32_e32 v73, v5, v75
	ds_bpermute_b32 v4, v230, v58
	ds_bpermute_b32 v5, v230, v59
	ds_bpermute_b32 v74, v230, v72
	ds_bpermute_b32 v75, v230, v73
	s_waitcnt lgkmcnt(3)
	v_add_f32_e32 v4, v58, v4
	s_waitcnt lgkmcnt(2)
	v_add_f32_e32 v5, v59, v5
	s_waitcnt lgkmcnt(1)
	v_add_f32_e32 v58, v72, v74
	s_waitcnt lgkmcnt(0)
	v_add_f32_e32 v74, v73, v75
	ds_bpermute_b32 v59, v231, v4
	ds_bpermute_b32 v72, v231, v5
	ds_bpermute_b32 v73, v231, v58
	ds_bpermute_b32 v75, v231, v74
	s_and_saveexec_b64 s[48:49], s[6:7]
	s_cbranch_execz .LBB0_128
	s_add_u32 s10, s0, s44
	s_addc_u32 s35, s1, s45
	s_lshl_b32 s47, s31, 2
	s_add_u32 s10, s10, s47
	s_addc_u32 s35, s35, 0
	s_lshl_b32 s47, s60, 2
	s_add_u32 s50, s10, s47
	s_waitcnt lgkmcnt(3)
	v_add_f32_e32 v59, v4, v59
	s_addc_u32 s51, s35, 0
	s_waitcnt lgkmcnt(2)
	v_add_f32_e32 v72, v5, v72
	v_lshl_add_u64 v[4:5], v[50:51], 2, s[50:51]
	v_mul_f32_e32 v59, 0x3b800000, v59
	s_waitcnt lgkmcnt(1)
	v_add_f32_e32 v58, v58, v73
	global_atomic_add_f32 v[4:5], v59, off
	v_mul_f32_e32 v59, 0x3b800000, v72
	s_waitcnt lgkmcnt(0)
	v_add_f32_e32 v74, v74, v75
	global_atomic_add_f32 v[4:5], v59, off offset:4
	v_mul_f32_e32 v58, 0x3b800000, v58
	global_atomic_add_f32 v[4:5], v58, off offset:8
	v_mul_f32_e32 v58, 0x3b800000, v74
	global_atomic_add_f32 v[4:5], v58, off offset:12

.LBB0_883:
	v_mov_b32_e32 v84, 0
	v_mov_b32_e32 v82, 0
	v_cvt_f32_i32_e32 v155, v155
	v_add_u32_e32 v82, v82, v1
	v_lshl_add_u32 v82, v82, 3, s67
	v_lshl_add_u32 v190, s42, 7, v82
	s_lshl_b32 s42, s42, 8
	s_ashr_i32 s43, s42, 31
	s_lshl_b64 s[42:43], s[42:43], 2
	s_add_u32 s42, s65, s42
	s_addc_u32 s43, s66, s43
	s_lshl_b32 s2, s52, 8
	v_add3_u32 v182, s2, v184, v84
	v_ashrrev_i32_e32 v191, 31, v190
	v_ashrrev_i32_e32 v83, 31, v82
	v_ashrrev_i32_e32 v183, 31, v182
	v_lshlrev_b64 v[90:91], 2, v[190:191]
	v_lshl_add_u64 v[86:87], v[82:83], 2, s[42:43]
	v_lshl_add_u64 v[82:83], v[182:183], 2, s[12:13]
	v_lshl_add_u64 v[92:93], s[4:5], 0, v[90:91]
	global_load_dword v189, v[82:83], off
	global_load_dword v198, v[82:83], off offset:64
	global_load_dword v199, v[82:83], off offset:128
	global_load_dword v200, v[82:83], off offset:192
	global_load_dword v201, v[82:83], off offset:512
	global_load_dword v202, v[82:83], off offset:576
	global_load_dword v203, v[82:83], off offset:640
	global_load_dword v204, v[82:83], off offset:704
	global_load_dwordx4 v[94:97], v[86:87], off offset:16
	global_load_dwordx4 v[106:109], v[86:87], off
	s_nop 0
	global_load_dwordx4 v[82:85], v[86:87], off offset:528
	s_nop 0
	global_load_dwordx4 v[86:89], v[86:87], off offset:512
	s_nop 0
	global_load_dwordx4 v[102:105], v[92:93], off offset:16
	global_load_dwordx4 v[110:113], v[92:93], off
	v_lshl_add_u64 v[90:91], s[30:31], 0, v[90:91]
	global_load_dwordx4 v[98:101], v[90:91], off
	s_nop 0
	global_load_dwordx4 v[90:93], v[90:91], off offset:16
	v_cvt_f32_i32_e32 v154, v154
	v_cvt_f32_i32_e32 v158, v158
	v_cvt_f32_i32_e32 v147, v147
	v_cvt_f32_i32_e32 v146, v146
	v_cvt_f32_i32_e32 v150, v150
	v_cvt_f32_i32_e32 v160, v160
	v_cvt_f32_i32_e32 v156, v156
	v_cvt_f32_i32_e32 v152, v152
	v_cvt_f32_i32_e32 v148, v148
	v_cvt_f32_i32_e32 v159, v159
	v_cvt_f32_i32_e32 v161, v161
	v_cvt_f32_i32_e32 v157, v157
	v_cvt_f32_i32_e32 v153, v153
	v_cvt_f32_i32_e32 v151, v151
	v_cvt_f32_i32_e32 v149, v149
	v_cvt_f32_i32_e32 v142, v142
	v_cvt_f32_i32_e32 v138, v138
	v_cvt_f32_i32_e32 v134, v134
	v_cvt_f32_i32_e32 v130, v130
	v_cvt_f32_i32_e32 v143, v143
	v_cvt_f32_i32_e32 v139, v139
	v_cvt_f32_i32_e32 v135, v135
	v_cvt_f32_i32_e32 v131, v131
	v_cvt_f32_i32_e32 v144, v144
	v_cvt_f32_i32_e32 v140, v140
	v_cvt_f32_i32_e32 v136, v136
	v_cvt_f32_i32_e32 v132, v132
	v_cvt_f32_i32_e32 v145, v145
	v_cvt_f32_i32_e32 v141, v141
	v_cvt_f32_i32_e32 v137, v137
	v_cvt_f32_i32_e32 v133, v133
	v_cvt_f32_i32_e32 v126, v126
	v_cvt_f32_i32_e32 v122, v122
	v_cvt_f32_i32_e32 v118, v118
	v_cvt_f32_i32_e32 v114, v114
	v_cvt_f32_i32_e32 v127, v127
	v_cvt_f32_i32_e32 v123, v123
	v_cvt_f32_i32_e32 v119, v119
	v_cvt_f32_i32_e32 v115, v115
	v_cvt_f32_i32_e32 v128, v128
	v_cvt_f32_i32_e32 v124, v124
	v_cvt_f32_i32_e32 v120, v120
	v_cvt_f32_i32_e32 v116, v116
	v_cvt_f32_i32_e32 v129, v129
	v_cvt_f32_i32_e32 v125, v125
	v_cvt_f32_i32_e32 v121, v121
	v_cvt_f32_i32_e32 v117, v117
	v_cvt_f32_i32_e32 v78, v78
	v_cvt_f32_i32_e32 v74, v74
	v_cvt_f32_i32_e32 v70, v70
	v_cvt_f32_i32_e32 v66, v66
	v_cvt_f32_i32_e32 v79, v79
	v_cvt_f32_i32_e32 v75, v75
	v_cvt_f32_i32_e32 v71, v71
	v_cvt_f32_i32_e32 v67, v67
	v_cvt_f32_i32_e32 v80, v80
	v_cvt_f32_i32_e32 v76, v76
	v_cvt_f32_i32_e32 v72, v72
	v_cvt_f32_i32_e32 v68, v68
	v_cvt_f32_i32_e32 v81, v81
	v_cvt_f32_i32_e32 v77, v77
	v_cvt_f32_i32_e32 v73, v73
	v_cvt_f32_i32_e32 v69, v69
	v_cvt_f32_i32_e32 v50, v50
	v_cvt_f32_i32_e32 v54, v54
	v_cvt_f32_i32_e32 v62, v62
	v_cvt_f32_i32_e32 v58, v58
	v_cvt_f32_i32_e32 v55, v55
	v_cvt_f32_i32_e32 v51, v51
	v_cvt_f32_i32_e32 v59, v59
	v_cvt_f32_i32_e32 v63, v63
	v_cvt_f32_i32_e32 v56, v56
	s_waitcnt vmcnt(0)
	v_mul_f32_e32 v155, v155, v189
	v_mul_f32_e32 v154, v154, v189
	v_mul_f32_e32 v158, v158, v189
	v_mul_f32_e32 v147, v147, v189
	v_fma_f32 v155, v95, v155, v103
	v_mul_f32_e32 v155, 0xbfb8aa3b, v155
	v_fma_f32 v154, v94, v154, v102
	v_exp_f32_e32 v155, v155
	v_mul_f32_e32 v154, 0xbfb8aa3b, v154
	v_fma_f32 v158, v106, v158, v110
	v_fma_f32 v147, v83, v147, v91
	v_exp_f32_e32 v154, v154
	v_mul_f32_e32 v146, v146, v189
	v_mul_f32_e32 v158, 0xbfb8aa3b, v158
	v_mul_f32_e32 v147, 0xbfb8aa3b, v147
	v_fma_f32 v146, v82, v146, v90
	v_exp_f32_e32 v158, v158
	v_exp_f32_e32 v147, v147
	v_add_f32_e32 v155, 1.0, v155
	v_mul_f32_e32 v150, v150, v189
	v_mul_f32_e32 v146, 0xbfb8aa3b, v146
	v_rcp_f32_e32 v155, v155
	v_fma_f32 v150, v86, v150, v98
	v_exp_f32_e32 v146, v146
	v_add_f32_e32 v154, 1.0, v154
	v_mul_f32_e32 v150, 0xbfb8aa3b, v150
	v_rcp_f32_e32 v154, v154
	v_exp_f32_e32 v150, v150
	v_add_f32_e32 v158, 1.0, v158
	v_add_f32_e32 v147, 1.0, v147
	v_mul_f32_e32 v160, v160, v189
	v_rcp_f32_e32 v158, v158
	v_rcp_f32_e32 v195, v147
	v_mul_f32_e32 v197, v147, v155
	v_mul_f32_e32 v147, v156, v189
	v_fma_f32 v160, v108, v160, v112
	v_add_f32_e32 v146, 1.0, v146
	v_fma_f32 v147, v96, v147, v104
	v_rcp_f32_e32 v193, v146
	v_mul_f32_e32 v196, v146, v154
	v_mul_f32_e32 v146, 0xbfb8aa3b, v160
	v_mul_f32_e32 v147, 0xbfb8aa3b, v147
	v_add_f32_e32 v150, 1.0, v150
	v_exp_f32_e32 v146, v146
	v_exp_f32_e32 v147, v147
	v_rcp_f32_e32 v192, v150
	v_mul_f32_e32 v158, v150, v158
	v_mul_f32_e32 v150, v152, v189
	v_mul_f32_e32 v148, v148, v189
	v_fma_f32 v150, v88, v150, v100
	v_fma_f32 v148, v84, v148, v92
	v_mul_f32_e32 v150, 0xbfb8aa3b, v150
	v_mul_f32_e32 v148, 0xbfb8aa3b, v148
	v_exp_f32_e32 v150, v150
	v_exp_f32_e32 v148, v148
	v_add_f32_e32 v146, 1.0, v146
	v_add_f32_e32 v147, 1.0, v147
	v_rcp_f32_e32 v146, v146
	v_rcp_f32_e32 v147, v147
	v_mul_f32_e32 v159, v159, v189
	v_add_f32_e32 v150, 1.0, v150
	v_add_f32_e32 v148, 1.0, v148
	v_fma_f32 v159, v107, v159, v111
	v_mul_f32_e32 v156, v150, v146
	v_mul_f32_e32 v160, v148, v147
	v_mul_f32_e32 v146, v161, v189
	v_mul_f32_e32 v147, v157, v189
	v_mul_f32_e32 v159, 0xbfb8aa3b, v159
	v_fma_f32 v146, v109, v146, v113
	v_fma_f32 v147, v97, v147, v105
	v_exp_f32_e32 v159, v159
	v_mul_f32_e32 v146, 0xbfb8aa3b, v146
	v_mul_f32_e32 v147, 0xbfb8aa3b, v147
	v_mul_f32_e32 v151, v151, v189
	v_rcp_f32_e32 v152, v148
	v_exp_f32_e32 v146, v146
	v_exp_f32_e32 v147, v147
	v_mul_f32_e32 v148, v153, v189
	v_mul_f32_e32 v149, v149, v189
	v_fma_f32 v151, v87, v151, v99
	v_fma_f32 v148, v89, v148, v101
	v_fma_f32 v149, v85, v149, v93
	v_mul_f32_e32 v151, 0xbfb8aa3b, v151
	v_mul_f32_e32 v148, 0xbfb8aa3b, v148
	v_mul_f32_e32 v149, 0xbfb8aa3b, v149
	v_exp_f32_e32 v151, v151
	v_add_f32_e32 v159, 1.0, v159
	v_exp_f32_e32 v148, v148
	v_exp_f32_e32 v149, v149
	v_rcp_f32_e32 v159, v159
	v_add_f32_e32 v146, 1.0, v146
	v_add_f32_e32 v147, 1.0, v147
	v_rcp_f32_e32 v146, v146
	v_rcp_f32_e32 v147, v147
	v_add_f32_e32 v151, 1.0, v151
	v_add_f32_e32 v148, 1.0, v148
	v_add_f32_e32 v149, 1.0, v149
	v_rcp_f32_e32 v194, v151
	v_mul_f32_e32 v159, v151, v159
	v_rcp_f32_e32 v151, v150
	v_rcp_f32_e32 v150, v148
	v_rcp_f32_e32 v153, v149
	v_mul_f32_e32 v157, v148, v146
	v_mul_f32_e32 v161, v149, v147
	v_cvt_pk_bf16_f32 v148, v192, v194
	v_cvt_pk_bf16_f32 v149, v151, v150
	v_cvt_pk_bf16_f32 v150, v193, v195
	v_cvt_pk_bf16_f32 v151, v152, v153
	v_lshlrev_b64 v[152:153], 12, v[182:183]
	v_lshl_add_u64 v[154:155], s[16:17], 0, v[152:153]
	v_lshlrev_b64 v[146:147], 1, v[190:191]
	v_lshl_add_u64 v[154:155], v[154:155], 0, v[146:147]
	v_lshl_add_u64 v[152:153], s[10:11], 0, v[152:153]
	global_store_dwordx4 v[154:155], v[148:151], off sc0 sc1
	v_lshl_add_u64 v[152:153], v[152:153], 0, v[146:147]
	v_cvt_f32_i32_e32 v52, v52
	v_cvt_pk_bf16_f32 v148, v158, v159
	v_cvt_pk_bf16_f32 v149, v156, v157
	v_cvt_pk_bf16_f32 v150, v196, v197
	v_cvt_pk_bf16_f32 v151, v160, v161
	global_store_dwordx4 v[152:153], v[148:151], off sc0 sc1
	v_cvt_f32_i32_e32 v60, v60
	v_cvt_f32_i32_e32 v64, v64
	v_add_u32_e32 v148, 16, v182
	v_ashrrev_i32_e32 v149, 31, v148
	v_lshl_add_u64 v[150:151], v[148:149], 2, s[12:13]
	v_mov_b32_e32 v150, v198
	v_cvt_f32_i32_e32 v57, v57
	v_cvt_f32_i32_e32 v53, v53
	v_cvt_f32_i32_e32 v61, v61
	v_cvt_f32_i32_e32 v65, v65
	v_cvt_f32_i32_e32 v34, v34
	v_cvt_f32_i32_e32 v38, v38
	v_cvt_f32_i32_e32 v46, v46
	v_cvt_f32_i32_e32 v42, v42
	v_cvt_f32_i32_e32 v39, v39
	v_cvt_f32_i32_e32 v35, v35
	v_cvt_f32_i32_e32 v43, v43
	v_cvt_f32_i32_e32 v47, v47
	v_cvt_f32_i32_e32 v40, v40
	v_cvt_f32_i32_e32 v36, v36
	v_cvt_f32_i32_e32 v44, v44
	v_cvt_f32_i32_e32 v48, v48
	v_cvt_f32_i32_e32 v41, v41
	v_cvt_f32_i32_e32 v37, v37
	v_cvt_f32_i32_e32 v45, v45
	v_cvt_f32_i32_e32 v49, v49
	v_cvt_f32_i32_e32 v18, v18
	v_cvt_f32_i32_e32 v22, v22
	v_cvt_f32_i32_e32 v30, v30
	v_cvt_f32_i32_e32 v26, v26
	v_cvt_f32_i32_e32 v23, v23
	v_cvt_f32_i32_e32 v19, v19
	v_cvt_f32_i32_e32 v27, v27
	v_cvt_f32_i32_e32 v31, v31
	v_cvt_f32_i32_e32 v24, v24
	v_cvt_f32_i32_e32 v20, v20
	v_cvt_f32_i32_e32 v28, v28
	v_cvt_f32_i32_e32 v32, v32
	v_cvt_f32_i32_e32 v25, v25
	v_cvt_f32_i32_e32 v21, v21
	v_cvt_f32_i32_e32 v29, v29
	v_cvt_f32_i32_e32 v33, v33
	v_cvt_f32_i32_e32 v2, v2
	v_cvt_f32_i32_e32 v6, v6
	v_cvt_f32_i32_e32 v14, v14
	v_cvt_f32_i32_e32 v10, v10
	v_cvt_f32_i32_e32 v7, v7
	v_cvt_f32_i32_e32 v3, v3
	v_cvt_f32_i32_e32 v11, v11
	v_cvt_f32_i32_e32 v15, v15
	v_cvt_f32_i32_e32 v8, v8
	v_cvt_f32_i32_e32 v4, v4
	v_cvt_f32_i32_e32 v12, v12
	v_cvt_f32_i32_e32 v16, v16
	v_cvt_f32_i32_e32 v9, v9
	v_cvt_f32_i32_e32 v5, v5
	v_cvt_f32_i32_e32 v13, v13
	v_cvt_f32_i32_e32 v17, v17
	s_andn2_b64 vcc, exec, s[6:7]
	s_mov_b64 s[6:7], -1
	v_mul_f32_e32 v142, v142, v150
	v_mul_f32_e32 v138, v138, v150
	v_fma_f32 v142, v106, v142, v110
	v_fma_f32 v138, v94, v138, v102
	v_mul_f32_e32 v142, 0xbfb8aa3b, v142
	v_mul_f32_e32 v138, 0xbfb8aa3b, v138
	v_exp_f32_e32 v142, v142
	v_exp_f32_e32 v138, v138
	v_mul_f32_e32 v134, v134, v150
	v_mul_f32_e32 v130, v130, v150
	v_fma_f32 v134, v86, v134, v98
	v_fma_f32 v130, v82, v130, v90
	v_mul_f32_e32 v134, 0xbfb8aa3b, v134
	v_mul_f32_e32 v130, 0xbfb8aa3b, v130
	v_exp_f32_e32 v134, v134
	v_exp_f32_e32 v130, v130
	v_add_f32_e32 v142, 1.0, v142
	v_add_f32_e32 v138, 1.0, v138
	v_rcp_f32_e32 v142, v142
	v_rcp_f32_e32 v138, v138
	v_add_f32_e32 v134, 1.0, v134
	v_add_f32_e32 v130, 1.0, v130
	v_rcp_f32_e32 v151, v134
	v_rcp_f32_e32 v152, v130
	v_mul_f32_e32 v142, v134, v142
	v_mul_f32_e32 v138, v130, v138
	v_mul_f32_e32 v130, v143, v150
	v_mul_f32_e32 v134, v139, v150
	v_fma_f32 v130, v107, v130, v111
	v_fma_f32 v134, v95, v134, v103
	v_mul_f32_e32 v130, 0xbfb8aa3b, v130
	v_mul_f32_e32 v134, 0xbfb8aa3b, v134
	v_exp_f32_e32 v130, v130
	v_exp_f32_e32 v134, v134
	v_mul_f32_e32 v135, v135, v150
	v_mul_f32_e32 v131, v131, v150
	v_fma_f32 v135, v87, v135, v99
	v_fma_f32 v131, v83, v131, v91
	v_mul_f32_e32 v135, 0xbfb8aa3b, v135
	v_mul_f32_e32 v131, 0xbfb8aa3b, v131
	v_exp_f32_e32 v135, v135
	v_exp_f32_e32 v131, v131
	v_add_f32_e32 v130, 1.0, v130
	v_add_f32_e32 v134, 1.0, v134
	v_rcp_f32_e32 v130, v130
	v_rcp_f32_e32 v134, v134
	v_add_f32_e32 v135, 1.0, v135
	v_add_f32_e32 v131, 1.0, v131
	v_rcp_f32_e32 v143, v131
	v_mul_f32_e32 v153, v135, v130
	v_mul_f32_e32 v154, v131, v134
	v_mul_f32_e32 v130, v144, v150
	v_mul_f32_e32 v131, v140, v150
	v_fma_f32 v130, v108, v130, v112
	v_fma_f32 v131, v96, v131, v104
	v_mul_f32_e32 v130, 0xbfb8aa3b, v130
	v_mul_f32_e32 v131, 0xbfb8aa3b, v131
	v_exp_f32_e32 v130, v130
	v_exp_f32_e32 v131, v131
	v_mul_f32_e32 v134, v136, v150
	v_mul_f32_e32 v132, v132, v150
	v_fma_f32 v134, v88, v134, v100
	v_fma_f32 v132, v84, v132, v92
	v_mul_f32_e32 v134, 0xbfb8aa3b, v134
	v_mul_f32_e32 v132, 0xbfb8aa3b, v132
	v_exp_f32_e32 v134, v134
	v_exp_f32_e32 v132, v132
	v_add_f32_e32 v130, 1.0, v130
	v_add_f32_e32 v131, 1.0, v131
	v_rcp_f32_e32 v130, v130
	v_rcp_f32_e32 v131, v131
	v_add_f32_e32 v134, 1.0, v134
	v_add_f32_e32 v132, 1.0, v132
	v_mul_f32_e32 v140, v134, v130
	v_mul_f32_e32 v144, v132, v131
	v_mul_f32_e32 v130, v145, v150
	v_mul_f32_e32 v131, v141, v150
	v_fma_f32 v130, v109, v130, v113
	v_fma_f32 v131, v97, v131, v105
	v_mul_f32_e32 v130, 0xbfb8aa3b, v130
	v_mul_f32_e32 v131, 0xbfb8aa3b, v131
	v_rcp_f32_e32 v136, v132
	v_exp_f32_e32 v130, v130
	v_exp_f32_e32 v131, v131
	v_mul_f32_e32 v132, v137, v150
	v_fma_f32 v132, v89, v132, v101
	v_mul_f32_e32 v133, v133, v150
	v_mul_f32_e32 v132, 0xbfb8aa3b, v132
	v_fma_f32 v133, v85, v133, v93
	v_exp_f32_e32 v132, v132
	v_mul_f32_e32 v133, 0xbfb8aa3b, v133
	v_exp_f32_e32 v133, v133
	v_add_f32_e32 v130, 1.0, v130
	v_add_f32_e32 v131, 1.0, v131
	v_rcp_f32_e32 v130, v130
	v_rcp_f32_e32 v131, v131
	v_add_f32_e32 v132, 1.0, v132
	v_rcp_f32_e32 v139, v135
	v_rcp_f32_e32 v135, v134
	v_add_f32_e32 v133, 1.0, v133
	v_rcp_f32_e32 v134, v132
	v_rcp_f32_e32 v137, v133
	v_mul_f32_e32 v141, v132, v130
	v_mul_f32_e32 v145, v133, v131
	v_cvt_pk_bf16_f32 v130, v151, v139
	v_cvt_pk_bf16_f32 v131, v135, v134
	v_lshlrev_b64 v[134:135], 12, v[148:149]
	v_cvt_pk_bf16_f32 v132, v152, v143
	v_cvt_pk_bf16_f32 v133, v136, v137
	v_lshl_add_u64 v[136:137], s[16:17], 0, v[134:135]
	v_lshl_add_u64 v[136:137], v[136:137], 0, v[146:147]
	v_lshl_add_u64 v[134:135], s[10:11], 0, v[134:135]
	global_store_dwordx4 v[136:137], v[130:133], off sc0 sc1
	v_lshl_add_u64 v[134:135], v[134:135], 0, v[146:147]
	s_nop 0
	v_cvt_pk_bf16_f32 v130, v142, v153
	v_cvt_pk_bf16_f32 v131, v140, v141
	v_cvt_pk_bf16_f32 v132, v138, v154
	v_cvt_pk_bf16_f32 v133, v144, v145
	global_store_dwordx4 v[134:135], v[130:133], off sc0 sc1
	s_nop 1
	v_add_u32_e32 v130, 32, v182
	v_ashrrev_i32_e32 v131, 31, v130
	v_lshl_add_u64 v[132:133], v[130:131], 2, s[12:13]
	v_mov_b32_e32 v132, v199
	v_mul_f32_e32 v126, v126, v132
	v_mul_f32_e32 v122, v122, v132
	v_fma_f32 v126, v106, v126, v110
	v_fma_f32 v122, v94, v122, v102
	v_mul_f32_e32 v126, 0xbfb8aa3b, v126
	v_mul_f32_e32 v122, 0xbfb8aa3b, v122
	v_exp_f32_e32 v126, v126
	v_exp_f32_e32 v122, v122
	v_mul_f32_e32 v118, v118, v132
	v_mul_f32_e32 v114, v114, v132
	v_fma_f32 v118, v86, v118, v98
	v_fma_f32 v114, v82, v114, v90
	v_mul_f32_e32 v118, 0xbfb8aa3b, v118
	v_mul_f32_e32 v114, 0xbfb8aa3b, v114
	v_exp_f32_e32 v118, v118
	v_exp_f32_e32 v114, v114
	v_add_f32_e32 v126, 1.0, v126
	v_add_f32_e32 v122, 1.0, v122
	v_rcp_f32_e32 v126, v126
	v_rcp_f32_e32 v122, v122
	v_add_f32_e32 v118, 1.0, v118
	v_add_f32_e32 v114, 1.0, v114
	v_rcp_f32_e32 v133, v118
	v_rcp_f32_e32 v134, v114
	v_mul_f32_e32 v126, v118, v126
	v_mul_f32_e32 v122, v114, v122
	v_mul_f32_e32 v114, v127, v132
	v_mul_f32_e32 v118, v123, v132
	v_fma_f32 v114, v107, v114, v111
	v_fma_f32 v118, v95, v118, v103
	v_mul_f32_e32 v114, 0xbfb8aa3b, v114
	v_mul_f32_e32 v118, 0xbfb8aa3b, v118
	v_exp_f32_e32 v114, v114
	v_exp_f32_e32 v118, v118
	v_mul_f32_e32 v119, v119, v132
	v_mul_f32_e32 v115, v115, v132
	v_fma_f32 v119, v87, v119, v99
	v_fma_f32 v115, v83, v115, v91
	v_mul_f32_e32 v119, 0xbfb8aa3b, v119
	v_mul_f32_e32 v115, 0xbfb8aa3b, v115
	v_exp_f32_e32 v119, v119
	v_exp_f32_e32 v115, v115
	v_add_f32_e32 v114, 1.0, v114
	v_add_f32_e32 v118, 1.0, v118
	v_rcp_f32_e32 v114, v114
	v_rcp_f32_e32 v118, v118
	v_add_f32_e32 v119, 1.0, v119
	v_add_f32_e32 v115, 1.0, v115
	v_rcp_f32_e32 v127, v115
	v_mul_f32_e32 v135, v119, v114
	v_mul_f32_e32 v136, v115, v118
	v_mul_f32_e32 v114, v128, v132
	v_mul_f32_e32 v115, v124, v132
	v_fma_f32 v114, v108, v114, v112
	v_fma_f32 v115, v96, v115, v104
	v_mul_f32_e32 v114, 0xbfb8aa3b, v114
	v_mul_f32_e32 v115, 0xbfb8aa3b, v115
	v_exp_f32_e32 v114, v114
	v_exp_f32_e32 v115, v115
	v_mul_f32_e32 v118, v120, v132
	v_mul_f32_e32 v116, v116, v132
	v_fma_f32 v118, v88, v118, v100
	v_fma_f32 v116, v84, v116, v92
	v_mul_f32_e32 v118, 0xbfb8aa3b, v118
	v_mul_f32_e32 v116, 0xbfb8aa3b, v116
	v_exp_f32_e32 v118, v118
	v_exp_f32_e32 v116, v116
	v_add_f32_e32 v114, 1.0, v114
	v_add_f32_e32 v115, 1.0, v115
	v_rcp_f32_e32 v114, v114
	v_rcp_f32_e32 v115, v115
	v_add_f32_e32 v118, 1.0, v118
	v_add_f32_e32 v116, 1.0, v116
	v_mul_f32_e32 v124, v118, v114
	v_mul_f32_e32 v128, v116, v115
	v_mul_f32_e32 v114, v129, v132
	v_mul_f32_e32 v115, v125, v132
	v_fma_f32 v114, v109, v114, v113
	v_fma_f32 v115, v97, v115, v105
	v_mul_f32_e32 v114, 0xbfb8aa3b, v114
	v_mul_f32_e32 v115, 0xbfb8aa3b, v115
	v_rcp_f32_e32 v120, v116
	v_exp_f32_e32 v114, v114
	v_exp_f32_e32 v115, v115
	v_mul_f32_e32 v116, v121, v132
	v_fma_f32 v116, v89, v116, v101
	v_mul_f32_e32 v117, v117, v132
	v_mul_f32_e32 v116, 0xbfb8aa3b, v116
	v_fma_f32 v117, v85, v117, v93
	v_exp_f32_e32 v116, v116
	v_mul_f32_e32 v117, 0xbfb8aa3b, v117
	v_exp_f32_e32 v117, v117
	v_add_f32_e32 v114, 1.0, v114
	v_add_f32_e32 v115, 1.0, v115
	v_rcp_f32_e32 v114, v114
	v_rcp_f32_e32 v115, v115
	v_add_f32_e32 v116, 1.0, v116
	v_rcp_f32_e32 v123, v119
	v_rcp_f32_e32 v119, v118
	v_add_f32_e32 v117, 1.0, v117
	v_rcp_f32_e32 v118, v116
	v_rcp_f32_e32 v121, v117
	v_mul_f32_e32 v125, v116, v114
	v_mul_f32_e32 v129, v117, v115
	v_cvt_pk_bf16_f32 v114, v133, v123
	v_cvt_pk_bf16_f32 v115, v119, v118
	v_lshlrev_b64 v[118:119], 12, v[130:131]
	v_cvt_pk_bf16_f32 v116, v134, v127
	v_cvt_pk_bf16_f32 v117, v120, v121
	v_lshl_add_u64 v[120:121], s[16:17], 0, v[118:119]
	v_lshl_add_u64 v[120:121], v[120:121], 0, v[146:147]
	v_lshl_add_u64 v[118:119], s[10:11], 0, v[118:119]
	global_store_dwordx4 v[120:121], v[114:117], off sc0 sc1
	v_lshl_add_u64 v[118:119], v[118:119], 0, v[146:147]
	s_nop 0
	v_cvt_pk_bf16_f32 v114, v126, v135
	v_cvt_pk_bf16_f32 v115, v124, v125
	v_cvt_pk_bf16_f32 v116, v122, v136
	v_cvt_pk_bf16_f32 v117, v128, v129
	global_store_dwordx4 v[118:119], v[114:117], off sc0 sc1
	s_nop 1
	v_add_u32_e32 v114, 48, v182
	v_ashrrev_i32_e32 v115, 31, v114
	v_lshl_add_u64 v[116:117], v[114:115], 2, s[12:13]
	v_mov_b32_e32 v116, v200
	v_mul_f32_e32 v78, v78, v116
	v_mul_f32_e32 v74, v74, v116
	v_fma_f32 v78, v106, v78, v110
	v_fma_f32 v74, v94, v74, v102
	v_mul_f32_e32 v78, 0xbfb8aa3b, v78
	v_mul_f32_e32 v74, 0xbfb8aa3b, v74
	v_exp_f32_e32 v78, v78
	v_exp_f32_e32 v74, v74
	v_mul_f32_e32 v70, v70, v116
	v_mul_f32_e32 v66, v66, v116
	v_fma_f32 v70, v86, v70, v98
	v_fma_f32 v66, v82, v66, v90
	v_mul_f32_e32 v70, 0xbfb8aa3b, v70
	v_mul_f32_e32 v66, 0xbfb8aa3b, v66
	v_exp_f32_e32 v70, v70
	v_exp_f32_e32 v66, v66
	v_add_f32_e32 v78, 1.0, v78
	v_add_f32_e32 v74, 1.0, v74
	v_rcp_f32_e32 v78, v78
	v_rcp_f32_e32 v74, v74
	v_add_f32_e32 v70, 1.0, v70
	v_add_f32_e32 v66, 1.0, v66
	v_rcp_f32_e32 v117, v70
	v_rcp_f32_e32 v118, v66
	v_mul_f32_e32 v78, v70, v78
	v_mul_f32_e32 v74, v66, v74
	v_mul_f32_e32 v66, v79, v116
	v_mul_f32_e32 v70, v75, v116
	v_fma_f32 v66, v107, v66, v111
	v_fma_f32 v70, v95, v70, v103
	v_mul_f32_e32 v66, 0xbfb8aa3b, v66
	v_mul_f32_e32 v70, 0xbfb8aa3b, v70
	v_exp_f32_e32 v66, v66
	v_exp_f32_e32 v70, v70
	v_mul_f32_e32 v71, v71, v116
	v_mul_f32_e32 v67, v67, v116
	v_fma_f32 v71, v87, v71, v99
	v_fma_f32 v67, v83, v67, v91
	v_mul_f32_e32 v71, 0xbfb8aa3b, v71
	v_mul_f32_e32 v67, 0xbfb8aa3b, v67
	v_exp_f32_e32 v71, v71
	v_exp_f32_e32 v67, v67
	v_add_f32_e32 v66, 1.0, v66
	v_add_f32_e32 v70, 1.0, v70
	v_rcp_f32_e32 v66, v66
	v_rcp_f32_e32 v70, v70
	v_add_f32_e32 v71, 1.0, v71
	v_add_f32_e32 v67, 1.0, v67
	v_rcp_f32_e32 v79, v67
	v_mul_f32_e32 v119, v71, v66
	v_mul_f32_e32 v120, v67, v70
	v_mul_f32_e32 v66, v80, v116
	v_mul_f32_e32 v67, v76, v116
	v_fma_f32 v66, v108, v66, v112
	v_fma_f32 v67, v96, v67, v104
	v_mul_f32_e32 v66, 0xbfb8aa3b, v66
	v_mul_f32_e32 v67, 0xbfb8aa3b, v67
	v_exp_f32_e32 v66, v66
	v_exp_f32_e32 v67, v67
	v_mul_f32_e32 v70, v72, v116
	v_mul_f32_e32 v68, v68, v116
	v_fma_f32 v70, v88, v70, v100
	v_fma_f32 v68, v84, v68, v92
	v_mul_f32_e32 v70, 0xbfb8aa3b, v70
	v_mul_f32_e32 v68, 0xbfb8aa3b, v68
	v_exp_f32_e32 v70, v70
	v_exp_f32_e32 v68, v68
	v_add_f32_e32 v66, 1.0, v66
	v_add_f32_e32 v67, 1.0, v67
	v_rcp_f32_e32 v66, v66
	v_rcp_f32_e32 v67, v67
	v_add_f32_e32 v70, 1.0, v70
	v_add_f32_e32 v68, 1.0, v68
	v_mul_f32_e32 v76, v70, v66
	v_mul_f32_e32 v80, v68, v67
	v_mul_f32_e32 v66, v81, v116
	v_mul_f32_e32 v67, v77, v116
	v_fma_f32 v66, v109, v66, v113
	v_fma_f32 v67, v97, v67, v105
	v_mul_f32_e32 v66, 0xbfb8aa3b, v66
	v_mul_f32_e32 v67, 0xbfb8aa3b, v67
	v_rcp_f32_e32 v72, v68
	v_exp_f32_e32 v66, v66
	v_exp_f32_e32 v67, v67
	v_mul_f32_e32 v68, v73, v116
	v_fma_f32 v68, v89, v68, v101
	v_mul_f32_e32 v69, v69, v116
	v_mul_f32_e32 v68, 0xbfb8aa3b, v68
	v_fma_f32 v69, v85, v69, v93
	v_exp_f32_e32 v68, v68
	v_mul_f32_e32 v69, 0xbfb8aa3b, v69
	v_exp_f32_e32 v69, v69
	v_add_f32_e32 v66, 1.0, v66
	v_add_f32_e32 v67, 1.0, v67
	v_rcp_f32_e32 v66, v66
	v_rcp_f32_e32 v67, v67
	v_add_f32_e32 v68, 1.0, v68
	v_rcp_f32_e32 v75, v71
	v_rcp_f32_e32 v71, v70
	v_add_f32_e32 v69, 1.0, v69
	v_rcp_f32_e32 v70, v68
	v_rcp_f32_e32 v73, v69
	v_mul_f32_e32 v77, v68, v66
	v_mul_f32_e32 v81, v69, v67
	v_cvt_pk_bf16_f32 v66, v117, v75
	v_cvt_pk_bf16_f32 v67, v71, v70
	v_lshlrev_b64 v[70:71], 12, v[114:115]
	v_cvt_pk_bf16_f32 v68, v118, v79
	v_cvt_pk_bf16_f32 v69, v72, v73
	v_lshl_add_u64 v[72:73], s[16:17], 0, v[70:71]
	v_lshl_add_u64 v[72:73], v[72:73], 0, v[146:147]
	v_lshl_add_u64 v[70:71], s[10:11], 0, v[70:71]
	global_store_dwordx4 v[72:73], v[66:69], off sc0 sc1
	v_lshl_add_u64 v[70:71], v[70:71], 0, v[146:147]
	s_nop 0
	v_cvt_pk_bf16_f32 v66, v78, v119
	v_cvt_pk_bf16_f32 v67, v76, v77
	v_cvt_pk_bf16_f32 v68, v74, v120
	v_cvt_pk_bf16_f32 v69, v80, v81
	global_store_dwordx4 v[70:71], v[66:69], off sc0 sc1
	s_nop 1
	v_add_u32_e32 v66, 0x80, v182
	v_ashrrev_i32_e32 v67, 31, v66
	v_lshl_add_u64 v[68:69], v[66:67], 2, s[12:13]
	v_mov_b32_e32 v68, v201
	v_mul_f32_e32 v50, v50, v68
	v_fma_f32 v50, v94, v50, v102
	v_mul_f32_e32 v50, 0xbfb8aa3b, v50
	v_exp_f32_e32 v50, v50
	v_mul_f32_e32 v54, v54, v68
	v_mul_f32_e32 v62, v62, v68
	v_fma_f32 v54, v106, v54, v110
	v_fma_f32 v62, v82, v62, v90
	v_mul_f32_e32 v54, 0xbfb8aa3b, v54
	v_mul_f32_e32 v62, 0xbfb8aa3b, v62
	v_exp_f32_e32 v54, v54
	v_exp_f32_e32 v62, v62
	v_add_f32_e32 v50, 1.0, v50
	v_mul_f32_e32 v58, v58, v68
	v_rcp_f32_e32 v50, v50
	v_fma_f32 v58, v86, v58, v98
	v_mul_f32_e32 v58, 0xbfb8aa3b, v58
	v_exp_f32_e32 v58, v58
	v_add_f32_e32 v54, 1.0, v54
	v_add_f32_e32 v62, 1.0, v62
	v_rcp_f32_e32 v54, v54
	v_rcp_f32_e32 v70, v62
	v_mul_f32_e32 v62, v62, v50
	v_mul_f32_e32 v50, v55, v68
	v_mul_f32_e32 v51, v51, v68
	v_fma_f32 v50, v107, v50, v111
	v_fma_f32 v51, v95, v51, v103
	v_mul_f32_e32 v50, 0xbfb8aa3b, v50
	v_mul_f32_e32 v51, 0xbfb8aa3b, v51
	v_add_f32_e32 v58, 1.0, v58
	v_exp_f32_e32 v50, v50
	v_exp_f32_e32 v51, v51
	v_rcp_f32_e32 v69, v58
	v_mul_f32_e32 v58, v58, v54
	v_mul_f32_e32 v54, v59, v68
	v_mul_f32_e32 v55, v63, v68
	v_fma_f32 v54, v87, v54, v99
	v_fma_f32 v55, v83, v55, v91
	v_mul_f32_e32 v54, 0xbfb8aa3b, v54
	v_mul_f32_e32 v55, 0xbfb8aa3b, v55
	v_exp_f32_e32 v54, v54
	v_exp_f32_e32 v55, v55
	v_add_f32_e32 v50, 1.0, v50
	v_add_f32_e32 v51, 1.0, v51
	v_rcp_f32_e32 v50, v50
	v_rcp_f32_e32 v51, v51
	v_add_f32_e32 v54, 1.0, v54
	v_add_f32_e32 v55, 1.0, v55
	v_mul_f32_e32 v71, v54, v50
	v_mul_f32_e32 v72, v55, v51
	v_mul_f32_e32 v50, v56, v68
	v_mul_f32_e32 v51, v52, v68
	v_fma_f32 v50, v108, v50, v112
	v_fma_f32 v51, v96, v51, v104
	v_mul_f32_e32 v50, 0xbfb8aa3b, v50
	v_mul_f32_e32 v51, 0xbfb8aa3b, v51
	v_exp_f32_e32 v50, v50
	v_exp_f32_e32 v51, v51
	v_rcp_f32_e32 v59, v54
	v_mul_f32_e32 v52, v60, v68
	v_mul_f32_e32 v54, v64, v68
	v_fma_f32 v52, v88, v52, v100
	v_fma_f32 v54, v84, v54, v92
	v_mul_f32_e32 v52, 0xbfb8aa3b, v52
	v_mul_f32_e32 v54, 0xbfb8aa3b, v54
	v_exp_f32_e32 v52, v52
	v_exp_f32_e32 v54, v54
	v_add_f32_e32 v50, 1.0, v50
	v_add_f32_e32 v51, 1.0, v51
	v_rcp_f32_e32 v50, v50
	v_rcp_f32_e32 v51, v51
	v_add_f32_e32 v52, 1.0, v52
	v_add_f32_e32 v54, 1.0, v54
	v_mul_f32_e32 v60, v52, v50
	v_mul_f32_e32 v64, v54, v51
	v_mul_f32_e32 v50, v57, v68
	v_mul_f32_e32 v51, v53, v68
	v_fma_f32 v50, v109, v50, v113
	v_fma_f32 v51, v97, v51, v105
	v_mul_f32_e32 v50, 0xbfb8aa3b, v50
	v_mul_f32_e32 v51, 0xbfb8aa3b, v51
	v_rcp_f32_e32 v63, v55
	v_rcp_f32_e32 v55, v52
	v_exp_f32_e32 v50, v50
	v_exp_f32_e32 v51, v51
	v_mul_f32_e32 v52, v61, v68
	v_fma_f32 v52, v89, v52, v101
	v_mul_f32_e32 v53, v65, v68
	v_mul_f32_e32 v52, 0xbfb8aa3b, v52
	v_fma_f32 v53, v85, v53, v93
	v_exp_f32_e32 v52, v52
	v_mul_f32_e32 v53, 0xbfb8aa3b, v53
	v_exp_f32_e32 v53, v53
	v_add_f32_e32 v50, 1.0, v50
	v_add_f32_e32 v51, 1.0, v51
	v_rcp_f32_e32 v50, v50
	v_rcp_f32_e32 v51, v51
	v_add_f32_e32 v52, 1.0, v52
	v_rcp_f32_e32 v56, v54
	v_add_f32_e32 v53, 1.0, v53
	v_rcp_f32_e32 v54, v52
	v_rcp_f32_e32 v57, v53
	v_mul_f32_e32 v61, v52, v50
	v_mul_f32_e32 v65, v53, v51
	v_cvt_pk_bf16_f32 v50, v69, v59
	v_cvt_pk_bf16_f32 v51, v55, v54
	v_lshlrev_b64 v[54:55], 12, v[66:67]
	v_cvt_pk_bf16_f32 v52, v70, v63
	v_cvt_pk_bf16_f32 v53, v56, v57
	v_lshl_add_u64 v[56:57], s[16:17], 0, v[54:55]
	v_lshl_add_u64 v[56:57], v[56:57], 0, v[146:147]
	v_lshl_add_u64 v[54:55], s[10:11], 0, v[54:55]
	global_store_dwordx4 v[56:57], v[50:53], off sc0 sc1
	v_lshl_add_u64 v[54:55], v[54:55], 0, v[146:147]
	s_nop 0
	v_cvt_pk_bf16_f32 v50, v58, v71
	v_cvt_pk_bf16_f32 v51, v60, v61
	v_cvt_pk_bf16_f32 v52, v62, v72
	v_cvt_pk_bf16_f32 v53, v64, v65
	global_store_dwordx4 v[54:55], v[50:53], off sc0 sc1
	s_nop 1
	v_add_u32_e32 v50, 0x90, v182
	v_ashrrev_i32_e32 v51, 31, v50
	v_lshl_add_u64 v[52:53], v[50:51], 2, s[12:13]
	v_mov_b32_e32 v52, v202
	v_mul_f32_e32 v34, v34, v52
	v_fma_f32 v34, v94, v34, v102
	v_mul_f32_e32 v34, 0xbfb8aa3b, v34
	v_exp_f32_e32 v34, v34
	v_mul_f32_e32 v38, v38, v52
	v_mul_f32_e32 v46, v46, v52
	v_fma_f32 v38, v106, v38, v110
	v_fma_f32 v46, v82, v46, v90
	v_mul_f32_e32 v38, 0xbfb8aa3b, v38
	v_mul_f32_e32 v46, 0xbfb8aa3b, v46
	v_exp_f32_e32 v38, v38
	v_exp_f32_e32 v46, v46
	v_add_f32_e32 v34, 1.0, v34
	v_mul_f32_e32 v42, v42, v52
	v_rcp_f32_e32 v34, v34
	v_fma_f32 v42, v86, v42, v98
	v_mul_f32_e32 v42, 0xbfb8aa3b, v42
	v_exp_f32_e32 v42, v42
	v_add_f32_e32 v38, 1.0, v38
	v_add_f32_e32 v46, 1.0, v46
	v_rcp_f32_e32 v38, v38
	v_rcp_f32_e32 v54, v46
	v_mul_f32_e32 v46, v46, v34
	v_mul_f32_e32 v34, v39, v52
	v_mul_f32_e32 v35, v35, v52
	v_fma_f32 v34, v107, v34, v111
	v_fma_f32 v35, v95, v35, v103
	v_mul_f32_e32 v34, 0xbfb8aa3b, v34
	v_mul_f32_e32 v35, 0xbfb8aa3b, v35
	v_add_f32_e32 v42, 1.0, v42
	v_exp_f32_e32 v34, v34
	v_exp_f32_e32 v35, v35
	v_rcp_f32_e32 v53, v42
	v_mul_f32_e32 v42, v42, v38
	v_mul_f32_e32 v38, v43, v52
	v_mul_f32_e32 v39, v47, v52
	v_fma_f32 v38, v87, v38, v99
	v_fma_f32 v39, v83, v39, v91
	v_mul_f32_e32 v38, 0xbfb8aa3b, v38
	v_mul_f32_e32 v39, 0xbfb8aa3b, v39
	v_exp_f32_e32 v38, v38
	v_exp_f32_e32 v39, v39
	v_add_f32_e32 v34, 1.0, v34
	v_add_f32_e32 v35, 1.0, v35
	v_rcp_f32_e32 v34, v34
	v_rcp_f32_e32 v35, v35
	v_add_f32_e32 v38, 1.0, v38
	v_add_f32_e32 v39, 1.0, v39
	v_mul_f32_e32 v55, v38, v34
	v_mul_f32_e32 v56, v39, v35
	v_mul_f32_e32 v34, v40, v52
	v_mul_f32_e32 v35, v36, v52
	v_fma_f32 v34, v108, v34, v112
	v_fma_f32 v35, v96, v35, v104
	v_mul_f32_e32 v34, 0xbfb8aa3b, v34
	v_mul_f32_e32 v35, 0xbfb8aa3b, v35
	v_exp_f32_e32 v34, v34
	v_exp_f32_e32 v35, v35
	v_rcp_f32_e32 v43, v38
	v_mul_f32_e32 v36, v44, v52
	v_mul_f32_e32 v38, v48, v52
	v_fma_f32 v36, v88, v36, v100
	v_fma_f32 v38, v84, v38, v92
	v_mul_f32_e32 v36, 0xbfb8aa3b, v36
	v_mul_f32_e32 v38, 0xbfb8aa3b, v38
	v_exp_f32_e32 v36, v36
	v_exp_f32_e32 v38, v38
	v_add_f32_e32 v34, 1.0, v34
	v_add_f32_e32 v35, 1.0, v35
	v_rcp_f32_e32 v34, v34
	v_rcp_f32_e32 v35, v35
	v_add_f32_e32 v36, 1.0, v36
	v_add_f32_e32 v38, 1.0, v38
	v_mul_f32_e32 v44, v36, v34
	v_mul_f32_e32 v48, v38, v35
	v_mul_f32_e32 v34, v41, v52
	v_mul_f32_e32 v35, v37, v52
	v_fma_f32 v34, v109, v34, v113
	v_fma_f32 v35, v97, v35, v105
	v_mul_f32_e32 v34, 0xbfb8aa3b, v34
	v_mul_f32_e32 v35, 0xbfb8aa3b, v35
	v_rcp_f32_e32 v47, v39
	v_rcp_f32_e32 v39, v36
	v_exp_f32_e32 v34, v34
	v_exp_f32_e32 v35, v35
	v_mul_f32_e32 v36, v45, v52
	v_fma_f32 v36, v89, v36, v101
	v_mul_f32_e32 v37, v49, v52
	v_mul_f32_e32 v36, 0xbfb8aa3b, v36
	v_fma_f32 v37, v85, v37, v93
	v_exp_f32_e32 v36, v36
	v_mul_f32_e32 v37, 0xbfb8aa3b, v37
	v_exp_f32_e32 v37, v37
	v_add_f32_e32 v34, 1.0, v34
	v_add_f32_e32 v35, 1.0, v35
	v_rcp_f32_e32 v34, v34
	v_rcp_f32_e32 v35, v35
	v_add_f32_e32 v36, 1.0, v36
	v_rcp_f32_e32 v40, v38
	v_add_f32_e32 v37, 1.0, v37
	v_rcp_f32_e32 v38, v36
	v_rcp_f32_e32 v41, v37
	v_mul_f32_e32 v45, v36, v34
	v_mul_f32_e32 v49, v37, v35
	v_cvt_pk_bf16_f32 v34, v53, v43
	v_cvt_pk_bf16_f32 v35, v39, v38
	v_lshlrev_b64 v[38:39], 12, v[50:51]
	v_cvt_pk_bf16_f32 v36, v54, v47
	v_cvt_pk_bf16_f32 v37, v40, v41
	v_lshl_add_u64 v[40:41], s[16:17], 0, v[38:39]
	v_lshl_add_u64 v[40:41], v[40:41], 0, v[146:147]
	v_lshl_add_u64 v[38:39], s[10:11], 0, v[38:39]
	global_store_dwordx4 v[40:41], v[34:37], off sc0 sc1
	v_lshl_add_u64 v[38:39], v[38:39], 0, v[146:147]
	s_nop 0
	v_cvt_pk_bf16_f32 v34, v42, v55
	v_cvt_pk_bf16_f32 v35, v44, v45
	v_cvt_pk_bf16_f32 v36, v46, v56
	v_cvt_pk_bf16_f32 v37, v48, v49
	global_store_dwordx4 v[38:39], v[34:37], off sc0 sc1
	s_nop 1
	v_add_u32_e32 v34, 0xa0, v182
	v_ashrrev_i32_e32 v35, 31, v34
	v_lshl_add_u64 v[36:37], v[34:35], 2, s[12:13]
	v_mov_b32_e32 v36, v203
	v_mul_f32_e32 v18, v18, v36
	v_fma_f32 v18, v94, v18, v102
	v_mul_f32_e32 v18, 0xbfb8aa3b, v18
	v_exp_f32_e32 v18, v18
	v_mul_f32_e32 v22, v22, v36
	v_mul_f32_e32 v30, v30, v36
	v_fma_f32 v22, v106, v22, v110
	v_fma_f32 v30, v82, v30, v90
	v_mul_f32_e32 v22, 0xbfb8aa3b, v22
	v_mul_f32_e32 v30, 0xbfb8aa3b, v30
	v_exp_f32_e32 v22, v22
	v_exp_f32_e32 v30, v30
	v_add_f32_e32 v18, 1.0, v18
	v_mul_f32_e32 v26, v26, v36
	v_rcp_f32_e32 v18, v18
	v_fma_f32 v26, v86, v26, v98
	v_mul_f32_e32 v26, 0xbfb8aa3b, v26
	v_exp_f32_e32 v26, v26
	v_add_f32_e32 v22, 1.0, v22
	v_add_f32_e32 v30, 1.0, v30
	v_rcp_f32_e32 v22, v22
	v_rcp_f32_e32 v38, v30
	v_mul_f32_e32 v30, v30, v18
	v_mul_f32_e32 v18, v23, v36
	v_mul_f32_e32 v19, v19, v36
	v_fma_f32 v18, v107, v18, v111
	v_fma_f32 v19, v95, v19, v103
	v_mul_f32_e32 v18, 0xbfb8aa3b, v18
	v_mul_f32_e32 v19, 0xbfb8aa3b, v19
	v_add_f32_e32 v26, 1.0, v26
	v_exp_f32_e32 v18, v18
	v_exp_f32_e32 v19, v19
	v_rcp_f32_e32 v37, v26
	v_mul_f32_e32 v26, v26, v22
	v_mul_f32_e32 v22, v27, v36
	v_mul_f32_e32 v23, v31, v36
	v_fma_f32 v22, v87, v22, v99
	v_fma_f32 v23, v83, v23, v91
	v_mul_f32_e32 v22, 0xbfb8aa3b, v22
	v_mul_f32_e32 v23, 0xbfb8aa3b, v23
	v_exp_f32_e32 v22, v22
	v_exp_f32_e32 v23, v23
	v_add_f32_e32 v18, 1.0, v18
	v_add_f32_e32 v19, 1.0, v19
	v_rcp_f32_e32 v18, v18
	v_rcp_f32_e32 v19, v19
	v_add_f32_e32 v22, 1.0, v22
	v_add_f32_e32 v23, 1.0, v23
	v_mul_f32_e32 v39, v22, v18
	v_mul_f32_e32 v40, v23, v19
	v_mul_f32_e32 v18, v24, v36
	v_mul_f32_e32 v19, v20, v36
	v_fma_f32 v18, v108, v18, v112
	v_fma_f32 v19, v96, v19, v104
	v_mul_f32_e32 v18, 0xbfb8aa3b, v18
	v_mul_f32_e32 v19, 0xbfb8aa3b, v19
	v_exp_f32_e32 v18, v18
	v_exp_f32_e32 v19, v19
	v_rcp_f32_e32 v27, v22
	v_mul_f32_e32 v20, v28, v36
	v_mul_f32_e32 v22, v32, v36
	v_fma_f32 v20, v88, v20, v100
	v_fma_f32 v22, v84, v22, v92
	v_mul_f32_e32 v20, 0xbfb8aa3b, v20
	v_mul_f32_e32 v22, 0xbfb8aa3b, v22
	v_exp_f32_e32 v20, v20
	v_exp_f32_e32 v22, v22
	v_add_f32_e32 v18, 1.0, v18
	v_add_f32_e32 v19, 1.0, v19
	v_rcp_f32_e32 v18, v18
	v_rcp_f32_e32 v19, v19
	v_add_f32_e32 v20, 1.0, v20
	v_add_f32_e32 v22, 1.0, v22
	v_mul_f32_e32 v28, v20, v18
	v_mul_f32_e32 v32, v22, v19
	v_mul_f32_e32 v18, v25, v36
	v_mul_f32_e32 v19, v21, v36
	v_fma_f32 v18, v109, v18, v113
	v_fma_f32 v19, v97, v19, v105
	v_mul_f32_e32 v18, 0xbfb8aa3b, v18
	v_mul_f32_e32 v19, 0xbfb8aa3b, v19
	v_rcp_f32_e32 v31, v23
	v_rcp_f32_e32 v23, v20
	v_exp_f32_e32 v18, v18
	v_exp_f32_e32 v19, v19
	v_mul_f32_e32 v20, v29, v36
	v_fma_f32 v20, v89, v20, v101
	v_mul_f32_e32 v21, v33, v36
	v_mul_f32_e32 v20, 0xbfb8aa3b, v20
	v_fma_f32 v21, v85, v21, v93
	v_exp_f32_e32 v20, v20
	v_mul_f32_e32 v21, 0xbfb8aa3b, v21
	v_exp_f32_e32 v21, v21
	v_add_f32_e32 v18, 1.0, v18
	v_add_f32_e32 v19, 1.0, v19
	v_rcp_f32_e32 v18, v18
	v_rcp_f32_e32 v19, v19
	v_add_f32_e32 v20, 1.0, v20
	v_rcp_f32_e32 v24, v22
	v_add_f32_e32 v21, 1.0, v21
	v_rcp_f32_e32 v22, v20
	v_rcp_f32_e32 v25, v21
	v_mul_f32_e32 v29, v20, v18
	v_mul_f32_e32 v33, v21, v19
	v_cvt_pk_bf16_f32 v18, v37, v27
	v_cvt_pk_bf16_f32 v19, v23, v22
	v_lshlrev_b64 v[22:23], 12, v[34:35]
	v_cvt_pk_bf16_f32 v20, v38, v31
	v_cvt_pk_bf16_f32 v21, v24, v25
	v_lshl_add_u64 v[24:25], s[16:17], 0, v[22:23]
	v_lshl_add_u64 v[24:25], v[24:25], 0, v[146:147]
	v_lshl_add_u64 v[22:23], s[10:11], 0, v[22:23]
	global_store_dwordx4 v[24:25], v[18:21], off sc0 sc1
	v_lshl_add_u64 v[22:23], v[22:23], 0, v[146:147]
	s_nop 0
	v_cvt_pk_bf16_f32 v18, v26, v39
	v_cvt_pk_bf16_f32 v19, v28, v29
	v_cvt_pk_bf16_f32 v20, v30, v40
	v_cvt_pk_bf16_f32 v21, v32, v33
	global_store_dwordx4 v[22:23], v[18:21], off sc0 sc1
	s_nop 1
	v_add_u32_e32 v18, 0xb0, v182
	v_ashrrev_i32_e32 v19, 31, v18
	v_lshl_add_u64 v[20:21], v[18:19], 2, s[12:13]
	v_mov_b32_e32 v20, v204
	v_mul_f32_e32 v2, v2, v20
	v_fma_f32 v2, v94, v2, v102
	v_mul_f32_e32 v2, 0xbfb8aa3b, v2
	v_exp_f32_e32 v2, v2
	v_mul_f32_e32 v6, v6, v20
	v_mul_f32_e32 v14, v14, v20
	v_fma_f32 v6, v106, v6, v110
	v_fma_f32 v14, v82, v14, v90
	v_mul_f32_e32 v6, 0xbfb8aa3b, v6
	v_mul_f32_e32 v14, 0xbfb8aa3b, v14
	v_exp_f32_e32 v6, v6
	v_exp_f32_e32 v14, v14
	v_add_f32_e32 v2, 1.0, v2
	v_mul_f32_e32 v10, v10, v20
	v_rcp_f32_e32 v2, v2
	v_fma_f32 v10, v86, v10, v98
	v_mul_f32_e32 v10, 0xbfb8aa3b, v10
	v_exp_f32_e32 v10, v10
	v_add_f32_e32 v6, 1.0, v6
	v_add_f32_e32 v14, 1.0, v14
	v_rcp_f32_e32 v6, v6
	v_rcp_f32_e32 v22, v14
	v_mul_f32_e32 v14, v14, v2
	v_mul_f32_e32 v2, v7, v20
	v_mul_f32_e32 v3, v3, v20
	v_fma_f32 v2, v107, v2, v111
	v_fma_f32 v3, v95, v3, v103
	v_mul_f32_e32 v2, 0xbfb8aa3b, v2
	v_mul_f32_e32 v3, 0xbfb8aa3b, v3
	v_add_f32_e32 v10, 1.0, v10
	v_exp_f32_e32 v2, v2
	v_exp_f32_e32 v3, v3
	v_rcp_f32_e32 v21, v10
	v_mul_f32_e32 v10, v10, v6
	v_mul_f32_e32 v6, v11, v20
	v_mul_f32_e32 v7, v15, v20
	v_fma_f32 v6, v87, v6, v99
	v_fma_f32 v7, v83, v7, v91
	v_mul_f32_e32 v6, 0xbfb8aa3b, v6
	v_mul_f32_e32 v7, 0xbfb8aa3b, v7
	v_exp_f32_e32 v6, v6
	v_exp_f32_e32 v7, v7
	v_add_f32_e32 v2, 1.0, v2
	v_add_f32_e32 v3, 1.0, v3
	v_rcp_f32_e32 v2, v2
	v_rcp_f32_e32 v3, v3
	v_add_f32_e32 v6, 1.0, v6
	v_add_f32_e32 v7, 1.0, v7
	v_mul_f32_e32 v23, v6, v2
	v_mul_f32_e32 v24, v7, v3
	v_mul_f32_e32 v2, v8, v20
	v_mul_f32_e32 v3, v4, v20
	v_fma_f32 v2, v108, v2, v112
	v_fma_f32 v3, v96, v3, v104
	v_mul_f32_e32 v2, 0xbfb8aa3b, v2
	v_mul_f32_e32 v3, 0xbfb8aa3b, v3
	v_exp_f32_e32 v2, v2
	v_exp_f32_e32 v3, v3
	v_rcp_f32_e32 v11, v6
	v_mul_f32_e32 v4, v12, v20
	v_mul_f32_e32 v6, v16, v20
	v_fma_f32 v4, v88, v4, v100
	v_fma_f32 v6, v84, v6, v92
	v_mul_f32_e32 v4, 0xbfb8aa3b, v4
	v_mul_f32_e32 v6, 0xbfb8aa3b, v6
	v_exp_f32_e32 v4, v4
	v_exp_f32_e32 v6, v6
	v_add_f32_e32 v2, 1.0, v2
	v_add_f32_e32 v3, 1.0, v3
	v_rcp_f32_e32 v2, v2
	v_rcp_f32_e32 v3, v3
	v_add_f32_e32 v4, 1.0, v4
	v_add_f32_e32 v6, 1.0, v6
	v_mul_f32_e32 v12, v4, v2
	v_mul_f32_e32 v16, v6, v3
	v_mul_f32_e32 v2, v9, v20
	v_mul_f32_e32 v3, v5, v20
	v_fmac_f32_e32 v113, v109, v2
	v_fmac_f32_e32 v105, v97, v3
	v_mul_f32_e32 v2, 0xbfb8aa3b, v113
	v_mul_f32_e32 v3, 0xbfb8aa3b, v105
	v_rcp_f32_e32 v15, v7
	v_rcp_f32_e32 v7, v4
	v_exp_f32_e32 v2, v2
	v_exp_f32_e32 v3, v3
	v_mul_f32_e32 v4, v13, v20
	v_fmac_f32_e32 v101, v89, v4
	v_mul_f32_e32 v5, v17, v20
	v_mul_f32_e32 v4, 0xbfb8aa3b, v101
	v_fmac_f32_e32 v93, v85, v5
	v_exp_f32_e32 v4, v4
	v_mul_f32_e32 v5, 0xbfb8aa3b, v93
	v_exp_f32_e32 v5, v5
	v_add_f32_e32 v2, 1.0, v2
	v_add_f32_e32 v3, 1.0, v3
	v_rcp_f32_e32 v2, v2
	v_rcp_f32_e32 v3, v3
	v_add_f32_e32 v4, 1.0, v4
	v_rcp_f32_e32 v8, v6
	v_add_f32_e32 v5, 1.0, v5
	v_rcp_f32_e32 v6, v4
	v_rcp_f32_e32 v9, v5
	v_mul_f32_e32 v13, v4, v2
	v_mul_f32_e32 v17, v5, v3
	v_cvt_pk_bf16_f32 v2, v21, v11
	v_cvt_pk_bf16_f32 v3, v7, v6
	v_lshlrev_b64 v[6:7], 12, v[18:19]
	v_cvt_pk_bf16_f32 v4, v22, v15
	v_cvt_pk_bf16_f32 v5, v8, v9
	v_lshl_add_u64 v[8:9], s[16:17], 0, v[6:7]
	v_lshl_add_u64 v[6:7], s[10:11], 0, v[6:7]
	v_lshl_add_u64 v[8:9], v[8:9], 0, v[146:147]
	v_lshl_add_u64 v[6:7], v[6:7], 0, v[146:147]
	global_store_dwordx4 v[8:9], v[2:5], off sc0 sc1
	s_nop 1
	v_cvt_pk_bf16_f32 v2, v10, v23
	v_cvt_pk_bf16_f32 v3, v12, v13
	v_cvt_pk_bf16_f32 v4, v14, v24
	v_cvt_pk_bf16_f32 v5, v16, v17
	global_store_dwordx4 v[6:7], v[2:5], off sc0 sc1
	s_cbranch_vccnz .LBB0_872
	s_andn2_b64 vcc, exec, s[8:9]
	s_cbranch_vccnz .LBB0_871
	s_barrier
	s_branch .LBB0_871

.LBB0_966:
	v_mov_b32_e32 v3, 0
	v_mov_b32_e32 v132, 0
	s_or_b32 s2, s52, s67
	v_add_u32_e32 v199, v132, v1
	v_add3_u32 v178, s31, v194, v3
	v_lshlrev_b32_e32 v176, 3, v199
	s_add_u32 s42, s74, s54
	v_ashrrev_i32_e32 v177, 31, v176
	s_addc_u32 s43, s75, s55
	v_ashrrev_i32_e32 v179, 31, v178
	v_lshl_add_u64 v[180:181], v[176:177], 1, s[42:43]
	v_lshlrev_b64 v[208:209], 12, v[178:179]
	v_lshl_add_u64 v[132:133], v[180:181], 0, v[208:209]
	global_load_dwordx4 v[200:203], v[132:133], off
	global_load_dwordx4 v[204:207], v[132:133], off offset:256
	v_add_u32_e32 v190, 16, v178
	v_add_u32_e32 v186, 32, v178
	v_add_u32_e32 v182, 48, v178
	v_ashrrev_i32_e32 v191, 31, v190
	v_ashrrev_i32_e32 v187, 31, v186
	v_ashrrev_i32_e32 v183, 31, v182
	v_lshlrev_b64 v[192:193], 12, v[190:191]
	v_lshlrev_b64 v[188:189], 12, v[186:187]
	v_lshlrev_b64 v[184:185], 12, v[182:183]
	v_lshl_add_u64 v[132:133], v[180:181], 0, v[192:193]
	v_lshl_add_u64 v[134:135], v[180:181], 0, v[188:189]
	v_lshl_add_u64 v[210:211], v[180:181], 0, v[184:185]
	global_load_dwordx4 v[152:155], v[132:133], off
	global_load_dwordx4 v[148:151], v[132:133], off offset:256
	global_load_dwordx4 v[144:147], v[134:135], off
	global_load_dwordx4 v[140:143], v[134:135], off offset:256
	global_load_dwordx4 v[136:139], v[210:211], off
	s_nop 0
	global_load_dwordx4 v[132:135], v[210:211], off offset:256
	v_add_u32_e32 v176, s2, v176
	v_lshl_add_u64 v[208:209], s[14:15], 0, v[208:209]
	v_ashrrev_i32_e32 v177, 31, v176
	v_cmp_eq_u32_e32 vcc, 0, v199
	s_waitcnt vmcnt(0)
	v_lshlrev_b32_e32 v210, 16, v200
	v_and_b32_e32 v211, 0xffff0000, v200
	v_lshlrev_b32_e32 v212, 16, v202
	v_and_b32_e32 v213, 0xffff0000, v202
	v_lshlrev_b32_e32 v200, 16, v201
	v_and_b32_e32 v201, 0xffff0000, v201
	v_lshlrev_b32_e32 v202, 16, v203
	v_and_b32_e32 v203, 0xffff0000, v203
	v_lshlrev_b32_e32 v216, 16, v206
	v_and_b32_e32 v217, 0xffff0000, v206
	v_lshlrev_b32_e32 v206, 16, v207
	v_and_b32_e32 v207, 0xffff0000, v207
	v_pk_mul_f32 v[128:129], v[128:129], v[210:211]
	v_pk_mul_f32 v[124:125], v[124:125], v[212:213]
	v_lshlrev_b32_e32 v214, 16, v204
	v_and_b32_e32 v215, 0xffff0000, v204
	v_pk_mul_f32 v[130:131], v[130:131], v[200:201]
	v_pk_mul_f32 v[126:127], v[126:127], v[202:203]
	v_pk_mul_f32 v[200:201], v[118:119], v[206:207]
	v_pk_mul_f32 v[202:203], v[116:117], v[216:217]
	v_cvt_pk_bf16_f32 v116, v128, v129
	v_cvt_pk_bf16_f32 v117, v130, v131
	v_cvt_pk_bf16_f32 v118, v124, v125
	v_max_f32_e64 v3, |v128|, |v124|
	v_max_f32_e64 v124, |v129|, |v125|
	v_lshlrev_b32_e32 v204, 16, v205
	v_and_b32_e32 v205, 0xffff0000, v205
	v_pk_mul_f32 v[120:121], v[120:121], v[214:215]
	v_cvt_pk_bf16_f32 v119, v126, v127
	v_max_f32_e64 v125, |v130|, |v126|
	v_max_f32_e64 v126, |v131|, |v127|
	v_max3_f32 v3, v3, 0, v124
	v_pk_mul_f32 v[122:123], v[122:123], v[204:205]
	v_max_f32_e64 v127, |v120|, |v202|
	v_max_f32_e64 v128, |v121|, |v203|
	v_max3_f32 v3, v3, v125, v126
	v_max_f32_e64 v129, |v122|, |v200|
	v_max3_f32 v3, v3, v127, v128
	v_max_f32_e64 v124, |v123|, |v201|
	v_max3_f32 v3, v3, v129, v124
	ds_bpermute_b32 v126, v196, v3
	v_lshl_add_u64 v[124:125], v[176:177], 1, v[208:209]
	global_store_dwordx4 v[124:125], v[116:119], off sc0 sc1
	s_waitcnt lgkmcnt(0)
	s_nop 0
	v_max_f32_e32 v116, v126, v126
	v_max_f32_e32 v3, v3, v116
	ds_bpermute_b32 v116, v197, v3
	v_cvt_pk_bf16_f32 v118, v120, v121
	v_cvt_pk_bf16_f32 v119, v122, v123
	v_cvt_pk_bf16_f32 v120, v202, v203
	v_cvt_pk_bf16_f32 v121, v200, v201
	global_store_dwordx4 v[124:125], v[118:121], off offset:256 sc0 sc1
	s_and_saveexec_b64 s[48:49], vcc
	s_cbranch_execz .LBB0_968
	s_waitcnt lgkmcnt(0)
	v_max_f32_e32 v116, v116, v116
	v_max_f32_e32 v3, v3, v3
	v_lshl_add_u64 v[118:119], v[178:179], 2, s[10:11]
	v_max_f32_e32 v3, v3, v116
	global_atomic_umax v[118:119], v3, off
.LBB0_968:
	s_or_b64 exec, exec, s[48:49]
	s_waitcnt lgkmcnt(0)
	v_lshlrev_b32_e32 v116, 16, v152
	v_and_b32_e32 v117, 0xffff0000, v152
	v_lshlrev_b32_e32 v118, 16, v153
	v_and_b32_e32 v119, 0xffff0000, v153
	v_lshlrev_b32_e32 v120, 16, v154
	v_and_b32_e32 v121, 0xffff0000, v154
	v_lshlrev_b32_e32 v122, 16, v155
	v_and_b32_e32 v123, 0xffff0000, v155
	v_pk_mul_f32 v[114:115], v[114:115], v[118:119]
	v_pk_mul_f32 v[112:113], v[112:113], v[116:117]
	v_pk_mul_f32 v[118:119], v[108:109], v[120:121]
	v_pk_mul_f32 v[116:117], v[110:111], v[122:123]
	v_cvt_pk_bf16_f32 v108, v112, v113
	v_max_f32_e64 v3, |v112|, |v118|
	v_max_f32_e64 v112, |v113|, |v119|
	v_max3_f32 v3, v3, 0, v112
	v_max_f32_e64 v112, |v114|, |v116|
	v_max_f32_e64 v113, |v115|, |v117|
	v_cvt_pk_bf16_f32 v109, v114, v115
	v_cvt_pk_bf16_f32 v110, v118, v119
	v_cvt_pk_bf16_f32 v111, v116, v117
	v_max3_f32 v3, v3, v112, v113
	v_lshlrev_b32_e32 v112, 16, v148
	v_and_b32_e32 v113, 0xffff0000, v148
	v_lshlrev_b32_e32 v114, 16, v149
	v_and_b32_e32 v115, 0xffff0000, v149
	v_lshlrev_b32_e32 v116, 16, v150
	v_and_b32_e32 v117, 0xffff0000, v150
	v_lshlrev_b32_e32 v118, 16, v151
	v_and_b32_e32 v119, 0xffff0000, v151
	v_pk_mul_f32 v[106:107], v[106:107], v[114:115]
	v_pk_mul_f32 v[104:105], v[104:105], v[112:113]
	v_pk_mul_f32 v[114:115], v[100:101], v[116:117]
	v_pk_mul_f32 v[112:113], v[102:103], v[118:119]
	v_max_f32_e64 v100, |v104|, |v114|
	v_max_f32_e64 v101, |v105|, |v115|
	v_max3_f32 v3, v3, v100, v101
	v_max_f32_e64 v100, |v106|, |v112|
	v_max_f32_e64 v101, |v107|, |v113|
	v_max3_f32 v3, v3, v100, v101
	ds_bpermute_b32 v103, v196, v3
	v_lshl_add_u64 v[100:101], s[14:15], 0, v[192:193]
	v_lshl_add_u64 v[116:117], v[176:177], 1, v[100:101]
	global_store_dwordx4 v[116:117], v[108:111], off sc0 sc1
	v_cvt_pk_bf16_f32 v102, v104, v105
	s_waitcnt lgkmcnt(0)
	v_max_f32_e32 v100, v103, v103
	v_max_f32_e32 v3, v3, v100
	ds_bpermute_b32 v100, v197, v3
	v_cvt_pk_bf16_f32 v103, v106, v107
	v_cvt_pk_bf16_f32 v104, v114, v115
	v_cvt_pk_bf16_f32 v105, v112, v113
	global_store_dwordx4 v[116:117], v[102:105], off offset:256 sc0 sc1
	s_and_saveexec_b64 s[48:49], vcc
	s_cbranch_execz .LBB0_970
	s_waitcnt lgkmcnt(0)
	v_max_f32_e32 v100, v100, v100
	v_max_f32_e32 v3, v3, v3
	v_lshl_add_u64 v[102:103], v[190:191], 2, s[10:11]
	v_max_f32_e32 v3, v3, v100
	global_atomic_umax v[102:103], v3, off
.LBB0_970:
	s_or_b64 exec, exec, s[48:49]
	s_waitcnt lgkmcnt(0)
	v_lshlrev_b32_e32 v100, 16, v144
	v_and_b32_e32 v101, 0xffff0000, v144
	v_lshlrev_b32_e32 v102, 16, v145
	v_and_b32_e32 v103, 0xffff0000, v145
	v_lshlrev_b32_e32 v104, 16, v146
	v_and_b32_e32 v105, 0xffff0000, v146
	v_lshlrev_b32_e32 v106, 16, v147
	v_and_b32_e32 v107, 0xffff0000, v147
	v_pk_mul_f32 v[98:99], v[98:99], v[102:103]
	v_pk_mul_f32 v[96:97], v[96:97], v[100:101]
	v_pk_mul_f32 v[102:103], v[92:93], v[104:105]
	v_pk_mul_f32 v[100:101], v[94:95], v[106:107]
	v_cvt_pk_bf16_f32 v92, v96, v97
	v_max_f32_e64 v3, |v96|, |v102|
	v_max_f32_e64 v96, |v97|, |v103|
	v_max3_f32 v3, v3, 0, v96
	v_max_f32_e64 v96, |v98|, |v100|
	v_max_f32_e64 v97, |v99|, |v101|
	v_cvt_pk_bf16_f32 v93, v98, v99
	v_cvt_pk_bf16_f32 v94, v102, v103
	v_cvt_pk_bf16_f32 v95, v100, v101
	v_max3_f32 v3, v3, v96, v97
	v_lshlrev_b32_e32 v96, 16, v140
	v_and_b32_e32 v97, 0xffff0000, v140
	v_lshlrev_b32_e32 v98, 16, v141
	v_and_b32_e32 v99, 0xffff0000, v141
	v_lshlrev_b32_e32 v100, 16, v142
	v_and_b32_e32 v101, 0xffff0000, v142
	v_lshlrev_b32_e32 v102, 16, v143
	v_and_b32_e32 v103, 0xffff0000, v143
	v_pk_mul_f32 v[90:91], v[90:91], v[98:99]
	v_pk_mul_f32 v[88:89], v[88:89], v[96:97]
	v_pk_mul_f32 v[98:99], v[84:85], v[100:101]
	v_pk_mul_f32 v[96:97], v[86:87], v[102:103]
	v_max_f32_e64 v84, |v88|, |v98|
	v_max_f32_e64 v85, |v89|, |v99|
	v_max3_f32 v3, v3, v84, v85
	v_max_f32_e64 v84, |v90|, |v96|
	v_max_f32_e64 v85, |v91|, |v97|
	v_max3_f32 v3, v3, v84, v85
	ds_bpermute_b32 v87, v196, v3
	v_lshl_add_u64 v[84:85], s[14:15], 0, v[188:189]
	v_lshl_add_u64 v[100:101], v[176:177], 1, v[84:85]
	global_store_dwordx4 v[100:101], v[92:95], off sc0 sc1
	v_cvt_pk_bf16_f32 v86, v88, v89
	s_waitcnt lgkmcnt(0)
	v_max_f32_e32 v84, v87, v87
	v_max_f32_e32 v3, v3, v84
	ds_bpermute_b32 v84, v197, v3
	v_cvt_pk_bf16_f32 v87, v90, v91
	v_cvt_pk_bf16_f32 v88, v98, v99
	v_cvt_pk_bf16_f32 v89, v96, v97
	global_store_dwordx4 v[100:101], v[86:89], off offset:256 sc0 sc1
	s_and_saveexec_b64 s[48:49], vcc
	s_cbranch_execz .LBB0_972
	s_waitcnt lgkmcnt(0)
	v_max_f32_e32 v84, v84, v84
	v_max_f32_e32 v3, v3, v3
	v_lshl_add_u64 v[86:87], v[186:187], 2, s[10:11]
	v_max_f32_e32 v3, v3, v84
	global_atomic_umax v[86:87], v3, off
.LBB0_972:
	s_or_b64 exec, exec, s[48:49]
	s_waitcnt lgkmcnt(0)
	v_lshlrev_b32_e32 v84, 16, v136
	v_and_b32_e32 v85, 0xffff0000, v136
	v_lshlrev_b32_e32 v86, 16, v137
	v_and_b32_e32 v87, 0xffff0000, v137
	v_lshlrev_b32_e32 v88, 16, v138
	v_and_b32_e32 v89, 0xffff0000, v138
	v_lshlrev_b32_e32 v90, 16, v139
	v_and_b32_e32 v91, 0xffff0000, v139
	v_pk_mul_f32 v[82:83], v[82:83], v[86:87]
	v_pk_mul_f32 v[80:81], v[80:81], v[84:85]
	v_pk_mul_f32 v[86:87], v[76:77], v[88:89]
	v_pk_mul_f32 v[84:85], v[78:79], v[90:91]
	v_cvt_pk_bf16_f32 v76, v80, v81
	v_max_f32_e64 v3, |v80|, |v86|
	v_max_f32_e64 v80, |v81|, |v87|
	v_max3_f32 v3, v3, 0, v80
	v_max_f32_e64 v80, |v82|, |v84|
	v_max_f32_e64 v81, |v83|, |v85|
	v_cvt_pk_bf16_f32 v77, v82, v83
	v_cvt_pk_bf16_f32 v78, v86, v87
	v_cvt_pk_bf16_f32 v79, v84, v85
	v_max3_f32 v3, v3, v80, v81
	v_lshlrev_b32_e32 v80, 16, v132
	v_and_b32_e32 v81, 0xffff0000, v132
	v_lshlrev_b32_e32 v82, 16, v133
	v_and_b32_e32 v83, 0xffff0000, v133
	v_lshlrev_b32_e32 v84, 16, v134
	v_and_b32_e32 v85, 0xffff0000, v134
	v_lshlrev_b32_e32 v86, 16, v135
	v_and_b32_e32 v87, 0xffff0000, v135
	v_pk_mul_f32 v[74:75], v[74:75], v[82:83]
	v_pk_mul_f32 v[72:73], v[72:73], v[80:81]
	v_pk_mul_f32 v[82:83], v[68:69], v[84:85]
	v_pk_mul_f32 v[80:81], v[70:71], v[86:87]
	v_max_f32_e64 v68, |v72|, |v82|
	v_max_f32_e64 v69, |v73|, |v83|
	v_max3_f32 v3, v3, v68, v69
	v_max_f32_e64 v68, |v74|, |v80|
	v_max_f32_e64 v69, |v75|, |v81|
	v_max3_f32 v3, v3, v68, v69
	ds_bpermute_b32 v71, v196, v3
	v_lshl_add_u64 v[68:69], s[14:15], 0, v[184:185]
	v_lshl_add_u64 v[84:85], v[176:177], 1, v[68:69]
	global_store_dwordx4 v[84:85], v[76:79], off sc0 sc1
	v_cvt_pk_bf16_f32 v70, v72, v73
	s_waitcnt lgkmcnt(0)
	v_max_f32_e32 v68, v71, v71
	v_max_f32_e32 v3, v3, v68
	ds_bpermute_b32 v68, v197, v3
	v_cvt_pk_bf16_f32 v71, v74, v75
	v_cvt_pk_bf16_f32 v72, v82, v83
	v_cvt_pk_bf16_f32 v73, v80, v81
	global_store_dwordx4 v[84:85], v[70:73], off offset:256 sc0 sc1
	s_and_saveexec_b64 s[48:49], vcc
	s_cbranch_execz .LBB0_974
	s_waitcnt lgkmcnt(0)
	v_max_f32_e32 v68, v68, v68
	v_max_f32_e32 v3, v3, v3
	v_lshl_add_u64 v[70:71], v[182:183], 2, s[10:11]
	v_max_f32_e32 v3, v3, v68
	global_atomic_umax v[70:71], v3, off
.LBB0_974:
	s_or_b64 exec, exec, s[48:49]
	v_add_u32_e32 v104, 0x80, v178
	v_ashrrev_i32_e32 v105, 31, v104
	v_lshlrev_b64 v[114:115], 12, v[104:105]
	s_waitcnt lgkmcnt(0)
	v_lshl_add_u64 v[68:69], v[180:181], 0, v[114:115]
	global_load_dwordx4 v[106:109], v[68:69], off
	global_load_dwordx4 v[110:113], v[68:69], off offset:256
	v_add_u32_e32 v100, 0x90, v178
	v_add_u32_e32 v96, 0xa0, v178
	v_add_u32_e32 v92, 0xb0, v178
	v_ashrrev_i32_e32 v101, 31, v100
	v_ashrrev_i32_e32 v97, 31, v96
	v_ashrrev_i32_e32 v93, 31, v92
	v_lshlrev_b64 v[102:103], 12, v[100:101]
	v_lshlrev_b64 v[98:99], 12, v[96:97]
	v_lshlrev_b64 v[94:95], 12, v[92:93]
	v_lshl_add_u64 v[68:69], v[180:181], 0, v[102:103]
	v_lshl_add_u64 v[70:71], v[180:181], 0, v[98:99]
	v_lshl_add_u64 v[116:117], v[180:181], 0, v[94:95]
	global_load_dwordx4 v[88:91], v[68:69], off
	global_load_dwordx4 v[84:87], v[68:69], off offset:256
	global_load_dwordx4 v[80:83], v[70:71], off
	global_load_dwordx4 v[76:79], v[70:71], off offset:256
	global_load_dwordx4 v[72:75], v[116:117], off
	s_nop 0
	global_load_dwordx4 v[68:71], v[116:117], off offset:256
	s_waitcnt vmcnt(7)
	v_lshlrev_b32_e32 v116, 16, v106
	v_and_b32_e32 v117, 0xffff0000, v106
	v_lshlrev_b32_e32 v106, 16, v107
	v_and_b32_e32 v107, 0xffff0000, v107
	v_lshlrev_b32_e32 v118, 16, v108
	v_and_b32_e32 v119, 0xffff0000, v108
	v_lshlrev_b32_e32 v108, 16, v109
	v_and_b32_e32 v109, 0xffff0000, v109
	v_pk_mul_f32 v[58:59], v[58:59], v[106:107]
	v_pk_mul_f32 v[56:57], v[56:57], v[116:117]
	v_pk_mul_f32 v[106:107], v[54:55], v[108:109]
	v_pk_mul_f32 v[108:109], v[52:53], v[118:119]
	s_waitcnt vmcnt(6)
	v_lshlrev_b32_e32 v120, 16, v110
	v_and_b32_e32 v121, 0xffff0000, v110
	v_lshlrev_b32_e32 v122, 16, v112
	v_and_b32_e32 v123, 0xffff0000, v112
	v_cvt_pk_bf16_f32 v52, v56, v57
	v_max_f32_e64 v3, |v56|, |v108|
	v_max_f32_e64 v56, |v57|, |v109|
	v_lshlrev_b32_e32 v110, 16, v111
	v_and_b32_e32 v111, 0xffff0000, v111
	v_lshlrev_b32_e32 v112, 16, v113
	v_and_b32_e32 v113, 0xffff0000, v113
	v_pk_mul_f32 v[64:65], v[64:65], v[120:121]
	v_pk_mul_f32 v[60:61], v[60:61], v[122:123]
	v_cvt_pk_bf16_f32 v53, v58, v59
	v_max_f32_e64 v57, |v58|, |v106|
	v_max_f32_e64 v58, |v59|, |v107|
	v_max3_f32 v3, v3, 0, v56
	v_pk_mul_f32 v[66:67], v[66:67], v[110:111]
	v_pk_mul_f32 v[62:63], v[62:63], v[112:113]
	v_cvt_pk_bf16_f32 v54, v108, v109
	v_cvt_pk_bf16_f32 v55, v106, v107
	v_max_f32_e64 v59, |v64|, |v60|
	v_max_f32_e64 v106, |v65|, |v61|
	v_max3_f32 v3, v3, v57, v58
	v_max_f32_e64 v107, |v66|, |v62|
	v_max3_f32 v3, v3, v59, v106
	v_max_f32_e64 v56, |v67|, |v63|
	v_max3_f32 v3, v3, v107, v56
	ds_bpermute_b32 v106, v196, v3
	v_lshl_add_u64 v[56:57], s[14:15], 0, v[114:115]
	v_lshl_add_u64 v[58:59], v[176:177], 1, v[56:57]
	global_store_dwordx4 v[58:59], v[52:55], off sc0 sc1
	s_waitcnt lgkmcnt(0)
	s_nop 0
	v_max_f32_e32 v52, v106, v106
	v_max_f32_e32 v3, v3, v52
	ds_bpermute_b32 v52, v197, v3
	v_cvt_pk_bf16_f32 v54, v64, v65
	v_cvt_pk_bf16_f32 v55, v66, v67
	v_cvt_pk_bf16_f32 v56, v60, v61
	v_cvt_pk_bf16_f32 v57, v62, v63
	global_store_dwordx4 v[58:59], v[54:57], off offset:256 sc0 sc1
	s_and_saveexec_b64 s[48:49], vcc
	s_cbranch_execz .LBB0_976
	s_waitcnt lgkmcnt(0)
	v_max_f32_e32 v52, v52, v52
	v_max_f32_e32 v3, v3, v3
	v_lshl_add_u64 v[54:55], v[104:105], 2, s[10:11]
	v_max_f32_e32 v3, v3, v52
	global_atomic_umax v[54:55], v3, off
.LBB0_976:
	s_or_b64 exec, exec, s[48:49]
	s_waitcnt vmcnt(7) lgkmcnt(0)
	v_lshlrev_b32_e32 v52, 16, v88
	v_and_b32_e32 v53, 0xffff0000, v88
	v_lshlrev_b32_e32 v54, 16, v89
	v_and_b32_e32 v55, 0xffff0000, v89
	v_lshlrev_b32_e32 v56, 16, v90
	v_and_b32_e32 v57, 0xffff0000, v90
	v_lshlrev_b32_e32 v58, 16, v91
	v_and_b32_e32 v59, 0xffff0000, v91
	v_pk_mul_f32 v[50:51], v[50:51], v[54:55]
	v_pk_mul_f32 v[48:49], v[48:49], v[52:53]
	v_pk_mul_f32 v[54:55], v[44:45], v[56:57]
	v_pk_mul_f32 v[52:53], v[46:47], v[58:59]
	v_cvt_pk_bf16_f32 v44, v48, v49
	v_max_f32_e64 v3, |v48|, |v54|
	v_max_f32_e64 v48, |v49|, |v55|
	v_max3_f32 v3, v3, 0, v48
	v_max_f32_e64 v48, |v50|, |v52|
	v_max_f32_e64 v49, |v51|, |v53|
	v_cvt_pk_bf16_f32 v45, v50, v51
	v_cvt_pk_bf16_f32 v46, v54, v55
	v_cvt_pk_bf16_f32 v47, v52, v53
	v_max3_f32 v3, v3, v48, v49
	s_waitcnt vmcnt(6)
	v_lshlrev_b32_e32 v48, 16, v84
	v_and_b32_e32 v49, 0xffff0000, v84
	v_lshlrev_b32_e32 v50, 16, v85
	v_and_b32_e32 v51, 0xffff0000, v85
	v_lshlrev_b32_e32 v52, 16, v86
	v_and_b32_e32 v53, 0xffff0000, v86
	v_lshlrev_b32_e32 v54, 16, v87
	v_and_b32_e32 v55, 0xffff0000, v87
	v_pk_mul_f32 v[42:43], v[42:43], v[50:51]
	v_pk_mul_f32 v[40:41], v[40:41], v[48:49]
	v_pk_mul_f32 v[50:51], v[36:37], v[52:53]
	v_pk_mul_f32 v[48:49], v[38:39], v[54:55]
	v_max_f32_e64 v36, |v40|, |v50|
	v_max_f32_e64 v37, |v41|, |v51|
	v_max3_f32 v3, v3, v36, v37
	v_max_f32_e64 v36, |v42|, |v48|
	v_max_f32_e64 v37, |v43|, |v49|
	v_max3_f32 v3, v3, v36, v37
	ds_bpermute_b32 v39, v196, v3
	v_lshl_add_u64 v[36:37], s[14:15], 0, v[102:103]
	v_lshl_add_u64 v[52:53], v[176:177], 1, v[36:37]
	global_store_dwordx4 v[52:53], v[44:47], off sc0 sc1
	v_cvt_pk_bf16_f32 v38, v40, v41
	s_waitcnt lgkmcnt(0)
	v_max_f32_e32 v36, v39, v39
	v_max_f32_e32 v3, v3, v36
	ds_bpermute_b32 v36, v197, v3
	v_cvt_pk_bf16_f32 v39, v42, v43
	v_cvt_pk_bf16_f32 v40, v50, v51
	v_cvt_pk_bf16_f32 v41, v48, v49
	global_store_dwordx4 v[52:53], v[38:41], off offset:256 sc0 sc1
	s_and_saveexec_b64 s[48:49], vcc
	s_cbranch_execz .LBB0_978
	s_waitcnt lgkmcnt(0)
	v_max_f32_e32 v36, v36, v36
	v_max_f32_e32 v3, v3, v3
	v_lshl_add_u64 v[38:39], v[100:101], 2, s[10:11]
	v_max_f32_e32 v3, v3, v36
	global_atomic_umax v[38:39], v3, off
.LBB0_978:
	s_or_b64 exec, exec, s[48:49]
	s_waitcnt vmcnt(7) lgkmcnt(0)
	v_lshlrev_b32_e32 v36, 16, v80
	v_and_b32_e32 v37, 0xffff0000, v80
	v_lshlrev_b32_e32 v38, 16, v81
	v_and_b32_e32 v39, 0xffff0000, v81
	v_lshlrev_b32_e32 v40, 16, v82
	v_and_b32_e32 v41, 0xffff0000, v82
	v_lshlrev_b32_e32 v42, 16, v83
	v_and_b32_e32 v43, 0xffff0000, v83
	v_pk_mul_f32 v[34:35], v[34:35], v[38:39]
	v_pk_mul_f32 v[32:33], v[32:33], v[36:37]
	v_pk_mul_f32 v[38:39], v[28:29], v[40:41]
	v_pk_mul_f32 v[36:37], v[30:31], v[42:43]
	v_cvt_pk_bf16_f32 v28, v32, v33
	v_max_f32_e64 v3, |v32|, |v38|
	v_max_f32_e64 v32, |v33|, |v39|
	v_max3_f32 v3, v3, 0, v32
	v_max_f32_e64 v32, |v34|, |v36|
	v_max_f32_e64 v33, |v35|, |v37|
	v_cvt_pk_bf16_f32 v29, v34, v35
	v_cvt_pk_bf16_f32 v30, v38, v39
	v_cvt_pk_bf16_f32 v31, v36, v37
	v_max3_f32 v3, v3, v32, v33
	s_waitcnt vmcnt(6)
	v_lshlrev_b32_e32 v32, 16, v76
	v_and_b32_e32 v33, 0xffff0000, v76
	v_lshlrev_b32_e32 v34, 16, v77
	v_and_b32_e32 v35, 0xffff0000, v77
	v_lshlrev_b32_e32 v36, 16, v78
	v_and_b32_e32 v37, 0xffff0000, v78
	v_lshlrev_b32_e32 v38, 16, v79
	v_and_b32_e32 v39, 0xffff0000, v79
	v_pk_mul_f32 v[26:27], v[26:27], v[34:35]
	v_pk_mul_f32 v[24:25], v[24:25], v[32:33]
	v_pk_mul_f32 v[34:35], v[20:21], v[36:37]
	v_pk_mul_f32 v[32:33], v[22:23], v[38:39]
	v_max_f32_e64 v20, |v24|, |v34|
	v_max_f32_e64 v21, |v25|, |v35|
	v_max3_f32 v3, v3, v20, v21
	v_max_f32_e64 v20, |v26|, |v32|
	v_max_f32_e64 v21, |v27|, |v33|
	v_max3_f32 v3, v3, v20, v21
	ds_bpermute_b32 v23, v196, v3
	v_lshl_add_u64 v[20:21], s[14:15], 0, v[98:99]
	v_lshl_add_u64 v[36:37], v[176:177], 1, v[20:21]
	global_store_dwordx4 v[36:37], v[28:31], off sc0 sc1
	v_cvt_pk_bf16_f32 v22, v24, v25
	s_waitcnt lgkmcnt(0)
	v_max_f32_e32 v20, v23, v23
	v_max_f32_e32 v3, v3, v20
	ds_bpermute_b32 v20, v197, v3
	v_cvt_pk_bf16_f32 v23, v26, v27
	v_cvt_pk_bf16_f32 v24, v34, v35
	v_cvt_pk_bf16_f32 v25, v32, v33
	global_store_dwordx4 v[36:37], v[22:25], off offset:256 sc0 sc1
	s_and_saveexec_b64 s[48:49], vcc
	s_cbranch_execz .LBB0_980
	s_waitcnt lgkmcnt(0)
	v_max_f32_e32 v20, v20, v20
	v_max_f32_e32 v3, v3, v3
	v_lshl_add_u64 v[22:23], v[96:97], 2, s[10:11]
	v_max_f32_e32 v3, v3, v20
	global_atomic_umax v[22:23], v3, off
.LBB0_980:
	s_or_b64 exec, exec, s[48:49]
	s_waitcnt vmcnt(7) lgkmcnt(0)
	v_lshlrev_b32_e32 v20, 16, v72
	v_and_b32_e32 v21, 0xffff0000, v72
	v_lshlrev_b32_e32 v22, 16, v73
	v_and_b32_e32 v23, 0xffff0000, v73
	v_lshlrev_b32_e32 v24, 16, v74
	v_and_b32_e32 v25, 0xffff0000, v74
	v_lshlrev_b32_e32 v26, 16, v75
	v_and_b32_e32 v27, 0xffff0000, v75
	v_pk_mul_f32 v[18:19], v[18:19], v[22:23]
	v_pk_mul_f32 v[16:17], v[16:17], v[20:21]
	v_pk_mul_f32 v[22:23], v[12:13], v[24:25]
	v_pk_mul_f32 v[20:21], v[14:15], v[26:27]
	v_cvt_pk_bf16_f32 v12, v16, v17
	v_max_f32_e64 v3, |v16|, |v22|
	v_max_f32_e64 v16, |v17|, |v23|
	v_max3_f32 v3, v3, 0, v16
	v_max_f32_e64 v16, |v18|, |v20|
	v_max_f32_e64 v17, |v19|, |v21|
	v_cvt_pk_bf16_f32 v13, v18, v19
	v_cvt_pk_bf16_f32 v14, v22, v23
	v_cvt_pk_bf16_f32 v15, v20, v21
	v_max3_f32 v3, v3, v16, v17
	s_waitcnt vmcnt(6)
	v_lshlrev_b32_e32 v16, 16, v68
	v_and_b32_e32 v17, 0xffff0000, v68
	v_lshlrev_b32_e32 v18, 16, v69
	v_and_b32_e32 v19, 0xffff0000, v69
	v_lshlrev_b32_e32 v20, 16, v70
	v_and_b32_e32 v21, 0xffff0000, v70
	v_lshlrev_b32_e32 v22, 16, v71
	v_and_b32_e32 v23, 0xffff0000, v71
	v_pk_mul_f32 v[10:11], v[10:11], v[18:19]
	v_pk_mul_f32 v[8:9], v[8:9], v[16:17]
	v_pk_mul_f32 v[18:19], v[4:5], v[20:21]
	v_pk_mul_f32 v[16:17], v[6:7], v[22:23]
	v_max_f32_e64 v4, |v8|, |v18|
	v_max_f32_e64 v5, |v9|, |v19|
	v_max3_f32 v3, v3, v4, v5
	v_max_f32_e64 v4, |v10|, |v16|
	v_max_f32_e64 v5, |v11|, |v17|
	v_max3_f32 v3, v3, v4, v5
	ds_bpermute_b32 v7, v196, v3
	v_lshl_add_u64 v[4:5], s[14:15], 0, v[94:95]
	v_lshl_add_u64 v[20:21], v[176:177], 1, v[4:5]
	global_store_dwordx4 v[20:21], v[12:15], off sc0 sc1
	v_cvt_pk_bf16_f32 v6, v8, v9
	s_waitcnt lgkmcnt(0)
	v_max_f32_e32 v4, v7, v7
	v_max_f32_e32 v3, v3, v4
	ds_bpermute_b32 v4, v197, v3
	v_cvt_pk_bf16_f32 v7, v10, v11
	v_cvt_pk_bf16_f32 v8, v18, v19
	v_cvt_pk_bf16_f32 v9, v16, v17
	global_store_dwordx4 v[20:21], v[6:9], off offset:256 sc0 sc1
	s_and_saveexec_b64 s[48:49], vcc
	s_cbranch_execz .LBB0_982
	s_waitcnt lgkmcnt(0)
	v_max_f32_e32 v4, v4, v4
	v_max_f32_e32 v3, v3, v3
	v_lshl_add_u64 v[6:7], v[92:93], 2, s[10:11]
	v_max_f32_e32 v3, v3, v4
	global_atomic_umax v[6:7], v3, off

.LBB0_1125:
	v_mov_b32_e32 v84, 0
	v_mov_b32_e32 v82, 0
	s_lshl_b32 s42, s56, 8
	v_add_u32_e32 v228, v82, v1
	v_lshlrev_b32_e32 v146, 3, v228
	s_or_b32 s2, s42, s8
	v_add_u32_e32 v86, s2, v146
	s_lshl_b32 s2, s54, 8
	s_ashr_i32 s43, s42, 31
	v_add3_u32 v214, s2, v185, v84
	s_or_b64 s[44:45], s[42:43], s[8:9]
	s_lshl_b64 s[42:43], s[42:43], 2
	v_ashrrev_i32_e32 v215, 31, v214
	s_add_u32 s42, s71, s42
	v_lshl_add_u64 v[84:85], v[214:215], 2, s[16:17]
	v_ashrrev_i32_e32 v147, 31, v146
	s_addc_u32 s43, s72, s43
	v_ashrrev_i32_e32 v87, 31, v86
	global_load_dword v234, v[84:85], off
	v_lshl_add_u64 v[192:193], v[146:147], 2, s[42:43]
	v_lshlrev_b64 v[88:89], 13, v[214:215]
	v_lshlrev_b64 v[82:83], 2, v[86:87]
	v_lshl_add_u64 v[148:149], v[192:193], 0, v[88:89]
	v_lshl_add_u64 v[84:85], s[18:19], 0, v[82:83]
	global_load_dwordx4 v[216:219], v[148:149], off
	global_load_dwordx4 v[94:97], v[84:85], off
	global_load_dwordx4 v[90:93], v[84:85], off offset:16
	global_load_dwordx4 v[220:223], v[148:149], off offset:16
	v_cvt_f32_i32_e32 v247, v55
	v_cvt_f32_i32_e32 v246, v54
	v_lshl_add_u64 v[54:55], s[4:5], 0, v[82:83]
	v_cvt_f32_i32_e32 v237, v73
	v_cvt_f32_i32_e32 v236, v72
	v_cvt_f32_i32_e32 v239, v71
	v_cvt_f32_i32_e32 v238, v70
	global_load_dwordx4 v[70:73], v[54:55], off offset:16
	global_load_dwordx4 v[82:85], v[54:55], off
	v_cvt_f32_i32_e32 v242, v66
	v_add_u32_e32 v66, 0x80, v86
	v_cvt_f32_i32_e32 v243, v67
	v_ashrrev_i32_e32 v67, 31, v66
	v_lshl_add_u64 v[86:87], v[66:67], 2, s[18:19]
	v_cvt_f32_i32_e32 v241, v69
	v_cvt_f32_i32_e32 v240, v68
	v_cvt_f32_i32_e32 v245, v57
	v_cvt_f32_i32_e32 v244, v56
	v_cvt_f32_i32_e32 v249, v53
	v_cvt_f32_i32_e32 v248, v52
	v_cvt_f32_i32_e32 v251, v51
	v_cvt_f32_i32_e32 v250, v50
	global_load_dwordx4 v[50:53], v[54:55], off offset:528
	s_nop 0
	global_load_dwordx4 v[54:57], v[54:55], off offset:512
	s_nop 0
	global_load_dwordx4 v[66:69], v[86:87], off offset:16
	s_nop 0
	global_load_dwordx4 v[86:89], v[86:87], off
	s_nop 0
	global_load_dwordx4 v[224:227], v[148:149], off offset:528
	global_load_dwordx4 v[230:233], v[148:149], off offset:512
	v_add_u32_e32 v210, 16, v214
	v_ashrrev_i32_e32 v211, 31, v210
	v_add_u32_e32 v206, 32, v214
	v_add_u32_e32 v202, 48, v214
	v_add_u32_e32 v198, 0x80, v214
	v_add_u32_e32 v194, 0x90, v214
	v_add_u32_e32 v188, 0xa0, v214
	v_add_u32_e32 v182, 0xb0, v214
	v_lshl_add_u64 v[150:151], v[210:211], 2, s[16:17]
	v_ashrrev_i32_e32 v207, 31, v206
	v_ashrrev_i32_e32 v203, 31, v202
	v_ashrrev_i32_e32 v199, 31, v198
	v_ashrrev_i32_e32 v195, 31, v194
	v_ashrrev_i32_e32 v189, 31, v188
	v_ashrrev_i32_e32 v183, 31, v182
	v_lshl_add_u64 v[152:153], v[206:207], 2, s[16:17]
	v_lshl_add_u64 v[154:155], v[202:203], 2, s[16:17]
	v_lshl_add_u64 v[156:157], v[198:199], 2, s[16:17]
	v_lshl_add_u64 v[148:149], v[194:195], 2, s[16:17]
	v_lshl_add_u64 v[158:159], v[188:189], 2, s[16:17]
	v_lshl_add_u64 v[160:161], v[182:183], 2, s[16:17]
	global_load_dword v212, v[150:151], off
	global_load_dword v208, v[152:153], off
	global_load_dword v204, v[154:155], off
	global_load_dword v200, v[156:157], off
	global_load_dword v196, v[148:149], off
	global_load_dword v190, v[158:159], off
	global_load_dword v184, v[160:161], off
	v_lshl_add_u64 v[186:187], s[44:45], 0, v[146:147]
	v_lshlrev_b64 v[146:147], 13, v[210:211]
	v_lshl_add_u64 v[150:151], v[192:193], 0, v[146:147]
	global_load_dwordx4 v[154:157], v[150:151], off offset:16
	global_load_dwordx4 v[158:161], v[150:151], off
	global_load_dwordx4 v[146:149], v[150:151], off offset:528
	s_nop 0
	global_load_dwordx4 v[150:153], v[150:151], off offset:512
	v_lshlrev_b64 v[252:253], 11, v[214:215]
	v_cmp_eq_u32_e32 vcc, 0, v228
	v_lshl_add_u64 v[252:253], v[186:187], 0, v[252:253]
	v_lshlrev_b64 v[252:253], 1, v[252:253]
	s_waitcnt vmcnt(0)
	v_pk_mul_f32 v[238:239], v[234:235], v[238:239] op_sel_hi:[0,1]
	v_pk_mul_f32 v[236:237], v[234:235], v[236:237] op_sel_hi:[0,1]
	v_pk_fma_f32 v[236:237], v[236:237], v[96:97], v[218:219]
	v_pk_fma_f32 v[238:239], v[238:239], v[94:95], v[216:217]
	v_pk_mul_f32 v[216:217], v[234:235], v[242:243] op_sel_hi:[0,1]
	v_pk_mul_f32 v[218:219], v[234:235], v[240:241] op_sel_hi:[0,1]
	v_pk_fma_f32 v[240:241], v[218:219], v[92:93], v[222:223]
	v_pk_fma_f32 v[242:243], v[216:217], v[90:91], v[220:221]
	v_cvt_pk_bf16_f32 v216, v238, v239
	s_nop 0
	v_lshlrev_b32_e32 v217, 16, v216
	v_and_b32_e32 v218, 0xffff0000, v216
	v_sub_f32_e32 v217, v238, v217
	v_sub_f32_e32 v218, v239, v218
	v_cvt_pk_bf16_f32 v220, v217, v218
	v_cvt_pk_bf16_f32 v217, v236, v237
	s_nop 0
	v_lshlrev_b32_e32 v218, 16, v217
	v_and_b32_e32 v219, 0xffff0000, v217
	v_sub_f32_e32 v218, v236, v218
	v_sub_f32_e32 v219, v237, v219
	v_cvt_pk_bf16_f32 v221, v218, v219
	v_cvt_pk_bf16_f32 v218, v242, v243
	s_nop 0
	v_lshlrev_b32_e32 v219, 16, v218
	v_and_b32_e32 v222, 0xffff0000, v218
	v_sub_f32_e32 v219, v242, v219
	v_sub_f32_e32 v222, v243, v222
	v_cvt_pk_bf16_f32 v222, v219, v222
	v_cvt_pk_bf16_f32 v219, v240, v241
	s_nop 0
	v_lshlrev_b32_e32 v223, 16, v219
	v_and_b32_e32 v228, 0xffff0000, v219
	v_sub_f32_e32 v223, v240, v223
	v_sub_f32_e32 v228, v241, v228
	v_cvt_pk_bf16_f32 v223, v223, v228
	v_lshl_add_u64 v[228:229], s[48:49], 0, v[252:253]
	global_store_dwordx4 v[228:229], v[216:219], off sc0 sc1
	v_lshl_add_u64 v[252:253], s[12:13], 0, v[252:253]
	global_store_dwordx4 v[252:253], v[220:223], off sc0 sc1
	v_mul_f32_e32 v216, v82, v238
	v_mul_f32_e32 v217, v70, v242
	v_max_f32_e64 v216, |v216|, |v217|
	v_mul_f32_e32 v217, v83, v239
	v_mul_f32_e32 v218, v71, v243
	v_max_f32_e64 v217, |v217|, |v218|
	v_max3_f32 v216, v216, 0, v217
	v_mul_f32_e32 v217, v84, v236
	v_mul_f32_e32 v218, v72, v240
	v_max_f32_e64 v217, |v217|, |v218|
	v_mul_f32_e32 v218, v85, v237
	v_mul_f32_e32 v219, v73, v241
	v_max_f32_e64 v218, |v218|, |v219|
	v_max3_f32 v235, v216, v217, v218
	v_pk_mul_f32 v[218:219], v[234:235], v[244:245] op_sel_hi:[0,1]
	v_pk_mul_f32 v[216:217], v[234:235], v[246:247] op_sel_hi:[0,1]
	v_pk_fma_f32 v[232:233], v[218:219], v[88:89], v[232:233]
	v_pk_mul_f32 v[218:219], v[234:235], v[250:251] op_sel_hi:[0,1]
	v_pk_mul_f32 v[220:221], v[234:235], v[248:249] op_sel_hi:[0,1]
	v_pk_fma_f32 v[216:217], v[216:217], v[86:87], v[230:231]
	v_pk_fma_f32 v[226:227], v[220:221], v[68:69], v[226:227]
	v_pk_fma_f32 v[230:231], v[218:219], v[66:67], v[224:225]
	v_cvt_pk_bf16_f32 v218, v216, v217
	v_mul_f32_e32 v225, v53, v227
	v_lshlrev_b32_e32 v219, 16, v218
	v_and_b32_e32 v220, 0xffff0000, v218
	v_sub_f32_e32 v219, v216, v219
	v_sub_f32_e32 v220, v217, v220
	v_cvt_pk_bf16_f32 v222, v219, v220
	v_cvt_pk_bf16_f32 v219, v232, v233
	v_mul_f32_e32 v216, v54, v216
	v_lshlrev_b32_e32 v220, 16, v219
	v_and_b32_e32 v221, 0xffff0000, v219
	v_sub_f32_e32 v220, v232, v220
	v_sub_f32_e32 v221, v233, v221
	v_cvt_pk_bf16_f32 v223, v220, v221
	v_cvt_pk_bf16_f32 v220, v230, v231
	v_mul_f32_e32 v217, v55, v217
	v_lshlrev_b32_e32 v221, 16, v220
	v_and_b32_e32 v224, 0xffff0000, v220
	v_sub_f32_e32 v221, v230, v221
	v_sub_f32_e32 v224, v231, v224
	v_cvt_pk_bf16_f32 v224, v221, v224
	v_mul_f32_e32 v221, v50, v230
	v_max_f32_e64 v216, |v216|, |v221|
	v_mul_f32_e32 v221, v51, v231
	v_max_f32_e64 v217, |v217|, |v221|
	v_max3_f32 v216, v235, v216, v217
	v_mul_f32_e32 v217, v56, v232
	v_mul_f32_e32 v221, v52, v226
	v_max_f32_e64 v217, |v217|, |v221|
	v_mul_f32_e32 v221, v57, v233
	v_max_f32_e64 v221, |v221|, |v225|
	v_max3_f32 v216, v216, v217, v221
	ds_bpermute_b32 v217, v197, v216
	v_cvt_pk_bf16_f32 v221, v226, v227
	s_waitcnt lgkmcnt(0)
	v_max_f32_e32 v217, v217, v217
	v_max_f32_e32 v216, v216, v217
	ds_bpermute_b32 v217, v201, v216
	v_lshlrev_b32_e32 v225, 16, v221
	v_sub_f32_e32 v225, v226, v225
	v_and_b32_e32 v226, 0xffff0000, v221
	v_sub_f32_e32 v226, v227, v226
	v_cvt_pk_bf16_f32 v225, v225, v226
	global_store_dwordx4 v[228:229], v[218:221], off offset:256 sc0 sc1
	global_store_dwordx4 v[252:253], v[222:225], off offset:256 sc0 sc1
	s_and_saveexec_b64 s[54:55], vcc
	s_cbranch_execz .LBB0_1127
	s_waitcnt lgkmcnt(0)
	v_max_f32_e32 v217, v217, v217
	v_max_f32_e32 v216, v216, v216
	v_lshl_add_u64 v[214:215], v[214:215], 2, s[14:15]
	v_max_f32_e32 v216, v216, v217
	global_atomic_umax v[214:215], v216, off
.LBB0_1127:
	s_or_b64 exec, exec, s[54:55]
	v_cvt_f32_i32_e32 v145, v145
	v_cvt_f32_i32_e32 v144, v144
	v_cvt_f32_i32_e32 v143, v143
	v_cvt_f32_i32_e32 v142, v142
	v_cvt_f32_i32_e32 v141, v141
	v_cvt_f32_i32_e32 v140, v140
	v_cvt_f32_i32_e32 v139, v139
	v_cvt_f32_i32_e32 v138, v138
	v_cvt_f32_i32_e32 v221, v131
	v_cvt_f32_i32_e32 v220, v130
	v_lshlrev_b64 v[130:131], 11, v[210:211]
	v_cvt_f32_i32_e32 v219, v133
	v_cvt_f32_i32_e32 v218, v132
	v_lshl_add_u64 v[222:223], v[186:187], 0, v[130:131]
	v_pk_mul_f32 v[130:131], v[212:213], v[142:143] op_sel_hi:[0,1]
	v_pk_mul_f32 v[132:133], v[212:213], v[144:145] op_sel_hi:[0,1]
	v_pk_fma_f32 v[142:143], v[132:133], v[96:97], v[160:161]
	v_pk_fma_f32 v[144:145], v[130:131], v[94:95], v[158:159]
	v_pk_mul_f32 v[130:131], v[212:213], v[138:139] op_sel_hi:[0,1]
	v_pk_mul_f32 v[132:133], v[212:213], v[140:141] op_sel_hi:[0,1]
	v_pk_fma_f32 v[138:139], v[132:133], v[92:93], v[156:157]
	v_pk_fma_f32 v[140:141], v[130:131], v[90:91], v[154:155]
	v_cvt_pk_bf16_f32 v130, v144, v145
	v_cvt_f32_i32_e32 v216, v134
	v_lshlrev_b32_e32 v131, 16, v130
	v_and_b32_e32 v132, 0xffff0000, v130
	v_sub_f32_e32 v131, v144, v131
	v_sub_f32_e32 v132, v145, v132
	v_cvt_pk_bf16_f32 v134, v131, v132
	v_cvt_pk_bf16_f32 v131, v142, v143
	v_cvt_f32_i32_e32 v214, v136
	v_lshlrev_b32_e32 v132, 16, v131
	v_and_b32_e32 v133, 0xffff0000, v131
	v_sub_f32_e32 v132, v142, v132
	v_sub_f32_e32 v133, v143, v133
	s_waitcnt lgkmcnt(0)
	v_cvt_f32_i32_e32 v217, v135
	v_cvt_pk_bf16_f32 v135, v132, v133
	v_cvt_pk_bf16_f32 v132, v140, v141
	v_cvt_f32_i32_e32 v215, v137
	v_lshlrev_b32_e32 v133, 16, v132
	v_and_b32_e32 v136, 0xffff0000, v132
	v_sub_f32_e32 v133, v140, v133
	v_sub_f32_e32 v136, v141, v136
	v_cvt_pk_bf16_f32 v136, v133, v136
	v_cvt_pk_bf16_f32 v133, v138, v139
	s_nop 0
	v_lshlrev_b32_e32 v137, 16, v133
	v_and_b32_e32 v154, 0xffff0000, v133
	v_sub_f32_e32 v137, v138, v137
	v_sub_f32_e32 v154, v139, v154
	v_cvt_pk_bf16_f32 v137, v137, v154
	v_lshlrev_b64 v[154:155], 1, v[222:223]
	v_lshl_add_u64 v[156:157], s[48:49], 0, v[154:155]
	global_store_dwordx4 v[156:157], v[130:133], off sc0 sc1
	v_lshl_add_u64 v[154:155], s[12:13], 0, v[154:155]
	global_store_dwordx4 v[154:155], v[134:137], off sc0 sc1
	v_mul_f32_e32 v130, v82, v144
	v_mul_f32_e32 v131, v70, v140
	v_max_f32_e64 v130, |v130|, |v131|
	v_mul_f32_e32 v131, v83, v145
	v_mul_f32_e32 v132, v71, v141
	v_max_f32_e64 v131, |v131|, |v132|
	v_max3_f32 v130, v130, 0, v131
	v_mul_f32_e32 v131, v84, v142
	v_mul_f32_e32 v132, v72, v138
	v_max_f32_e64 v131, |v131|, |v132|
	v_mul_f32_e32 v132, v85, v143
	v_mul_f32_e32 v133, v73, v139
	v_max_f32_e64 v132, |v132|, |v133|
	v_max3_f32 v139, v130, v131, v132
	v_pk_mul_f32 v[132:133], v[212:213], v[214:215] op_sel_hi:[0,1]
	v_pk_mul_f32 v[130:131], v[212:213], v[216:217] op_sel_hi:[0,1]
	v_pk_fma_f32 v[140:141], v[132:133], v[88:89], v[152:153]
	v_pk_mul_f32 v[132:133], v[212:213], v[220:221] op_sel_hi:[0,1]
	v_pk_mul_f32 v[134:135], v[212:213], v[218:219] op_sel_hi:[0,1]
	v_pk_fma_f32 v[130:131], v[130:131], v[86:87], v[150:151]
	v_pk_fma_f32 v[142:143], v[134:135], v[68:69], v[148:149]
	v_pk_fma_f32 v[144:145], v[132:133], v[66:67], v[146:147]
	v_cvt_pk_bf16_f32 v132, v130, v131
	s_nop 0
	v_lshlrev_b32_e32 v133, 16, v132
	v_and_b32_e32 v134, 0xffff0000, v132
	v_sub_f32_e32 v133, v130, v133
	v_sub_f32_e32 v134, v131, v134
	v_cvt_pk_bf16_f32 v136, v133, v134
	v_cvt_pk_bf16_f32 v133, v140, v141
	v_mul_f32_e32 v130, v54, v130
	v_lshlrev_b32_e32 v134, 16, v133
	v_and_b32_e32 v135, 0xffff0000, v133
	v_sub_f32_e32 v134, v140, v134
	v_sub_f32_e32 v135, v141, v135
	v_cvt_pk_bf16_f32 v137, v134, v135
	v_cvt_pk_bf16_f32 v134, v144, v145
	v_mul_f32_e32 v131, v55, v131
	v_lshlrev_b32_e32 v135, 16, v134
	v_and_b32_e32 v138, 0xffff0000, v134
	v_sub_f32_e32 v135, v144, v135
	v_sub_f32_e32 v138, v145, v138
	v_cvt_pk_bf16_f32 v138, v135, v138
	v_mul_f32_e32 v135, v50, v144
	v_max_f32_e64 v130, |v130|, |v135|
	v_mul_f32_e32 v135, v51, v145
	v_max_f32_e64 v131, |v131|, |v135|
	v_max3_f32 v130, v139, v130, v131
	v_mul_f32_e32 v131, v56, v140
	v_mul_f32_e32 v135, v52, v142
	v_max_f32_e64 v131, |v131|, |v135|
	v_mul_f32_e32 v135, v57, v141
	v_mul_f32_e32 v139, v53, v143
	v_max_f32_e64 v135, |v135|, |v139|
	v_max3_f32 v130, v130, v131, v135
	ds_bpermute_b32 v131, v197, v130
	v_cvt_pk_bf16_f32 v135, v142, v143
	s_waitcnt lgkmcnt(0)
	v_max_f32_e32 v131, v131, v131
	v_max_f32_e32 v130, v130, v131
	ds_bpermute_b32 v131, v201, v130
	v_lshlrev_b32_e32 v139, 16, v135
	v_sub_f32_e32 v139, v142, v139
	v_and_b32_e32 v140, 0xffff0000, v135
	v_sub_f32_e32 v140, v143, v140
	v_cvt_pk_bf16_f32 v139, v139, v140
	global_store_dwordx4 v[156:157], v[132:135], off offset:256 sc0 sc1
	global_store_dwordx4 v[154:155], v[136:139], off offset:256 sc0 sc1
	s_and_saveexec_b64 s[54:55], vcc
	s_cbranch_execz .LBB0_1129
	s_waitcnt lgkmcnt(0)
	v_max_f32_e32 v131, v131, v131
	v_max_f32_e32 v130, v130, v130
	v_lshl_add_u64 v[132:133], v[210:211], 2, s[14:15]
	v_max_f32_e32 v130, v130, v131
	global_atomic_umax v[132:133], v130, off
.LBB0_1129:
	s_or_b64 exec, exec, s[54:55]
	s_waitcnt lgkmcnt(0)
	v_lshlrev_b64 v[130:131], 13, v[206:207]
	v_lshl_add_u64 v[142:143], v[192:193], 0, v[130:131]
	global_load_dwordx4 v[130:133], v[142:143], off
	global_load_dwordx4 v[134:137], v[142:143], off offset:16
	global_load_dwordx4 v[138:141], v[142:143], off offset:512
	s_nop 0
	global_load_dwordx4 v[142:145], v[142:143], off offset:528
	v_cvt_f32_i32_e32 v161, v115
	v_cvt_f32_i32_e32 v160, v114
	v_lshlrev_b64 v[114:115], 13, v[202:203]
	v_cvt_f32_i32_e32 v157, v119
	v_cvt_f32_i32_e32 v156, v118
	v_cvt_f32_i32_e32 v159, v117
	v_cvt_f32_i32_e32 v158, v116
	v_lshlrev_b64 v[116:117], 11, v[206:207]
	v_lshl_add_u64 v[118:119], v[192:193], 0, v[114:115]
	v_cvt_f32_i32_e32 v147, v129
	v_cvt_f32_i32_e32 v146, v128
	v_cvt_f32_i32_e32 v149, v127
	v_cvt_f32_i32_e32 v148, v126
	v_cvt_f32_i32_e32 v151, v125
	v_cvt_f32_i32_e32 v150, v124
	v_cvt_f32_i32_e32 v153, v123
	v_cvt_f32_i32_e32 v152, v122
	v_cvt_f32_i32_e32 v155, v121
	v_cvt_f32_i32_e32 v154, v120
	v_lshl_add_u64 v[210:211], v[186:187], 0, v[116:117]
	global_load_dwordx4 v[122:125], v[118:119], off offset:16
	global_load_dwordx4 v[126:129], v[118:119], off
	global_load_dwordx4 v[114:117], v[118:119], off offset:528
	s_nop 0
	global_load_dwordx4 v[118:121], v[118:119], off offset:512
	v_pk_mul_f32 v[148:149], v[208:209], v[148:149] op_sel_hi:[0,1]
	v_pk_mul_f32 v[146:147], v[208:209], v[146:147] op_sel_hi:[0,1]
	v_pk_mul_f32 v[152:153], v[208:209], v[152:153] op_sel_hi:[0,1]
	v_pk_mul_f32 v[150:151], v[208:209], v[150:151] op_sel_hi:[0,1]
	v_pk_mul_f32 v[156:157], v[208:209], v[156:157] op_sel_hi:[0,1]
	v_pk_mul_f32 v[154:155], v[208:209], v[154:155] op_sel_hi:[0,1]
	v_lshlrev_b64 v[210:211], 1, v[210:211]
	v_lshl_add_u64 v[214:215], s[48:49], 0, v[210:211]
	v_lshl_add_u64 v[210:211], s[12:13], 0, v[210:211]
	v_pk_mul_f32 v[160:161], v[208:209], v[160:161] op_sel_hi:[0,1]
	v_pk_mul_f32 v[158:159], v[208:209], v[158:159] op_sel_hi:[0,1]
	s_waitcnt vmcnt(7)
	v_pk_fma_f32 v[132:133], v[146:147], v[96:97], v[132:133]
	v_pk_fma_f32 v[146:147], v[148:149], v[94:95], v[130:131]
	s_waitcnt vmcnt(6)
	v_pk_fma_f32 v[148:149], v[150:151], v[92:93], v[136:137]
	v_pk_fma_f32 v[136:137], v[152:153], v[90:91], v[134:135]
	s_waitcnt vmcnt(5)
	v_pk_fma_f32 v[150:151], v[156:157], v[86:87], v[138:139]
	v_mul_f32_e32 v131, v82, v146
	v_mul_f32_e32 v134, v70, v136
	v_mul_f32_e32 v135, v83, v147
	v_mul_f32_e32 v138, v71, v137
	v_pk_fma_f32 v[140:141], v[154:155], v[88:89], v[140:141]
	v_cvt_pk_bf16_f32 v130, v146, v147
	v_mul_f32_e32 v139, v84, v132
	v_mul_f32_e32 v152, v72, v148
	v_mul_f32_e32 v153, v85, v133
	v_mul_f32_e32 v154, v73, v149
	v_lshlrev_b32_e32 v155, 16, v130
	v_and_b32_e32 v156, 0xffff0000, v130
	v_max_f32_e64 v131, |v131|, |v134|
	v_max_f32_e64 v134, |v135|, |v138|
	v_max_f32_e64 v135, |v139|, |v152|
	v_max_f32_e64 v138, |v153|, |v154|
	v_sub_f32_e32 v139, v146, v155
	v_sub_f32_e32 v146, v147, v156
	v_max3_f32 v147, v131, 0, v134
	v_cvt_pk_bf16_f32 v134, v139, v146
	v_cvt_pk_bf16_f32 v131, v132, v133
	v_max3_f32 v139, v147, v135, v138
	v_lshlrev_b32_e32 v135, 16, v131
	v_and_b32_e32 v138, 0xffff0000, v131
	v_sub_f32_e32 v132, v132, v135
	v_sub_f32_e32 v133, v133, v138
	v_cvt_pk_bf16_f32 v135, v132, v133
	v_cvt_pk_bf16_f32 v132, v136, v137
	s_waitcnt vmcnt(4)
	v_pk_fma_f32 v[142:143], v[160:161], v[66:67], v[142:143]
	v_lshlrev_b32_e32 v133, 16, v132
	v_and_b32_e32 v138, 0xffff0000, v132
	v_sub_f32_e32 v133, v136, v133
	v_sub_f32_e32 v136, v137, v138
	v_cvt_pk_bf16_f32 v136, v133, v136
	v_cvt_pk_bf16_f32 v133, v148, v149
	v_pk_fma_f32 v[144:145], v[158:159], v[68:69], v[144:145]
	v_lshlrev_b32_e32 v137, 16, v133
	v_and_b32_e32 v138, 0xffff0000, v133
	v_sub_f32_e32 v137, v148, v137
	v_sub_f32_e32 v138, v149, v138
	v_cvt_pk_bf16_f32 v137, v137, v138
	global_store_dwordx4 v[214:215], v[130:133], off sc0 sc1
	global_store_dwordx4 v[210:211], v[134:137], off sc0 sc1
	s_nop 0
	v_cvt_pk_bf16_f32 v132, v150, v151
	s_nop 0
	v_lshlrev_b32_e32 v130, 16, v132
	v_and_b32_e32 v131, 0xffff0000, v132
	v_sub_f32_e32 v130, v150, v130
	v_sub_f32_e32 v131, v151, v131
	v_cvt_pk_bf16_f32 v136, v130, v131
	v_cvt_pk_bf16_f32 v133, v140, v141
	v_mul_f32_e32 v135, v51, v143
	v_lshlrev_b32_e32 v130, 16, v133
	v_and_b32_e32 v131, 0xffff0000, v133
	v_sub_f32_e32 v130, v140, v130
	v_sub_f32_e32 v131, v141, v131
	v_cvt_pk_bf16_f32 v137, v130, v131
	v_cvt_pk_bf16_f32 v134, v142, v143
	s_nop 0
	v_lshlrev_b32_e32 v130, 16, v134
	v_and_b32_e32 v131, 0xffff0000, v134
	v_sub_f32_e32 v130, v142, v130
	v_sub_f32_e32 v131, v143, v131
	v_cvt_pk_bf16_f32 v138, v130, v131
	v_mul_f32_e32 v130, v54, v150
	v_mul_f32_e32 v131, v50, v142
	v_max_f32_e64 v130, |v130|, |v131|
	v_mul_f32_e32 v131, v55, v151
	v_max_f32_e64 v131, |v131|, |v135|
	v_max3_f32 v130, v139, v130, v131
	v_mul_f32_e32 v131, v56, v140
	v_mul_f32_e32 v135, v52, v144
	v_max_f32_e64 v131, |v131|, |v135|
	v_mul_f32_e32 v135, v57, v141
	v_mul_f32_e32 v139, v53, v145
	v_max_f32_e64 v135, |v135|, |v139|
	v_max3_f32 v130, v130, v131, v135
	ds_bpermute_b32 v131, v197, v130
	v_cvt_pk_bf16_f32 v135, v144, v145
	s_waitcnt lgkmcnt(0)
	v_max_f32_e32 v131, v131, v131
	v_max_f32_e32 v130, v130, v131
	ds_bpermute_b32 v131, v201, v130
	v_lshlrev_b32_e32 v139, 16, v135
	v_sub_f32_e32 v139, v144, v139
	v_and_b32_e32 v140, 0xffff0000, v135
	v_sub_f32_e32 v140, v145, v140
	v_cvt_pk_bf16_f32 v139, v139, v140
	global_store_dwordx4 v[214:215], v[132:135], off offset:256 sc0 sc1
	global_store_dwordx4 v[210:211], v[136:139], off offset:256 sc0 sc1
	s_and_saveexec_b64 s[54:55], vcc
	s_cbranch_execz .LBB0_1131
	s_waitcnt lgkmcnt(0)
	v_max_f32_e32 v131, v131, v131
	v_max_f32_e32 v130, v130, v130
	v_lshl_add_u64 v[132:133], v[206:207], 2, s[14:15]
	v_max_f32_e32 v130, v130, v131
	global_atomic_umax v[132:133], v130, off
.LBB0_1131:
	s_or_b64 exec, exec, s[54:55]
	v_cvt_f32_i32_e32 v113, v113
	v_cvt_f32_i32_e32 v112, v112
	v_cvt_f32_i32_e32 v111, v111
	v_cvt_f32_i32_e32 v110, v110
	v_cvt_f32_i32_e32 v109, v109
	v_cvt_f32_i32_e32 v108, v108
	v_cvt_f32_i32_e32 v107, v107
	v_cvt_f32_i32_e32 v106, v106
	v_cvt_f32_i32_e32 v137, v99
	v_cvt_f32_i32_e32 v136, v98
	v_lshlrev_b64 v[98:99], 11, v[202:203]
	v_cvt_f32_i32_e32 v135, v101
	v_cvt_f32_i32_e32 v134, v100
	v_lshl_add_u64 v[138:139], v[186:187], 0, v[98:99]
	v_pk_mul_f32 v[98:99], v[204:205], v[110:111] op_sel_hi:[0,1]
	v_pk_mul_f32 v[100:101], v[204:205], v[112:113] op_sel_hi:[0,1]
	s_waitcnt vmcnt(6)
	v_pk_fma_f32 v[110:111], v[100:101], v[96:97], v[128:129]
	v_pk_fma_f32 v[112:113], v[98:99], v[94:95], v[126:127]
	v_pk_mul_f32 v[98:99], v[204:205], v[106:107] op_sel_hi:[0,1]
	v_pk_mul_f32 v[100:101], v[204:205], v[108:109] op_sel_hi:[0,1]
	v_pk_fma_f32 v[106:107], v[100:101], v[92:93], v[124:125]
	v_pk_fma_f32 v[108:109], v[98:99], v[90:91], v[122:123]
	v_cvt_pk_bf16_f32 v98, v112, v113
	v_cvt_f32_i32_e32 v132, v102
	v_lshlrev_b32_e32 v99, 16, v98
	v_and_b32_e32 v100, 0xffff0000, v98
	v_sub_f32_e32 v99, v112, v99
	v_sub_f32_e32 v100, v113, v100
	v_cvt_pk_bf16_f32 v102, v99, v100
	v_cvt_pk_bf16_f32 v99, v110, v111
	v_cvt_f32_i32_e32 v130, v104
	v_lshlrev_b32_e32 v100, 16, v99
	v_and_b32_e32 v101, 0xffff0000, v99
	v_sub_f32_e32 v100, v110, v100
	v_sub_f32_e32 v101, v111, v101
	v_cvt_f32_i32_e32 v133, v103
	v_cvt_pk_bf16_f32 v103, v100, v101
	v_cvt_pk_bf16_f32 v100, v108, v109
	s_waitcnt lgkmcnt(0)
	v_cvt_f32_i32_e32 v131, v105
	v_lshlrev_b32_e32 v101, 16, v100
	v_and_b32_e32 v104, 0xffff0000, v100
	v_sub_f32_e32 v101, v108, v101
	v_sub_f32_e32 v104, v109, v104
	v_cvt_pk_bf16_f32 v104, v101, v104
	v_cvt_pk_bf16_f32 v101, v106, v107
	s_nop 0
	v_lshlrev_b32_e32 v105, 16, v101
	v_and_b32_e32 v122, 0xffff0000, v101
	v_sub_f32_e32 v105, v106, v105
	v_sub_f32_e32 v122, v107, v122
	v_cvt_pk_bf16_f32 v105, v105, v122
	v_lshlrev_b64 v[122:123], 1, v[138:139]
	v_lshl_add_u64 v[124:125], s[48:49], 0, v[122:123]
	global_store_dwordx4 v[124:125], v[98:101], off sc0 sc1
	v_lshl_add_u64 v[122:123], s[12:13], 0, v[122:123]
	global_store_dwordx4 v[122:123], v[102:105], off sc0 sc1
	v_mul_f32_e32 v98, v82, v112
	v_mul_f32_e32 v99, v70, v108
	v_max_f32_e64 v98, |v98|, |v99|
	v_mul_f32_e32 v99, v83, v113
	v_mul_f32_e32 v100, v71, v109
	v_max_f32_e64 v99, |v99|, |v100|
	v_max3_f32 v98, v98, 0, v99
	v_mul_f32_e32 v99, v84, v110
	v_mul_f32_e32 v100, v72, v106
	v_max_f32_e64 v99, |v99|, |v100|
	v_mul_f32_e32 v100, v85, v111
	v_mul_f32_e32 v101, v73, v107
	v_max_f32_e64 v100, |v100|, |v101|
	v_max3_f32 v107, v98, v99, v100
	v_pk_mul_f32 v[100:101], v[204:205], v[130:131] op_sel_hi:[0,1]
	v_pk_mul_f32 v[98:99], v[204:205], v[132:133] op_sel_hi:[0,1]
	s_waitcnt vmcnt(6)
	v_pk_fma_f32 v[108:109], v[100:101], v[88:89], v[120:121]
	v_pk_mul_f32 v[100:101], v[204:205], v[136:137] op_sel_hi:[0,1]
	v_pk_mul_f32 v[102:103], v[204:205], v[134:135] op_sel_hi:[0,1]
	v_pk_fma_f32 v[98:99], v[98:99], v[86:87], v[118:119]
	v_pk_fma_f32 v[110:111], v[102:103], v[68:69], v[116:117]
	v_pk_fma_f32 v[112:113], v[100:101], v[66:67], v[114:115]
	v_cvt_pk_bf16_f32 v100, v98, v99
	s_nop 0
	v_lshlrev_b32_e32 v101, 16, v100
	v_and_b32_e32 v102, 0xffff0000, v100
	v_sub_f32_e32 v101, v98, v101
	v_sub_f32_e32 v102, v99, v102
	v_cvt_pk_bf16_f32 v104, v101, v102
	v_cvt_pk_bf16_f32 v101, v108, v109
	v_mul_f32_e32 v98, v54, v98
	v_lshlrev_b32_e32 v102, 16, v101
	v_and_b32_e32 v103, 0xffff0000, v101
	v_sub_f32_e32 v102, v108, v102
	v_sub_f32_e32 v103, v109, v103
	v_cvt_pk_bf16_f32 v105, v102, v103
	v_cvt_pk_bf16_f32 v102, v112, v113
	v_mul_f32_e32 v99, v55, v99
	v_lshlrev_b32_e32 v103, 16, v102
	v_and_b32_e32 v106, 0xffff0000, v102
	v_sub_f32_e32 v103, v112, v103
	v_sub_f32_e32 v106, v113, v106
	v_cvt_pk_bf16_f32 v106, v103, v106
	v_mul_f32_e32 v103, v50, v112
	v_max_f32_e64 v98, |v98|, |v103|
	v_mul_f32_e32 v103, v51, v113
	v_max_f32_e64 v99, |v99|, |v103|
	v_max3_f32 v98, v107, v98, v99
	v_mul_f32_e32 v99, v56, v108
	v_mul_f32_e32 v103, v52, v110
	v_max_f32_e64 v99, |v99|, |v103|
	v_mul_f32_e32 v103, v57, v109
	v_mul_f32_e32 v107, v53, v111
	v_max_f32_e64 v103, |v103|, |v107|
	v_max3_f32 v98, v98, v99, v103
	ds_bpermute_b32 v99, v197, v98
	v_cvt_pk_bf16_f32 v103, v110, v111
	s_waitcnt lgkmcnt(0)
	v_max_f32_e32 v99, v99, v99
	v_max_f32_e32 v98, v98, v99
	ds_bpermute_b32 v99, v201, v98
	v_lshlrev_b32_e32 v107, 16, v103
	v_sub_f32_e32 v107, v110, v107
	v_and_b32_e32 v108, 0xffff0000, v103
	v_sub_f32_e32 v108, v111, v108
	v_cvt_pk_bf16_f32 v107, v107, v108
	global_store_dwordx4 v[124:125], v[100:103], off offset:256 sc0 sc1
	global_store_dwordx4 v[122:123], v[104:107], off offset:256 sc0 sc1
	s_and_saveexec_b64 s[54:55], vcc
	s_cbranch_execz .LBB0_1133
	s_waitcnt lgkmcnt(0)
	v_max_f32_e32 v99, v99, v99
	v_max_f32_e32 v98, v98, v98
	v_lshl_add_u64 v[100:101], v[202:203], 2, s[14:15]
	v_max_f32_e32 v98, v98, v99
	global_atomic_umax v[100:101], v98, off
.LBB0_1133:
	s_or_b64 exec, exec, s[54:55]
	s_waitcnt lgkmcnt(0)
	v_lshlrev_b64 v[98:99], 13, v[198:199]
	v_lshl_add_u64 v[110:111], v[192:193], 0, v[98:99]
	global_load_dwordx4 v[98:101], v[110:111], off
	global_load_dwordx4 v[102:105], v[110:111], off offset:16
	global_load_dwordx4 v[106:109], v[110:111], off offset:512
	s_nop 0
	global_load_dwordx4 v[110:113], v[110:111], off offset:528
	v_cvt_f32_i32_e32 v121, v59
	v_cvt_f32_i32_e32 v120, v58
	v_lshlrev_b64 v[58:59], 13, v[194:195]
	v_cvt_f32_i32_e32 v117, v63
	v_cvt_f32_i32_e32 v116, v62
	v_cvt_f32_i32_e32 v119, v61
	v_cvt_f32_i32_e32 v118, v60
	v_lshlrev_b64 v[60:61], 11, v[198:199]
	v_lshl_add_u64 v[62:63], v[192:193], 0, v[58:59]
	v_cvt_f32_i32_e32 v115, v65
	v_cvt_f32_i32_e32 v114, v64
	v_cvt_f32_i32_e32 v123, v77
	v_cvt_f32_i32_e32 v122, v76
	v_cvt_f32_i32_e32 v125, v75
	v_cvt_f32_i32_e32 v124, v74
	v_cvt_f32_i32_e32 v127, v81
	v_cvt_f32_i32_e32 v126, v80
	v_cvt_f32_i32_e32 v129, v79
	v_cvt_f32_i32_e32 v128, v78
	v_lshl_add_u64 v[130:131], v[186:187], 0, v[60:61]
	global_load_dwordx4 v[74:77], v[62:63], off offset:16
	global_load_dwordx4 v[78:81], v[62:63], off
	global_load_dwordx4 v[58:61], v[62:63], off offset:528
	s_nop 0
	global_load_dwordx4 v[62:65], v[62:63], off offset:512
	v_pk_mul_f32 v[116:117], v[200:201], v[116:117] op_sel_hi:[0,1]
	v_pk_mul_f32 v[114:115], v[200:201], v[114:115] op_sel_hi:[0,1]
	v_pk_mul_f32 v[120:121], v[200:201], v[120:121] op_sel_hi:[0,1]
	v_pk_mul_f32 v[118:119], v[200:201], v[118:119] op_sel_hi:[0,1]
	v_pk_mul_f32 v[124:125], v[200:201], v[124:125] op_sel_hi:[0,1]
	v_pk_mul_f32 v[122:123], v[200:201], v[122:123] op_sel_hi:[0,1]
	v_lshlrev_b64 v[130:131], 1, v[130:131]
	v_lshl_add_u64 v[132:133], s[48:49], 0, v[130:131]
	v_lshl_add_u64 v[130:131], s[12:13], 0, v[130:131]
	v_pk_mul_f32 v[128:129], v[200:201], v[128:129] op_sel_hi:[0,1]
	v_pk_mul_f32 v[126:127], v[200:201], v[126:127] op_sel_hi:[0,1]
	s_waitcnt vmcnt(7)
	v_pk_fma_f32 v[100:101], v[114:115], v[96:97], v[100:101]
	v_pk_fma_f32 v[114:115], v[116:117], v[94:95], v[98:99]
	s_waitcnt vmcnt(6)
	v_pk_fma_f32 v[116:117], v[118:119], v[92:93], v[104:105]
	v_pk_fma_f32 v[104:105], v[120:121], v[90:91], v[102:103]
	s_waitcnt vmcnt(5)
	v_pk_fma_f32 v[118:119], v[124:125], v[86:87], v[106:107]
	v_mul_f32_e32 v99, v82, v114
	v_mul_f32_e32 v102, v70, v104
	v_mul_f32_e32 v103, v83, v115
	v_mul_f32_e32 v106, v71, v105
	v_pk_fma_f32 v[108:109], v[122:123], v[88:89], v[108:109]
	v_cvt_pk_bf16_f32 v98, v114, v115
	v_mul_f32_e32 v107, v84, v100
	v_mul_f32_e32 v120, v72, v116
	v_mul_f32_e32 v121, v85, v101
	v_mul_f32_e32 v122, v73, v117
	v_lshlrev_b32_e32 v123, 16, v98
	v_and_b32_e32 v124, 0xffff0000, v98
	v_max_f32_e64 v99, |v99|, |v102|
	v_max_f32_e64 v102, |v103|, |v106|
	v_max_f32_e64 v103, |v107|, |v120|
	v_max_f32_e64 v106, |v121|, |v122|
	v_sub_f32_e32 v107, v114, v123
	v_sub_f32_e32 v114, v115, v124
	v_max3_f32 v115, v99, 0, v102
	v_cvt_pk_bf16_f32 v102, v107, v114
	v_cvt_pk_bf16_f32 v99, v100, v101
	v_max3_f32 v107, v115, v103, v106
	v_lshlrev_b32_e32 v103, 16, v99
	v_and_b32_e32 v106, 0xffff0000, v99
	v_sub_f32_e32 v100, v100, v103
	v_sub_f32_e32 v101, v101, v106
	v_cvt_pk_bf16_f32 v103, v100, v101
	v_cvt_pk_bf16_f32 v100, v104, v105
	s_waitcnt vmcnt(4)
	v_pk_fma_f32 v[110:111], v[128:129], v[66:67], v[110:111]
	v_lshlrev_b32_e32 v101, 16, v100
	v_and_b32_e32 v106, 0xffff0000, v100
	v_sub_f32_e32 v101, v104, v101
	v_sub_f32_e32 v104, v105, v106
	v_cvt_pk_bf16_f32 v104, v101, v104
	v_cvt_pk_bf16_f32 v101, v116, v117
	v_pk_fma_f32 v[112:113], v[126:127], v[68:69], v[112:113]
	v_lshlrev_b32_e32 v105, 16, v101
	v_and_b32_e32 v106, 0xffff0000, v101
	v_sub_f32_e32 v105, v116, v105
	v_sub_f32_e32 v106, v117, v106
	v_cvt_pk_bf16_f32 v105, v105, v106
	global_store_dwordx4 v[132:133], v[98:101], off sc0 sc1
	global_store_dwordx4 v[130:131], v[102:105], off sc0 sc1
	s_nop 0
	v_cvt_pk_bf16_f32 v100, v118, v119
	s_nop 0
	v_lshlrev_b32_e32 v98, 16, v100
	v_and_b32_e32 v99, 0xffff0000, v100
	v_sub_f32_e32 v98, v118, v98
	v_sub_f32_e32 v99, v119, v99
	v_cvt_pk_bf16_f32 v104, v98, v99
	v_cvt_pk_bf16_f32 v101, v108, v109
	v_mul_f32_e32 v103, v51, v111
	v_lshlrev_b32_e32 v98, 16, v101
	v_and_b32_e32 v99, 0xffff0000, v101
	v_sub_f32_e32 v98, v108, v98
	v_sub_f32_e32 v99, v109, v99
	v_cvt_pk_bf16_f32 v105, v98, v99
	v_cvt_pk_bf16_f32 v102, v110, v111
	s_nop 0
	v_lshlrev_b32_e32 v98, 16, v102
	v_and_b32_e32 v99, 0xffff0000, v102
	v_sub_f32_e32 v98, v110, v98
	v_sub_f32_e32 v99, v111, v99
	v_cvt_pk_bf16_f32 v106, v98, v99
	v_mul_f32_e32 v98, v54, v118
	v_mul_f32_e32 v99, v50, v110
	v_max_f32_e64 v98, |v98|, |v99|
	v_mul_f32_e32 v99, v55, v119
	v_max_f32_e64 v99, |v99|, |v103|
	v_max3_f32 v98, v107, v98, v99
	v_mul_f32_e32 v99, v56, v108
	v_mul_f32_e32 v103, v52, v112
	v_max_f32_e64 v99, |v99|, |v103|
	v_mul_f32_e32 v103, v57, v109
	v_mul_f32_e32 v107, v53, v113
	v_max_f32_e64 v103, |v103|, |v107|
	v_max3_f32 v98, v98, v99, v103
	ds_bpermute_b32 v99, v197, v98
	v_cvt_pk_bf16_f32 v103, v112, v113
	s_waitcnt lgkmcnt(0)
	v_max_f32_e32 v99, v99, v99
	v_max_f32_e32 v98, v98, v99
	ds_bpermute_b32 v99, v201, v98
	v_lshlrev_b32_e32 v107, 16, v103
	v_sub_f32_e32 v107, v112, v107
	v_and_b32_e32 v108, 0xffff0000, v103
	v_sub_f32_e32 v108, v113, v108
	v_cvt_pk_bf16_f32 v107, v107, v108
	global_store_dwordx4 v[132:133], v[100:103], off offset:256 sc0 sc1
	global_store_dwordx4 v[130:131], v[104:107], off offset:256 sc0 sc1
	s_and_saveexec_b64 s[54:55], vcc
	s_cbranch_execz .LBB0_1135
	s_waitcnt lgkmcnt(0)
	v_max_f32_e32 v99, v99, v99
	v_max_f32_e32 v98, v98, v98
	v_lshl_add_u64 v[100:101], v[198:199], 2, s[14:15]
	v_max_f32_e32 v98, v98, v99
	global_atomic_umax v[100:101], v98, off
.LBB0_1135:
	s_or_b64 exec, exec, s[54:55]
	v_cvt_f32_i32_e32 v39, v39
	v_cvt_f32_i32_e32 v38, v38
	v_cvt_f32_i32_e32 v37, v37
	v_cvt_f32_i32_e32 v36, v36
	v_cvt_f32_i32_e32 v35, v35
	v_cvt_f32_i32_e32 v34, v34
	v_cvt_f32_i32_e32 v41, v41
	v_cvt_f32_i32_e32 v40, v40
	v_pk_mul_f32 v[38:39], v[196:197], v[38:39] op_sel_hi:[0,1]
	v_pk_mul_f32 v[34:35], v[196:197], v[34:35] op_sel_hi:[0,1]
	v_pk_mul_f32 v[36:37], v[196:197], v[36:37] op_sel_hi:[0,1]
	s_waitcnt vmcnt(6)
	v_pk_fma_f32 v[78:79], v[94:95], v[38:39], v[78:79]
	v_pk_fma_f32 v[76:77], v[36:37], v[92:93], v[76:77]
	v_pk_fma_f32 v[74:75], v[34:35], v[90:91], v[74:75]
	v_cvt_pk_bf16_f32 v34, v78, v79
	v_pk_mul_f32 v[40:41], v[196:197], v[40:41] op_sel_hi:[0,1]
	v_lshlrev_b32_e32 v35, 16, v34
	v_and_b32_e32 v36, 0xffff0000, v34
	v_sub_f32_e32 v35, v78, v35
	v_sub_f32_e32 v36, v79, v36
	v_pk_fma_f32 v[80:81], v[96:97], v[40:41], v[80:81]
	v_cvt_pk_bf16_f32 v38, v35, v36
	s_waitcnt lgkmcnt(0)
	v_lshlrev_b64 v[98:99], 11, v[194:195]
	v_cvt_pk_bf16_f32 v35, v80, v81
	v_lshl_add_u64 v[98:99], v[186:187], 0, v[98:99]
	v_lshlrev_b32_e32 v36, 16, v35
	v_and_b32_e32 v37, 0xffff0000, v35
	v_sub_f32_e32 v36, v80, v36
	v_sub_f32_e32 v37, v81, v37
	v_cvt_pk_bf16_f32 v39, v36, v37
	v_cvt_pk_bf16_f32 v36, v74, v75
	v_lshlrev_b64 v[98:99], 1, v[98:99]
	v_lshlrev_b32_e32 v37, 16, v36
	v_and_b32_e32 v40, 0xffff0000, v36
	v_sub_f32_e32 v37, v74, v37
	v_sub_f32_e32 v40, v75, v40
	v_cvt_pk_bf16_f32 v40, v37, v40
	v_cvt_pk_bf16_f32 v37, v76, v77
	v_cvt_f32_i32_e32 v45, v45
	v_lshlrev_b32_e32 v41, 16, v37
	v_and_b32_e32 v100, 0xffff0000, v37
	v_sub_f32_e32 v41, v76, v41
	v_sub_f32_e32 v100, v77, v100
	v_cvt_pk_bf16_f32 v41, v41, v100
	v_lshl_add_u64 v[100:101], s[48:49], 0, v[98:99]
	global_store_dwordx4 v[100:101], v[34:37], off sc0 sc1
	v_cvt_f32_i32_e32 v44, v44
	v_cvt_f32_i32_e32 v43, v43
	v_mul_f32_e32 v34, v82, v78
	v_mul_f32_e32 v35, v70, v74
	v_max_f32_e64 v34, |v34|, |v35|
	v_mul_f32_e32 v35, v83, v79
	v_mul_f32_e32 v36, v71, v75
	v_max_f32_e64 v35, |v35|, |v36|
	v_cvt_f32_i32_e32 v42, v42
	v_cvt_f32_i32_e32 v49, v49
	v_cvt_f32_i32_e32 v48, v48
	v_cvt_f32_i32_e32 v47, v47
	v_cvt_f32_i32_e32 v46, v46
	v_max3_f32 v34, v34, 0, v35
	v_mul_f32_e32 v35, v84, v80
	v_mul_f32_e32 v36, v72, v76
	v_max_f32_e64 v35, |v35|, |v36|
	v_mul_f32_e32 v36, v85, v81
	v_mul_f32_e32 v37, v73, v77
	v_max_f32_e64 v36, |v36|, |v37|
	v_lshl_add_u64 v[98:99], s[12:13], 0, v[98:99]
	v_max3_f32 v74, v34, v35, v36
	v_pk_mul_f32 v[36:37], v[196:197], v[44:45] op_sel_hi:[0,1]
	global_store_dwordx4 v[98:99], v[38:41], off sc0 sc1
	v_pk_mul_f32 v[34:35], v[196:197], v[42:43] op_sel_hi:[0,1]
	s_waitcnt vmcnt(6)
	v_pk_fma_f32 v[44:45], v[36:37], v[88:89], v[64:65]
	v_pk_mul_f32 v[36:37], v[196:197], v[46:47] op_sel_hi:[0,1]
	v_pk_mul_f32 v[38:39], v[196:197], v[48:49] op_sel_hi:[0,1]
	v_pk_fma_f32 v[34:35], v[34:35], v[86:87], v[62:63]
	v_pk_fma_f32 v[46:47], v[38:39], v[68:69], v[60:61]
	v_pk_fma_f32 v[48:49], v[36:37], v[66:67], v[58:59]
	v_cvt_pk_bf16_f32 v36, v34, v35
	v_mul_f32_e32 v43, v53, v47
	v_lshlrev_b32_e32 v37, 16, v36
	v_and_b32_e32 v38, 0xffff0000, v36
	v_sub_f32_e32 v37, v34, v37
	v_sub_f32_e32 v38, v35, v38
	v_cvt_pk_bf16_f32 v40, v37, v38
	v_cvt_pk_bf16_f32 v37, v44, v45
	v_mul_f32_e32 v34, v54, v34
	v_lshlrev_b32_e32 v38, 16, v37
	v_and_b32_e32 v39, 0xffff0000, v37
	v_sub_f32_e32 v38, v44, v38
	v_sub_f32_e32 v39, v45, v39
	v_cvt_pk_bf16_f32 v41, v38, v39
	v_cvt_pk_bf16_f32 v38, v48, v49
	v_mul_f32_e32 v35, v55, v35
	v_lshlrev_b32_e32 v39, 16, v38
	v_and_b32_e32 v42, 0xffff0000, v38
	v_sub_f32_e32 v39, v48, v39
	v_sub_f32_e32 v42, v49, v42
	v_cvt_pk_bf16_f32 v42, v39, v42
	v_mul_f32_e32 v39, v50, v48
	v_max_f32_e64 v34, |v34|, |v39|
	v_mul_f32_e32 v39, v51, v49
	v_max_f32_e64 v35, |v35|, |v39|
	v_max3_f32 v34, v74, v34, v35
	v_mul_f32_e32 v35, v56, v44
	v_mul_f32_e32 v39, v52, v46
	v_max_f32_e64 v35, |v35|, |v39|
	v_mul_f32_e32 v39, v57, v45
	v_max_f32_e64 v39, |v39|, |v43|
	v_max3_f32 v34, v34, v35, v39
	ds_bpermute_b32 v35, v197, v34
	v_cvt_pk_bf16_f32 v39, v46, v47
	s_waitcnt lgkmcnt(0)
	v_max_f32_e32 v35, v35, v35
	v_max_f32_e32 v34, v34, v35
	ds_bpermute_b32 v35, v201, v34
	v_lshlrev_b32_e32 v43, 16, v39
	v_sub_f32_e32 v43, v46, v43
	v_and_b32_e32 v44, 0xffff0000, v39
	v_sub_f32_e32 v44, v47, v44
	v_cvt_pk_bf16_f32 v43, v43, v44
	global_store_dwordx4 v[100:101], v[36:39], off offset:256 sc0 sc1
	global_store_dwordx4 v[98:99], v[40:43], off offset:256 sc0 sc1
	s_and_saveexec_b64 s[54:55], vcc
	s_cbranch_execz .LBB0_1137
	s_waitcnt lgkmcnt(0)
	v_max_f32_e32 v35, v35, v35
	v_max_f32_e32 v34, v34, v34
	v_lshl_add_u64 v[36:37], v[194:195], 2, s[14:15]
	v_max_f32_e32 v34, v34, v35
	global_atomic_umax v[36:37], v34, off
.LBB0_1137:
	s_or_b64 exec, exec, s[54:55]
	s_waitcnt lgkmcnt(0)
	v_lshlrev_b64 v[34:35], 13, v[188:189]
	v_lshl_add_u64 v[46:47], v[192:193], 0, v[34:35]
	global_load_dwordx4 v[34:37], v[46:47], off
	global_load_dwordx4 v[38:41], v[46:47], off offset:16
	global_load_dwordx4 v[42:45], v[46:47], off offset:512
	s_nop 0
	global_load_dwordx4 v[46:49], v[46:47], off offset:528
	v_cvt_f32_i32_e32 v65, v19
	v_cvt_f32_i32_e32 v64, v18
	v_lshlrev_b64 v[18:19], 13, v[182:183]
	v_cvt_f32_i32_e32 v61, v23
	v_cvt_f32_i32_e32 v60, v22
	v_cvt_f32_i32_e32 v63, v21
	v_cvt_f32_i32_e32 v62, v20
	v_lshlrev_b64 v[20:21], 11, v[188:189]
	v_lshl_add_u64 v[22:23], v[192:193], 0, v[18:19]
	v_cvt_f32_i32_e32 v59, v25
	v_cvt_f32_i32_e32 v58, v24
	v_cvt_f32_i32_e32 v75, v29
	v_cvt_f32_i32_e32 v74, v28
	v_cvt_f32_i32_e32 v77, v27
	v_cvt_f32_i32_e32 v76, v26
	v_cvt_f32_i32_e32 v79, v33
	v_cvt_f32_i32_e32 v78, v32
	v_cvt_f32_i32_e32 v81, v31
	v_cvt_f32_i32_e32 v80, v30
	v_lshl_add_u64 v[98:99], v[186:187], 0, v[20:21]
	global_load_dwordx4 v[26:29], v[22:23], off offset:16
	global_load_dwordx4 v[30:33], v[22:23], off
	global_load_dwordx4 v[18:21], v[22:23], off offset:528
	s_nop 0
	global_load_dwordx4 v[22:25], v[22:23], off offset:512
	v_pk_mul_f32 v[60:61], v[190:191], v[60:61] op_sel_hi:[0,1]
	v_pk_mul_f32 v[58:59], v[190:191], v[58:59] op_sel_hi:[0,1]
	v_pk_mul_f32 v[64:65], v[190:191], v[64:65] op_sel_hi:[0,1]
	v_pk_mul_f32 v[62:63], v[190:191], v[62:63] op_sel_hi:[0,1]
	v_pk_mul_f32 v[76:77], v[190:191], v[76:77] op_sel_hi:[0,1]
	v_pk_mul_f32 v[74:75], v[190:191], v[74:75] op_sel_hi:[0,1]
	v_lshlrev_b64 v[98:99], 1, v[98:99]
	v_lshl_add_u64 v[100:101], s[48:49], 0, v[98:99]
	v_lshl_add_u64 v[98:99], s[12:13], 0, v[98:99]
	v_pk_mul_f32 v[80:81], v[190:191], v[80:81] op_sel_hi:[0,1]
	v_pk_mul_f32 v[78:79], v[190:191], v[78:79] op_sel_hi:[0,1]
	s_waitcnt vmcnt(7)
	v_pk_fma_f32 v[36:37], v[96:97], v[58:59], v[36:37]
	v_pk_fma_f32 v[58:59], v[94:95], v[60:61], v[34:35]
	s_waitcnt vmcnt(6)
	v_pk_fma_f32 v[60:61], v[92:93], v[62:63], v[40:41]
	v_pk_fma_f32 v[40:41], v[90:91], v[64:65], v[38:39]
	s_waitcnt vmcnt(5)
	v_pk_fma_f32 v[62:63], v[76:77], v[86:87], v[42:43]
	v_mul_f32_e32 v35, v82, v58
	v_mul_f32_e32 v38, v70, v40
	v_mul_f32_e32 v39, v83, v59
	v_mul_f32_e32 v42, v71, v41
	v_pk_fma_f32 v[44:45], v[74:75], v[88:89], v[44:45]
	v_cvt_pk_bf16_f32 v34, v58, v59
	v_mul_f32_e32 v43, v84, v36
	v_mul_f32_e32 v64, v72, v60
	v_mul_f32_e32 v65, v85, v37
	v_mul_f32_e32 v74, v73, v61
	v_lshlrev_b32_e32 v75, 16, v34
	v_and_b32_e32 v76, 0xffff0000, v34
	v_max_f32_e64 v35, |v35|, |v38|
	v_max_f32_e64 v38, |v39|, |v42|
	v_max_f32_e64 v39, |v43|, |v64|
	v_max_f32_e64 v42, |v65|, |v74|
	v_sub_f32_e32 v43, v58, v75
	v_sub_f32_e32 v58, v59, v76
	v_max3_f32 v59, v35, 0, v38
	v_cvt_pk_bf16_f32 v38, v43, v58
	v_cvt_pk_bf16_f32 v35, v36, v37
	v_max3_f32 v43, v59, v39, v42
	v_lshlrev_b32_e32 v39, 16, v35
	v_and_b32_e32 v42, 0xffff0000, v35
	v_sub_f32_e32 v36, v36, v39
	v_sub_f32_e32 v37, v37, v42
	v_cvt_pk_bf16_f32 v39, v36, v37
	v_cvt_pk_bf16_f32 v36, v40, v41
	s_waitcnt vmcnt(4)
	v_pk_fma_f32 v[46:47], v[80:81], v[66:67], v[46:47]
	v_lshlrev_b32_e32 v37, 16, v36
	v_and_b32_e32 v42, 0xffff0000, v36
	v_sub_f32_e32 v37, v40, v37
	v_sub_f32_e32 v40, v41, v42
	v_cvt_pk_bf16_f32 v40, v37, v40
	v_cvt_pk_bf16_f32 v37, v60, v61
	v_pk_fma_f32 v[48:49], v[78:79], v[68:69], v[48:49]
	v_lshlrev_b32_e32 v41, 16, v37
	v_and_b32_e32 v42, 0xffff0000, v37
	v_sub_f32_e32 v41, v60, v41
	v_sub_f32_e32 v42, v61, v42
	v_cvt_pk_bf16_f32 v41, v41, v42
	global_store_dwordx4 v[100:101], v[34:37], off sc0 sc1
	global_store_dwordx4 v[98:99], v[38:41], off sc0 sc1
	s_nop 0
	v_cvt_pk_bf16_f32 v36, v62, v63
	s_nop 0
	v_lshlrev_b32_e32 v34, 16, v36
	v_and_b32_e32 v35, 0xffff0000, v36
	v_sub_f32_e32 v34, v62, v34
	v_sub_f32_e32 v35, v63, v35
	v_cvt_pk_bf16_f32 v40, v34, v35
	v_cvt_pk_bf16_f32 v37, v44, v45
	v_mul_f32_e32 v39, v51, v47
	v_lshlrev_b32_e32 v34, 16, v37
	v_and_b32_e32 v35, 0xffff0000, v37
	v_sub_f32_e32 v34, v44, v34
	v_sub_f32_e32 v35, v45, v35
	v_cvt_pk_bf16_f32 v41, v34, v35
	v_cvt_pk_bf16_f32 v38, v46, v47
	s_nop 0
	v_lshlrev_b32_e32 v34, 16, v38
	v_and_b32_e32 v35, 0xffff0000, v38
	v_sub_f32_e32 v34, v46, v34
	v_sub_f32_e32 v35, v47, v35
	v_cvt_pk_bf16_f32 v42, v34, v35
	v_mul_f32_e32 v34, v54, v62
	v_mul_f32_e32 v35, v50, v46
	v_max_f32_e64 v34, |v34|, |v35|
	v_mul_f32_e32 v35, v55, v63
	v_max_f32_e64 v35, |v35|, |v39|
	v_max3_f32 v34, v43, v34, v35
	v_mul_f32_e32 v35, v56, v44
	v_mul_f32_e32 v39, v52, v48
	v_max_f32_e64 v35, |v35|, |v39|
	v_mul_f32_e32 v39, v57, v45
	v_mul_f32_e32 v43, v53, v49
	v_max_f32_e64 v39, |v39|, |v43|
	v_max3_f32 v34, v34, v35, v39
	ds_bpermute_b32 v35, v197, v34
	v_cvt_pk_bf16_f32 v39, v48, v49
	s_waitcnt lgkmcnt(0)
	v_max_f32_e32 v35, v35, v35
	v_max_f32_e32 v34, v34, v35
	ds_bpermute_b32 v35, v201, v34
	v_lshlrev_b32_e32 v43, 16, v39
	v_sub_f32_e32 v43, v48, v43
	v_and_b32_e32 v44, 0xffff0000, v39
	v_sub_f32_e32 v44, v49, v44
	v_cvt_pk_bf16_f32 v43, v43, v44
	global_store_dwordx4 v[100:101], v[36:39], off offset:256 sc0 sc1
	global_store_dwordx4 v[98:99], v[40:43], off offset:256 sc0 sc1
	s_and_saveexec_b64 s[54:55], vcc
	s_cbranch_execz .LBB0_1139
	s_waitcnt lgkmcnt(0)
	v_max_f32_e32 v35, v35, v35
	v_max_f32_e32 v34, v34, v34
	v_lshl_add_u64 v[36:37], v[188:189], 2, s[14:15]
	v_max_f32_e32 v34, v34, v35
	global_atomic_umax v[36:37], v34, off
.LBB0_1139:
	s_or_b64 exec, exec, s[54:55]
	v_cvt_f32_i32_e32 v7, v7
	v_cvt_f32_i32_e32 v6, v6
	v_cvt_f32_i32_e32 v5, v5
	v_cvt_f32_i32_e32 v4, v4
	v_cvt_f32_i32_e32 v3, v3
	v_cvt_f32_i32_e32 v2, v2
	v_cvt_f32_i32_e32 v9, v9
	v_cvt_f32_i32_e32 v8, v8
	v_pk_mul_f32 v[6:7], v[184:185], v[6:7] op_sel_hi:[0,1]
	v_pk_mul_f32 v[2:3], v[184:185], v[2:3] op_sel_hi:[0,1]
	v_pk_mul_f32 v[4:5], v[184:185], v[4:5] op_sel_hi:[0,1]
	s_waitcnt vmcnt(6)
	v_pk_fma_f32 v[30:31], v[94:95], v[6:7], v[30:31]
	v_pk_fma_f32 v[28:29], v[92:93], v[4:5], v[28:29]
	v_pk_fma_f32 v[26:27], v[90:91], v[2:3], v[26:27]
	v_cvt_pk_bf16_f32 v2, v30, v31
	v_pk_mul_f32 v[8:9], v[184:185], v[8:9] op_sel_hi:[0,1]
	v_lshlrev_b32_e32 v3, 16, v2
	v_and_b32_e32 v4, 0xffff0000, v2
	v_sub_f32_e32 v3, v30, v3
	v_sub_f32_e32 v4, v31, v4
	v_pk_fma_f32 v[32:33], v[96:97], v[8:9], v[32:33]
	v_cvt_pk_bf16_f32 v6, v3, v4
	s_waitcnt lgkmcnt(0)
	v_lshlrev_b64 v[34:35], 11, v[182:183]
	v_cvt_pk_bf16_f32 v3, v32, v33
	v_lshl_add_u64 v[34:35], v[186:187], 0, v[34:35]
	v_lshlrev_b32_e32 v4, 16, v3
	v_and_b32_e32 v5, 0xffff0000, v3
	v_sub_f32_e32 v4, v32, v4
	v_sub_f32_e32 v5, v33, v5
	v_cvt_pk_bf16_f32 v7, v4, v5
	v_cvt_pk_bf16_f32 v4, v26, v27
	v_lshlrev_b64 v[34:35], 1, v[34:35]
	v_lshlrev_b32_e32 v5, 16, v4
	v_and_b32_e32 v8, 0xffff0000, v4
	v_sub_f32_e32 v5, v26, v5
	v_sub_f32_e32 v8, v27, v8
	v_cvt_pk_bf16_f32 v8, v5, v8
	v_cvt_pk_bf16_f32 v5, v28, v29
	v_cvt_f32_i32_e32 v13, v13
	v_lshlrev_b32_e32 v9, 16, v5
	v_and_b32_e32 v36, 0xffff0000, v5
	v_sub_f32_e32 v9, v28, v9
	v_sub_f32_e32 v36, v29, v36
	v_cvt_pk_bf16_f32 v9, v9, v36
	v_lshl_add_u64 v[36:37], s[48:49], 0, v[34:35]
	global_store_dwordx4 v[36:37], v[2:5], off sc0 sc1
	v_cvt_f32_i32_e32 v12, v12
	v_cvt_f32_i32_e32 v11, v11
	v_mul_f32_e32 v2, v82, v30
	v_mul_f32_e32 v3, v70, v26
	v_max_f32_e64 v2, |v2|, |v3|
	v_mul_f32_e32 v3, v83, v31
	v_mul_f32_e32 v4, v71, v27
	v_max_f32_e64 v3, |v3|, |v4|
	v_cvt_f32_i32_e32 v10, v10
	v_cvt_f32_i32_e32 v17, v17
	v_cvt_f32_i32_e32 v16, v16
	v_cvt_f32_i32_e32 v15, v15
	v_cvt_f32_i32_e32 v14, v14
	v_max3_f32 v2, v2, 0, v3
	v_mul_f32_e32 v3, v84, v32
	v_mul_f32_e32 v4, v72, v28
	v_max_f32_e64 v3, |v3|, |v4|
	v_mul_f32_e32 v4, v85, v33
	v_mul_f32_e32 v5, v73, v29
	v_max_f32_e64 v4, |v4|, |v5|
	v_lshl_add_u64 v[34:35], s[12:13], 0, v[34:35]
	v_max3_f32 v26, v2, v3, v4
	v_pk_mul_f32 v[4:5], v[184:185], v[12:13] op_sel_hi:[0,1]
	global_store_dwordx4 v[34:35], v[6:9], off sc0 sc1
	v_pk_mul_f32 v[2:3], v[184:185], v[10:11] op_sel_hi:[0,1]
	s_waitcnt vmcnt(6)
	v_pk_fma_f32 v[12:13], v[88:89], v[4:5], v[24:25]
	v_pk_mul_f32 v[4:5], v[184:185], v[14:15] op_sel_hi:[0,1]
	v_pk_mul_f32 v[6:7], v[184:185], v[16:17] op_sel_hi:[0,1]
	v_pk_fma_f32 v[2:3], v[86:87], v[2:3], v[22:23]
	v_pk_fma_f32 v[14:15], v[6:7], v[68:69], v[20:21]
	v_pk_fma_f32 v[16:17], v[4:5], v[66:67], v[18:19]
	v_cvt_pk_bf16_f32 v4, v2, v3
	v_mul_f32_e32 v11, v53, v15
	v_lshlrev_b32_e32 v5, 16, v4
	v_and_b32_e32 v6, 0xffff0000, v4
	v_sub_f32_e32 v5, v2, v5
	v_sub_f32_e32 v6, v3, v6
	v_cvt_pk_bf16_f32 v8, v5, v6
	v_cvt_pk_bf16_f32 v5, v12, v13
	v_mul_f32_e32 v2, v54, v2
	v_lshlrev_b32_e32 v6, 16, v5
	v_and_b32_e32 v7, 0xffff0000, v5
	v_sub_f32_e32 v6, v12, v6
	v_sub_f32_e32 v7, v13, v7
	v_cvt_pk_bf16_f32 v9, v6, v7
	v_cvt_pk_bf16_f32 v6, v16, v17
	v_mul_f32_e32 v3, v55, v3
	v_lshlrev_b32_e32 v7, 16, v6
	v_and_b32_e32 v10, 0xffff0000, v6
	v_sub_f32_e32 v7, v16, v7
	v_sub_f32_e32 v10, v17, v10
	v_cvt_pk_bf16_f32 v10, v7, v10
	v_mul_f32_e32 v7, v50, v16
	v_max_f32_e64 v2, |v2|, |v7|
	v_mul_f32_e32 v7, v51, v17
	v_max_f32_e64 v3, |v3|, |v7|
	v_max3_f32 v2, v26, v2, v3
	v_mul_f32_e32 v3, v56, v12
	v_mul_f32_e32 v7, v52, v14
	v_max_f32_e64 v3, |v3|, |v7|
	v_mul_f32_e32 v7, v57, v13
	v_max_f32_e64 v7, |v7|, |v11|
	v_max3_f32 v2, v2, v3, v7
	ds_bpermute_b32 v3, v197, v2
	v_cvt_pk_bf16_f32 v7, v14, v15
	s_waitcnt lgkmcnt(0)
	v_max_f32_e32 v3, v3, v3
	v_max_f32_e32 v2, v2, v3
	ds_bpermute_b32 v3, v201, v2
	v_lshlrev_b32_e32 v11, 16, v7
	v_sub_f32_e32 v11, v14, v11
	v_and_b32_e32 v12, 0xffff0000, v7
	v_sub_f32_e32 v12, v15, v12
	v_cvt_pk_bf16_f32 v11, v11, v12
	global_store_dwordx4 v[36:37], v[4:7], off offset:256 sc0 sc1
	global_store_dwordx4 v[34:35], v[8:11], off offset:256 sc0 sc1
	s_and_saveexec_b64 s[54:55], vcc
	s_cbranch_execz .LBB0_1141
	s_waitcnt lgkmcnt(0)
	v_max_f32_e32 v3, v3, v3
	v_max_f32_e32 v2, v2, v2
	v_lshl_add_u64 v[4:5], v[182:183], 2, s[14:15]
	v_max_f32_e32 v2, v2, v3
	global_atomic_umax v[4:5], v2, off
